# 8-phase K-loops: per-phase counted vmcnt(10) instead of whole-buffer vmcnt(6) in phases 4/8 (every DMA piece gets five phases of lead); plus W_o XCD map
# baseline (speedup 1.0000x reference)
; #define G_BAR() __builtin_amdgcn_s_barrier()
; #define G_SCHED() __builtin_amdgcn_sched_barrier(0)
; #define D_STAGE_A(slot, half, kt) D_STAGE(rsA, voffA, slot, half, kt)
; #define D_STAGE_B(slot, half, kt) D_STAGE(rsB, voffB, slot, half, kt)
; #define D_LDA(dst, slot) do { _Pragma("unroll") for (int m = 0; m < 4; ++m) _Pragma("unroll") for (int k = 0; k < 2; ++k) \
;     dst[m][k] = *(const LDS_AS bf16x8*)(lds + (slot) + aoff + m * 2048 + k * 1024); } while (0)
; #define D_LDB(dst, slot) do { _Pragma("unroll") for (int n = 0; n < 2; ++n) _Pragma("unroll") for (int k = 0; k < 2; ++k) \
;     dst[n][k] = *(const LDS_AS bf16x8*)(lds + (slot) + boff + n * 2048 + k * 1024); } while (0)
; #define D_MMA(ai, bj, At, Bf) do { __builtin_amdgcn_s_setprio(1); _Pragma("unroll") for (int m = 0; m < 4; ++m) _Pragma("unroll") for (int n = 0; n < 2; ++n) _Pragma("unroll") for (int k = 0; k < 2; ++k) \
;     acc[ai][bj][m][n] = __builtin_amdgcn_mfma_f32_16x16x32_bf16(Bf[n][k], At[m][k], acc[ai][bj][m][n], 0, 0, 0); __builtin_amdgcn_s_setprio(0); } while (0)
; #define D_WAIT_L(n) asm volatile("s_waitcnt lgkmcnt(" #n ")" ::: "memory")
; #define D_STAGE_A(slot, half, kt) D_STAGE(rsA, voffA, slot, half, kt)
; #define D_STAGE_B(slot, half, kt) do { _Pragma("unroll") for (int _i = 0; _i < 2; ++_i) { const unsigned _m0 = ldsw + (unsigned)((slot) + _i * 8192); const unsigned _so = (unsigned)(kt) * 128u + (half) * bt_half + _i * bt_piece; \
;     asm volatile("s_mov_b32 m0, %0\n\ts_nop 4\n\tbuffer_load_dwordx4 %1, %2, %3 offen lds" :: "s"(_m0), "v"(voffB0), "s"(rsB), "s"(_so) : "m0", "memory"); } } while (0)
; template <class Cfg>
; DI void gemm256dma_unit(LDS_AS unsigned char* lds, const Cfg& cfg) {
;     ...
;   for (int t = 0; t < nt; t += 2) {
;     const int t1 = t + 1;
;     const int t2 = (t + 2 < nt) ? t + 2 : 0;
;     const int t3 = (t + 2 < nt) ? t + 3 : 1;
;     D_LDB(B0, G_SB(0, 0)); G_SCHED(); D_LDA(At, G_SA(0, 0)); D_STAGE_A(G_SA(1, 1), 1, t1);
;     D_WAIT_L(8); G_BAR(); D_WAIT_L(0); G_SCHED(); D_MMA(0, 0, At, B0); G_BAR(); G_SCHED();
;     D_LDB(B1, G_SB(0, 1)); D_STAGE_B(G_SB(0, 0), 0, t2);
;     G_BAR(); D_WAIT_L(0); G_SCHED(); D_MMA(0, 1, At, B1); G_BAR(); G_SCHED();
;     D_LDA(At, G_SA(0, 1)); D_STAGE_A(G_SA(0, 0), 0, t2);
;     G_BAR(); D_WAIT_L(0); G_SCHED(); D_MMA(1, 0, At, B0); G_BAR(); G_SCHED();
.LBB0_279:
	ds_read_b128 v[142:145], v139
	ds_read_b128 v[150:153], v139 offset:1024
	ds_read_b128 v[154:157], v139 offset:2048
	ds_read_b128 v[158:161], v139 offset:3072
	s_add_i32 s30, s29, 2
	s_add_i32 s38, s28, 0xffffff00
	s_add_i32 s31, s28, 0xffffff80
	s_cmp_lt_u32 s29, 30
	s_cselect_b32 s96, s31, 0
	s_cselect_b32 s31, s28, 0x80
	s_addk_i32 s28, 0x100
	s_cmp_gt_u32 s29, 29
	ds_read_b128 v[162:165], v138 offset:16
	ds_read_b128 v[166:169], v138 offset:1040
	ds_read_b128 v[170:173], v138 offset:2064
	ds_read_b128 v[174:177], v138 offset:3088
	ds_read_b128 v[178:181], v138 offset:4112
	ds_read_b128 v[182:185], v138 offset:5136
	ds_read_b128 v[186:189], v138 offset:6160
	ds_read_b128 v[192:195], v138 offset:7184
	s_mov_b32 m0, vcc_lo
	s_nop 0
	buffer_load_dwordx4 v135, s[20:23], s38 offen lds
	s_nop 0
	s_mov_b32 m0, vcc_hi
	s_nop 0
	buffer_load_dwordx4 v132, s[20:23], s38 offen lds
	s_waitcnt lgkmcnt(8)
	s_waitcnt vmcnt(10)
	s_barrier
	s_waitcnt lgkmcnt(0)
	s_setprio 1
	s_waitcnt lgkmcnt(7)
	v_mfma_f32_16x16x32_bf16 v[124:127], v[142:145], v[162:165], v[124:127]
	v_mfma_f32_16x16x32_bf16 v[120:123], v[154:157], v[162:165], v[120:123]
	s_waitcnt lgkmcnt(5)
	v_mfma_f32_16x16x32_bf16 v[108:111], v[142:145], v[170:173], v[108:111]
	v_mfma_f32_16x16x32_bf16 v[104:107], v[154:157], v[170:173], v[104:107]
	s_waitcnt lgkmcnt(3)
	v_mfma_f32_16x16x32_bf16 v[92:95], v[142:145], v[178:181], v[92:95]
	v_mfma_f32_16x16x32_bf16 v[88:91], v[154:157], v[178:181], v[88:91]
	s_waitcnt lgkmcnt(1)
	v_mfma_f32_16x16x32_bf16 v[76:79], v[142:145], v[186:189], v[76:79]
	v_mfma_f32_16x16x32_bf16 v[72:75], v[154:157], v[186:189], v[72:75]
	v_mfma_f32_16x16x32_bf16 v[124:127], v[150:153], v[166:169], v[124:127]
	v_mfma_f32_16x16x32_bf16 v[120:123], v[158:161], v[166:169], v[120:123]
	v_mfma_f32_16x16x32_bf16 v[108:111], v[150:153], v[174:177], v[108:111]
	v_mfma_f32_16x16x32_bf16 v[104:107], v[158:161], v[174:177], v[104:107]
	v_mfma_f32_16x16x32_bf16 v[92:95], v[150:153], v[182:185], v[92:95]
	v_mfma_f32_16x16x32_bf16 v[88:91], v[158:161], v[182:185], v[88:91]
	s_waitcnt lgkmcnt(0)
	v_mfma_f32_16x16x32_bf16 v[76:79], v[150:153], v[192:195], v[76:79]
	v_mfma_f32_16x16x32_bf16 v[72:75], v[158:161], v[192:195], v[72:75]
	s_setprio 0
	s_barrier
	ds_read_b128 v[196:199], v140
	ds_read_b128 v[200:203], v140 offset:1024
	ds_read_b128 v[204:207], v140 offset:2048
	ds_read_b128 v[208:211], v140 offset:3072
	s_mov_b32 m0, s33
	s_nop 0
	buffer_load_dwordx4 v133, s[8:11], s96 offen lds
	s_nop 0
	s_mov_b32 m0, s39
	s_nop 0
	buffer_load_dwordx4 v128, s[8:11], s96 offen lds
	s_waitcnt vmcnt(10)
	s_barrier
	s_waitcnt lgkmcnt(0)
	s_setprio 1
	s_waitcnt lgkmcnt(3)
	v_mfma_f32_16x16x32_bf16 v[116:119], v[196:199], v[162:165], v[116:119]
	s_waitcnt lgkmcnt(1)
	v_mfma_f32_16x16x32_bf16 v[112:115], v[204:207], v[162:165], v[112:115]
	v_mfma_f32_16x16x32_bf16 v[100:103], v[196:199], v[170:173], v[100:103]
	v_mfma_f32_16x16x32_bf16 v[96:99], v[204:207], v[170:173], v[96:99]
	v_mfma_f32_16x16x32_bf16 v[84:87], v[196:199], v[178:181], v[84:87]
	v_mfma_f32_16x16x32_bf16 v[80:83], v[204:207], v[178:181], v[80:83]
	v_mfma_f32_16x16x32_bf16 v[68:71], v[196:199], v[186:189], v[68:71]
	v_mfma_f32_16x16x32_bf16 v[64:67], v[204:207], v[186:189], v[64:67]
	v_mfma_f32_16x16x32_bf16 v[116:119], v[200:203], v[166:169], v[116:119]
	s_waitcnt lgkmcnt(0)
	v_mfma_f32_16x16x32_bf16 v[112:115], v[208:211], v[166:169], v[112:115]
	v_mfma_f32_16x16x32_bf16 v[100:103], v[200:203], v[174:177], v[100:103]
	v_mfma_f32_16x16x32_bf16 v[96:99], v[208:211], v[174:177], v[96:99]
	v_mfma_f32_16x16x32_bf16 v[84:87], v[200:203], v[182:185], v[84:87]
	v_mfma_f32_16x16x32_bf16 v[80:83], v[208:211], v[182:185], v[80:83]
	v_mfma_f32_16x16x32_bf16 v[68:71], v[200:203], v[192:195], v[68:71]
	v_mfma_f32_16x16x32_bf16 v[64:67], v[208:211], v[192:195], v[64:67]
	s_setprio 0
	s_barrier
	ds_read_b128 v[162:165], v138 offset:16400
	ds_read_b128 v[166:169], v138 offset:17424
	ds_read_b128 v[170:173], v138 offset:18448
	ds_read_b128 v[174:177], v138 offset:19472
	ds_read_b128 v[178:181], v138 offset:20496
	ds_read_b128 v[182:185], v138 offset:21520
	ds_read_b128 v[186:189], v138 offset:22544
	ds_read_b128 v[192:195], v138 offset:23568
	s_mov_b32 m0, s1
	s_nop 0
	buffer_load_dwordx4 v134, s[20:23], s96 offen lds
	s_nop 0
	s_mov_b32 m0, s42
	s_nop 0
	buffer_load_dwordx4 v131, s[20:23], s96 offen lds
	s_barrier
	s_waitcnt lgkmcnt(0)
	s_setprio 1
	s_waitcnt lgkmcnt(7)
	v_mfma_f32_16x16x32_bf16 v[60:63], v[142:145], v[162:165], v[60:63]
	v_mfma_f32_16x16x32_bf16 v[56:59], v[154:157], v[162:165], v[56:59]
	s_waitcnt lgkmcnt(5)
	v_mfma_f32_16x16x32_bf16 v[44:47], v[142:145], v[170:173], v[44:47]
	v_mfma_f32_16x16x32_bf16 v[40:43], v[154:157], v[170:173], v[40:43]
	s_waitcnt lgkmcnt(3)
	v_mfma_f32_16x16x32_bf16 v[28:31], v[142:145], v[178:181], v[28:31]
	v_mfma_f32_16x16x32_bf16 v[24:27], v[154:157], v[178:181], v[24:27]
	s_waitcnt lgkmcnt(1)
	v_mfma_f32_16x16x32_bf16 v[12:15], v[142:145], v[186:189], v[12:15]
	v_mfma_f32_16x16x32_bf16 v[8:11], v[154:157], v[186:189], v[8:11]
	v_mfma_f32_16x16x32_bf16 v[60:63], v[150:153], v[166:169], v[60:63]
	v_mfma_f32_16x16x32_bf16 v[56:59], v[158:161], v[166:169], v[56:59]
	v_mfma_f32_16x16x32_bf16 v[44:47], v[150:153], v[174:177], v[44:47]
	v_mfma_f32_16x16x32_bf16 v[40:43], v[158:161], v[174:177], v[40:43]
	v_mfma_f32_16x16x32_bf16 v[28:31], v[150:153], v[182:185], v[28:31]
	v_mfma_f32_16x16x32_bf16 v[24:27], v[158:161], v[182:185], v[24:27]
	s_waitcnt lgkmcnt(0)
	v_mfma_f32_16x16x32_bf16 v[12:15], v[150:153], v[192:195], v[12:15]
	v_mfma_f32_16x16x32_bf16 v[8:11], v[158:161], v[192:195], v[8:11]
	s_setprio 0
	s_barrier
; #define G_WAIT_V(n) asm volatile("s_waitcnt vmcnt(" #n ")" ::: "memory")
; #define G_BAR() __builtin_amdgcn_s_barrier()
; #define G_SCHED() __builtin_amdgcn_sched_barrier(0)
; #define D_STAGE_A(slot, half, kt) D_STAGE(rsA, voffA, slot, half, kt)
; #define D_STAGE_B(slot, half, kt) D_STAGE(rsB, voffB, slot, half, kt)
; #define D_LDA(dst, slot) do { _Pragma("unroll") for (int m = 0; m < 4; ++m) _Pragma("unroll") for (int k = 0; k < 2; ++k) \
;     dst[m][k] = *(const LDS_AS bf16x8*)(lds + (slot) + aoff + m * 2048 + k * 1024); } while (0)
; #define D_LDB(dst, slot) do { _Pragma("unroll") for (int n = 0; n < 2; ++n) _Pragma("unroll") for (int k = 0; k < 2; ++k) \
;     dst[n][k] = *(const LDS_AS bf16x8*)(lds + (slot) + boff + n * 2048 + k * 1024); } while (0)
; #define D_MMA(ai, bj, At, Bf) do { __builtin_amdgcn_s_setprio(1); _Pragma("unroll") for (int m = 0; m < 4; ++m) _Pragma("unroll") for (int n = 0; n < 2; ++n) _Pragma("unroll") for (int k = 0; k < 2; ++k) \
;     acc[ai][bj][m][n] = __builtin_amdgcn_mfma_f32_16x16x32_bf16(Bf[n][k], At[m][k], acc[ai][bj][m][n], 0, 0, 0); __builtin_amdgcn_s_setprio(0); } while (0)
; #define D_WAIT_L(n) asm volatile("s_waitcnt lgkmcnt(" #n ")" ::: "memory")
; #define D_STAGE_A(slot, half, kt) D_STAGE(rsA, voffA, slot, half, kt)
; #define D_STAGE_B(slot, half, kt) do { _Pragma("unroll") for (int _i = 0; _i < 2; ++_i) { const unsigned _m0 = ldsw + (unsigned)((slot) + _i * 8192); const unsigned _so = (unsigned)(kt) * 128u + (half) * bt_half + _i * bt_piece; \
;     asm volatile("s_mov_b32 m0, %0\n\ts_nop 4\n\tbuffer_load_dwordx4 %1, %2, %3 offen lds" :: "s"(_m0), "v"(voffB0), "s"(rsB), "s"(_so) : "m0", "memory"); } } while (0)
; #define D_WAIT_L(n) asm volatile("s_waitcnt lgkmcnt(" #n ")" ::: "memory")
; template <class Cfg>
; DI void gemm256dma_unit(LDS_AS unsigned char* lds, const Cfg& cfg) {
;     ...
;     D_STAGE_B(G_SB(0, 1), 1, t2);
;     G_WAIT_V(6); G_BAR(); G_SCHED(); D_MMA(1, 1, At, B1); G_BAR(); G_SCHED();
;     D_LDB(B0, G_SB(1, 0)); G_SCHED(); D_LDA(At, G_SA(1, 0)); D_STAGE_A(G_SA(0, 1), 1, t2);
;     D_WAIT_L(8); G_BAR(); D_WAIT_L(0); G_SCHED(); D_MMA(0, 0, At, B0); G_BAR(); G_SCHED();
;     D_LDB(B1, G_SB(1, 1)); D_STAGE_B(G_SB(1, 0), 0, t3);
;     G_BAR(); D_WAIT_L(0); G_SCHED(); D_MMA(0, 1, At, B1); G_BAR(); G_SCHED();
	s_mov_b32 m0, s43
	s_nop 0
	buffer_load_dwordx4 v130, s[8:11], s96 offen lds
	s_nop 0
	s_mov_b32 m0, s54
	s_nop 0
	buffer_load_dwordx4 v136, s[8:11], s96 offen lds
	s_waitcnt vmcnt(10)
	s_barrier
	s_setprio 1
	v_mfma_f32_16x16x32_bf16 v[52:55], v[196:199], v[162:165], v[52:55]
	v_mfma_f32_16x16x32_bf16 v[48:51], v[204:207], v[162:165], v[48:51]
	v_mfma_f32_16x16x32_bf16 v[36:39], v[196:199], v[170:173], v[36:39]
	v_mfma_f32_16x16x32_bf16 v[32:35], v[204:207], v[170:173], v[32:35]
	v_mfma_f32_16x16x32_bf16 v[20:23], v[196:199], v[178:181], v[20:23]
	v_mfma_f32_16x16x32_bf16 v[16:19], v[204:207], v[178:181], v[16:19]
	v_mfma_f32_16x16x32_bf16 v[4:7], v[196:199], v[186:189], v[4:7]
	v_mfma_f32_16x16x32_bf16 v[0:3], v[204:207], v[186:189], v[0:3]
	v_mfma_f32_16x16x32_bf16 v[52:55], v[200:203], v[166:169], v[52:55]
	v_mfma_f32_16x16x32_bf16 v[48:51], v[208:211], v[166:169], v[48:51]
	v_mfma_f32_16x16x32_bf16 v[36:39], v[200:203], v[174:177], v[36:39]
	v_mfma_f32_16x16x32_bf16 v[32:35], v[208:211], v[174:177], v[32:35]
	v_mfma_f32_16x16x32_bf16 v[20:23], v[200:203], v[182:185], v[20:23]
	v_mfma_f32_16x16x32_bf16 v[16:19], v[208:211], v[182:185], v[16:19]
	v_mfma_f32_16x16x32_bf16 v[4:7], v[200:203], v[192:195], v[4:7]
	v_mfma_f32_16x16x32_bf16 v[0:3], v[208:211], v[192:195], v[0:3]
	s_setprio 0
	s_barrier
	v_add_u32_e32 v141, 0x18010, v137
	ds_read_b128 v[142:145], v141
	ds_read_b128 v[150:153], v141 offset:1024
	ds_read_b128 v[154:157], v141 offset:2048
	ds_read_b128 v[158:161], v141 offset:3072
	ds_read_b128 v[162:165], v138 offset:32784
	ds_read_b128 v[166:169], v138 offset:33808
	ds_read_b128 v[170:173], v138 offset:34832
	ds_read_b128 v[174:177], v138 offset:35856
	ds_read_b128 v[178:181], v138 offset:36880
	ds_read_b128 v[182:185], v138 offset:37904
	ds_read_b128 v[186:189], v138 offset:38928
	ds_read_b128 v[192:195], v138 offset:39952
	s_mov_b32 m0, s60
	s_nop 0
	buffer_load_dwordx4 v135, s[20:23], s96 offen lds
	s_nop 0
	s_mov_b32 m0, s61
	s_nop 0
	buffer_load_dwordx4 v132, s[20:23], s96 offen lds
	s_waitcnt lgkmcnt(8)
	s_waitcnt vmcnt(10)
	s_barrier
	s_waitcnt lgkmcnt(0)
	s_setprio 1
	s_waitcnt lgkmcnt(7)
	v_mfma_f32_16x16x32_bf16 v[124:127], v[142:145], v[162:165], v[124:127]
	v_mfma_f32_16x16x32_bf16 v[120:123], v[154:157], v[162:165], v[120:123]
	s_waitcnt lgkmcnt(5)
	v_mfma_f32_16x16x32_bf16 v[108:111], v[142:145], v[170:173], v[108:111]
	v_mfma_f32_16x16x32_bf16 v[104:107], v[154:157], v[170:173], v[104:107]
	s_waitcnt lgkmcnt(3)
	v_mfma_f32_16x16x32_bf16 v[92:95], v[142:145], v[178:181], v[92:95]
	v_mfma_f32_16x16x32_bf16 v[88:91], v[154:157], v[178:181], v[88:91]
	s_waitcnt lgkmcnt(1)
	v_mfma_f32_16x16x32_bf16 v[76:79], v[142:145], v[186:189], v[76:79]
	v_mfma_f32_16x16x32_bf16 v[72:75], v[154:157], v[186:189], v[72:75]
	v_mfma_f32_16x16x32_bf16 v[124:127], v[150:153], v[166:169], v[124:127]
	v_mfma_f32_16x16x32_bf16 v[120:123], v[158:161], v[166:169], v[120:123]
	v_mfma_f32_16x16x32_bf16 v[108:111], v[150:153], v[174:177], v[108:111]
	v_mfma_f32_16x16x32_bf16 v[104:107], v[158:161], v[174:177], v[104:107]
	v_mfma_f32_16x16x32_bf16 v[92:95], v[150:153], v[182:185], v[92:95]
	v_mfma_f32_16x16x32_bf16 v[88:91], v[158:161], v[182:185], v[88:91]
	s_waitcnt lgkmcnt(0)
	v_mfma_f32_16x16x32_bf16 v[76:79], v[150:153], v[192:195], v[76:79]
	v_mfma_f32_16x16x32_bf16 v[72:75], v[158:161], v[192:195], v[72:75]
	s_setprio 0
	s_barrier
	v_add_u32_e32 v141, 0x1c010, v137
	ds_read_b128 v[196:199], v141
	ds_read_b128 v[200:203], v141 offset:1024
	ds_read_b128 v[204:207], v141 offset:2048
	ds_read_b128 v[208:211], v141 offset:3072
	s_mov_b32 m0, s62
	s_nop 0
	buffer_load_dwordx4 v133, s[8:11], s31 offen lds
	s_nop 0
	s_mov_b32 m0, s63
	s_nop 0
	buffer_load_dwordx4 v128, s[8:11], s31 offen lds
	s_waitcnt vmcnt(10)
	s_barrier
; #define G_WAIT_V(n) asm volatile("s_waitcnt vmcnt(" #n ")" ::: "memory")
; #define G_BAR() __builtin_amdgcn_s_barrier()
; #define G_SCHED() __builtin_amdgcn_sched_barrier(0)
; #define D_STAGE_A(slot, half, kt) D_STAGE(rsA, voffA, slot, half, kt)
; #define D_STAGE_B(slot, half, kt) D_STAGE(rsB, voffB, slot, half, kt)
; #define D_LDA(dst, slot) do { _Pragma("unroll") for (int m = 0; m < 4; ++m) _Pragma("unroll") for (int k = 0; k < 2; ++k) \
;     dst[m][k] = *(const LDS_AS bf16x8*)(lds + (slot) + aoff + m * 2048 + k * 1024); } while (0)
; #define D_MMA(ai, bj, At, Bf) do { __builtin_amdgcn_s_setprio(1); _Pragma("unroll") for (int m = 0; m < 4; ++m) _Pragma("unroll") for (int n = 0; n < 2; ++n) _Pragma("unroll") for (int k = 0; k < 2; ++k) \
;     acc[ai][bj][m][n] = __builtin_amdgcn_mfma_f32_16x16x32_bf16(Bf[n][k], At[m][k], acc[ai][bj][m][n], 0, 0, 0); __builtin_amdgcn_s_setprio(0); } while (0)
; #define D_WAIT_L(n) asm volatile("s_waitcnt lgkmcnt(" #n ")" ::: "memory")
; #define D_STAGE_A(slot, half, kt) D_STAGE(rsA, voffA, slot, half, kt)
; #define D_STAGE_B(slot, half, kt) do { _Pragma("unroll") for (int _i = 0; _i < 2; ++_i) { const unsigned _m0 = ldsw + (unsigned)((slot) + _i * 8192); const unsigned _so = (unsigned)(kt) * 128u + (half) * bt_half + _i * bt_piece; \
;     asm volatile("s_mov_b32 m0, %0\n\ts_nop 4\n\tbuffer_load_dwordx4 %1, %2, %3 offen lds" :: "s"(_m0), "v"(voffB0), "s"(rsB), "s"(_so) : "m0", "memory"); } } while (0)
; #define D_LDA(dst, slot) do { _Pragma("unroll") for (int m = 0; m < 4; ++m) { \
;     const i32x4 _lo = *(const LDS_AS i32x4*)(lds + (slot) + aoff[0] + m * 2048); const i32x4 _hi = *(const LDS_AS i32x4*)(lds + (slot) + aoff[1] + m * 2048); \
;     dst[m] = __builtin_shufflevector(_lo, _hi, 0, 1, 2, 3, 4, 5, 6, 7); } } while (0)
; #define D_WAIT_L(n) asm volatile("s_waitcnt lgkmcnt(" #n ")" ::: "memory")
; template <class Cfg>
; DI void gemm256dma_unit(LDS_AS unsigned char* lds, const Cfg& cfg) {
;     ...
;     D_LDA(At, G_SA(1, 1)); D_STAGE_A(G_SA(1, 0), 0, t3);
;     G_BAR(); D_WAIT_L(0); G_SCHED(); D_MMA(1, 0, At, B0); G_BAR(); G_SCHED();
;     D_STAGE_B(G_SB(1, 1), 1, t3);
;     G_WAIT_V(6); G_BAR(); G_SCHED(); D_MMA(1, 1, At, B1); G_BAR(); G_SCHED();
;   }
;   G_WAIT_V(0);
;   if (wr == 0) G_BAR();
	s_waitcnt lgkmcnt(0)
	s_setprio 1
	s_waitcnt lgkmcnt(3)
	v_mfma_f32_16x16x32_bf16 v[116:119], v[196:199], v[162:165], v[116:119]
	s_waitcnt lgkmcnt(1)
	v_mfma_f32_16x16x32_bf16 v[112:115], v[204:207], v[162:165], v[112:115]
	v_mfma_f32_16x16x32_bf16 v[100:103], v[196:199], v[170:173], v[100:103]
	v_mfma_f32_16x16x32_bf16 v[96:99], v[204:207], v[170:173], v[96:99]
	v_mfma_f32_16x16x32_bf16 v[84:87], v[196:199], v[178:181], v[84:87]
	v_mfma_f32_16x16x32_bf16 v[80:83], v[204:207], v[178:181], v[80:83]
	v_mfma_f32_16x16x32_bf16 v[68:71], v[196:199], v[186:189], v[68:71]
	v_mfma_f32_16x16x32_bf16 v[64:67], v[204:207], v[186:189], v[64:67]
	v_mfma_f32_16x16x32_bf16 v[116:119], v[200:203], v[166:169], v[116:119]
	s_waitcnt lgkmcnt(0)
	v_mfma_f32_16x16x32_bf16 v[112:115], v[208:211], v[166:169], v[112:115]
	v_mfma_f32_16x16x32_bf16 v[100:103], v[200:203], v[174:177], v[100:103]
	v_mfma_f32_16x16x32_bf16 v[96:99], v[208:211], v[174:177], v[96:99]
	v_mfma_f32_16x16x32_bf16 v[84:87], v[200:203], v[182:185], v[84:87]
	v_mfma_f32_16x16x32_bf16 v[80:83], v[208:211], v[182:185], v[80:83]
	v_mfma_f32_16x16x32_bf16 v[68:71], v[200:203], v[192:195], v[68:71]
	v_mfma_f32_16x16x32_bf16 v[64:67], v[208:211], v[192:195], v[64:67]
	s_setprio 0
	s_barrier
	ds_read_b128 v[162:165], v138 offset:49168
	ds_read_b128 v[166:169], v138 offset:50192
	ds_read_b128 v[170:173], v138 offset:51216
	ds_read_b128 v[174:177], v138 offset:52240
	ds_read_b128 v[178:181], v138 offset:53264
	ds_read_b128 v[182:185], v138 offset:54288
	ds_read_b128 v[186:189], v138 offset:55312
	ds_read_b128 v[192:195], v138 offset:56336
	s_mov_b32 m0, s64
	s_nop 0
	buffer_load_dwordx4 v134, s[20:23], s31 offen lds
	s_nop 0
	s_mov_b32 m0, s65
	s_nop 0
	buffer_load_dwordx4 v131, s[20:23], s31 offen lds
	s_barrier
	s_waitcnt lgkmcnt(0)
	s_setprio 1
	s_waitcnt lgkmcnt(7)
	v_mfma_f32_16x16x32_bf16 v[60:63], v[142:145], v[162:165], v[60:63]
	v_mfma_f32_16x16x32_bf16 v[56:59], v[154:157], v[162:165], v[56:59]
	s_waitcnt lgkmcnt(5)
	v_mfma_f32_16x16x32_bf16 v[44:47], v[142:145], v[170:173], v[44:47]
	v_mfma_f32_16x16x32_bf16 v[40:43], v[154:157], v[170:173], v[40:43]
	s_waitcnt lgkmcnt(3)
	v_mfma_f32_16x16x32_bf16 v[28:31], v[142:145], v[178:181], v[28:31]
	v_mfma_f32_16x16x32_bf16 v[24:27], v[154:157], v[178:181], v[24:27]
	s_waitcnt lgkmcnt(1)
	v_mfma_f32_16x16x32_bf16 v[12:15], v[142:145], v[186:189], v[12:15]
	v_mfma_f32_16x16x32_bf16 v[8:11], v[154:157], v[186:189], v[8:11]
	v_mfma_f32_16x16x32_bf16 v[60:63], v[150:153], v[166:169], v[60:63]
	v_mfma_f32_16x16x32_bf16 v[56:59], v[158:161], v[166:169], v[56:59]
	v_mfma_f32_16x16x32_bf16 v[44:47], v[150:153], v[174:177], v[44:47]
	v_mfma_f32_16x16x32_bf16 v[40:43], v[158:161], v[174:177], v[40:43]
	v_mfma_f32_16x16x32_bf16 v[28:31], v[150:153], v[182:185], v[28:31]
	v_mfma_f32_16x16x32_bf16 v[24:27], v[158:161], v[182:185], v[24:27]
	s_waitcnt lgkmcnt(0)
	v_mfma_f32_16x16x32_bf16 v[12:15], v[150:153], v[192:195], v[12:15]
	v_mfma_f32_16x16x32_bf16 v[8:11], v[158:161], v[192:195], v[8:11]
	s_setprio 0
	s_barrier
	s_mov_b32 m0, s66
	s_nop 0
	buffer_load_dwordx4 v130, s[8:11], s31 offen lds
	s_nop 0
	s_mov_b32 m0, s67
	s_nop 0
	buffer_load_dwordx4 v136, s[8:11], s31 offen lds
	s_waitcnt vmcnt(10)
	s_barrier
	s_setprio 1
	v_mfma_f32_16x16x32_bf16 v[52:55], v[196:199], v[162:165], v[52:55]
	v_mfma_f32_16x16x32_bf16 v[48:51], v[204:207], v[162:165], v[48:51]
	v_mfma_f32_16x16x32_bf16 v[36:39], v[196:199], v[170:173], v[36:39]
	v_mfma_f32_16x16x32_bf16 v[32:35], v[204:207], v[170:173], v[32:35]
	v_mfma_f32_16x16x32_bf16 v[20:23], v[196:199], v[178:181], v[20:23]
	v_mfma_f32_16x16x32_bf16 v[16:19], v[204:207], v[178:181], v[16:19]
	v_mfma_f32_16x16x32_bf16 v[4:7], v[196:199], v[186:189], v[4:7]
	v_mfma_f32_16x16x32_bf16 v[0:3], v[204:207], v[186:189], v[0:3]
	v_mfma_f32_16x16x32_bf16 v[52:55], v[200:203], v[166:169], v[52:55]
	v_mfma_f32_16x16x32_bf16 v[48:51], v[208:211], v[166:169], v[48:51]
	v_mfma_f32_16x16x32_bf16 v[36:39], v[200:203], v[174:177], v[36:39]
	v_mfma_f32_16x16x32_bf16 v[32:35], v[208:211], v[174:177], v[32:35]
	v_mfma_f32_16x16x32_bf16 v[20:23], v[200:203], v[182:185], v[20:23]
	v_mfma_f32_16x16x32_bf16 v[16:19], v[208:211], v[182:185], v[16:19]
	v_mfma_f32_16x16x32_bf16 v[4:7], v[200:203], v[192:195], v[4:7]
	v_mfma_f32_16x16x32_bf16 v[0:3], v[208:211], v[192:195], v[0:3]
	s_setprio 0
	s_barrier
	s_mov_b32 s29, s30
	s_cbranch_scc0 .LBB0_279
	s_waitcnt vmcnt(0)
	s_cmpk_lt_u32 s24, 0x100
	s_cbranch_scc0 .LBB0_282
	s_barrier

; #define G_BAR() __builtin_amdgcn_s_barrier()
; #define G_SCHED() __builtin_amdgcn_sched_barrier(0)
; #define D_STAGE_A(slot, half, kt) D_STAGE(rsA, voffA, slot, half, kt)
; #define D_STAGE_B(slot, half, kt) D_STAGE(rsB, voffB, slot, half, kt)
; #define D_LDA(dst, slot) do { _Pragma("unroll") for (int m = 0; m < 4; ++m) _Pragma("unroll") for (int k = 0; k < 2; ++k) \
;     dst[m][k] = *(const LDS_AS bf16x8*)(lds + (slot) + aoff + m * 2048 + k * 1024); } while (0)
; #define D_LDB(dst, slot) do { _Pragma("unroll") for (int n = 0; n < 2; ++n) _Pragma("unroll") for (int k = 0; k < 2; ++k) \
;     dst[n][k] = *(const LDS_AS bf16x8*)(lds + (slot) + boff + n * 2048 + k * 1024); } while (0)
; #define D_MMA(ai, bj, At, Bf) do { __builtin_amdgcn_s_setprio(1); _Pragma("unroll") for (int m = 0; m < 4; ++m) _Pragma("unroll") for (int n = 0; n < 2; ++n) _Pragma("unroll") for (int k = 0; k < 2; ++k) \
;     acc[ai][bj][m][n] = __builtin_amdgcn_mfma_f32_16x16x32_bf16(Bf[n][k], At[m][k], acc[ai][bj][m][n], 0, 0, 0); __builtin_amdgcn_s_setprio(0); } while (0)
; #define D_WAIT_L(n) asm volatile("s_waitcnt lgkmcnt(" #n ")" ::: "memory")
; #define D_STAGE_A(slot, half, kt) D_STAGE(rsA, voffA, slot, half, kt)
; #define D_STAGE_B(slot, half, kt) do { _Pragma("unroll") for (int _i = 0; _i < 2; ++_i) { const unsigned _m0 = ldsw + (unsigned)((slot) + _i * 8192); const unsigned _so = (unsigned)(kt) * 128u + (half) * bt_half + _i * bt_piece; \
;     asm volatile("s_mov_b32 m0, %0\n\ts_nop 4\n\tbuffer_load_dwordx4 %1, %2, %3 offen lds" :: "s"(_m0), "v"(voffB0), "s"(rsB), "s"(_so) : "m0", "memory"); } } while (0)
; template <class Cfg>
; DI void gemm256dma_unit(LDS_AS unsigned char* lds, const Cfg& cfg) {
;     ...
;   for (int t = 0; t < nt; t += 2) {
;     const int t1 = t + 1;
;     const int t2 = (t + 2 < nt) ? t + 2 : 0;
;     const int t3 = (t + 2 < nt) ? t + 3 : 1;
;     D_LDB(B0, G_SB(0, 0)); G_SCHED(); D_LDA(At, G_SA(0, 0)); D_STAGE_A(G_SA(1, 1), 1, t1);
;     D_WAIT_L(8); G_BAR(); D_WAIT_L(0); G_SCHED(); D_MMA(0, 0, At, B0); G_BAR(); G_SCHED();
;     D_LDB(B1, G_SB(0, 1)); D_STAGE_B(G_SB(0, 0), 0, t2);
;     G_BAR(); D_WAIT_L(0); G_SCHED(); D_MMA(0, 1, At, B1); G_BAR(); G_SCHED();
;     D_LDA(At, G_SA(0, 1)); D_STAGE_A(G_SA(0, 0), 0, t2);
;     G_BAR(); D_WAIT_L(0); G_SCHED(); D_MMA(1, 0, At, B0); G_BAR(); G_SCHED();
.LBB0_830:
	v_add_u32_e32 v139, 0x10010, v136
	ds_read_b128 v[140:143], v139
	ds_read_b128 v[144:147], v139 offset:1024
	ds_read_b128 v[148:151], v139 offset:2048
	ds_read_b128 v[152:155], v139 offset:3072
	s_add_i32 s54, s47, 2
	s_add_i32 s38, s46, 0xffffff00
	s_add_i32 s55, s46, 0xffffff80
	s_cmp_lt_u32 s47, 6
	s_cselect_b32 s60, s55, 0
	s_cselect_b32 s55, s46, 0x80
	s_addk_i32 s46, 0x100
	s_cmp_gt_u32 s47, 5
	ds_read_b128 v[156:159], v137 offset:16
	ds_read_b128 v[160:163], v137 offset:1040
	ds_read_b128 v[164:167], v137 offset:2064
	ds_read_b128 v[168:171], v137 offset:3088
	ds_read_b128 v[172:175], v137 offset:4112
	ds_read_b128 v[176:179], v137 offset:5136
	ds_read_b128 v[180:183], v137 offset:6160
	ds_read_b128 v[184:187], v137 offset:7184
	s_mov_b32 m0, s42
	s_nop 0
	buffer_load_dwordx4 v134, s[12:15], s38 offen lds
	s_nop 0
	s_mov_b32 m0, s43
	s_nop 0
	buffer_load_dwordx4 v131, s[12:15], s38 offen lds
	s_waitcnt lgkmcnt(8)
	s_waitcnt vmcnt(10)
	s_barrier
	s_waitcnt lgkmcnt(0)
	s_setprio 1
	s_waitcnt lgkmcnt(7)
	v_mfma_f32_16x16x32_bf16 v[124:127], v[140:143], v[156:159], v[124:127]
	v_mfma_f32_16x16x32_bf16 v[120:123], v[148:151], v[156:159], v[120:123]
	s_waitcnt lgkmcnt(5)
	v_mfma_f32_16x16x32_bf16 v[108:111], v[140:143], v[164:167], v[108:111]
	v_mfma_f32_16x16x32_bf16 v[104:107], v[148:151], v[164:167], v[104:107]
	s_waitcnt lgkmcnt(3)
	v_mfma_f32_16x16x32_bf16 v[92:95], v[140:143], v[172:175], v[92:95]
	v_mfma_f32_16x16x32_bf16 v[88:91], v[148:151], v[172:175], v[88:91]
	s_waitcnt lgkmcnt(1)
	v_mfma_f32_16x16x32_bf16 v[76:79], v[140:143], v[180:183], v[76:79]
	v_mfma_f32_16x16x32_bf16 v[72:75], v[148:151], v[180:183], v[72:75]
	v_mfma_f32_16x16x32_bf16 v[124:127], v[144:147], v[160:163], v[124:127]
	v_mfma_f32_16x16x32_bf16 v[120:123], v[152:155], v[160:163], v[120:123]
	v_mfma_f32_16x16x32_bf16 v[108:111], v[144:147], v[168:171], v[108:111]
	v_mfma_f32_16x16x32_bf16 v[104:107], v[152:155], v[168:171], v[104:107]
	v_mfma_f32_16x16x32_bf16 v[92:95], v[144:147], v[176:179], v[92:95]
	v_mfma_f32_16x16x32_bf16 v[88:91], v[152:155], v[176:179], v[88:91]
	s_waitcnt lgkmcnt(0)
	v_mfma_f32_16x16x32_bf16 v[76:79], v[144:147], v[184:187], v[76:79]
	v_mfma_f32_16x16x32_bf16 v[72:75], v[152:155], v[184:187], v[72:75]
	s_setprio 0
	s_barrier
	v_add_u32_e32 v139, 0x14010, v136
	ds_read_b128 v[192:195], v139
	ds_read_b128 v[196:199], v139 offset:1024
	ds_read_b128 v[200:203], v139 offset:2048
	ds_read_b128 v[204:207], v139 offset:3072
	s_mov_b32 m0, s3
	s_nop 0
	buffer_load_dwordx4 v132, s[8:11], s60 offen lds
	s_nop 0
	s_mov_b32 m0, s19
	s_nop 0
	buffer_load_dwordx4 v128, s[8:11], s60 offen lds
	s_waitcnt vmcnt(10)
	s_barrier
	s_waitcnt lgkmcnt(0)
	s_setprio 1
	s_waitcnt lgkmcnt(3)
	v_mfma_f32_16x16x32_bf16 v[116:119], v[192:195], v[156:159], v[116:119]
	s_waitcnt lgkmcnt(1)
	v_mfma_f32_16x16x32_bf16 v[112:115], v[200:203], v[156:159], v[112:115]
	v_mfma_f32_16x16x32_bf16 v[100:103], v[192:195], v[164:167], v[100:103]
	v_mfma_f32_16x16x32_bf16 v[96:99], v[200:203], v[164:167], v[96:99]
	v_mfma_f32_16x16x32_bf16 v[84:87], v[192:195], v[172:175], v[84:87]
	v_mfma_f32_16x16x32_bf16 v[80:83], v[200:203], v[172:175], v[80:83]
	v_mfma_f32_16x16x32_bf16 v[68:71], v[192:195], v[180:183], v[68:71]
	v_mfma_f32_16x16x32_bf16 v[64:67], v[200:203], v[180:183], v[64:67]
	v_mfma_f32_16x16x32_bf16 v[116:119], v[196:199], v[160:163], v[116:119]
	s_waitcnt lgkmcnt(0)
	v_mfma_f32_16x16x32_bf16 v[112:115], v[204:207], v[160:163], v[112:115]
	v_mfma_f32_16x16x32_bf16 v[100:103], v[196:199], v[168:171], v[100:103]
	v_mfma_f32_16x16x32_bf16 v[96:99], v[204:207], v[168:171], v[96:99]
	v_mfma_f32_16x16x32_bf16 v[84:87], v[196:199], v[176:179], v[84:87]
	v_mfma_f32_16x16x32_bf16 v[80:83], v[204:207], v[176:179], v[80:83]
	v_mfma_f32_16x16x32_bf16 v[68:71], v[196:199], v[184:187], v[68:71]
	v_mfma_f32_16x16x32_bf16 v[64:67], v[204:207], v[184:187], v[64:67]
	s_setprio 0
	s_barrier
	ds_read_b128 v[156:159], v137 offset:16400
	ds_read_b128 v[160:163], v137 offset:17424
	ds_read_b128 v[164:167], v137 offset:18448
	ds_read_b128 v[168:171], v137 offset:19472
	ds_read_b128 v[172:175], v137 offset:20496
	ds_read_b128 v[176:179], v137 offset:21520
	ds_read_b128 v[180:183], v137 offset:22544
	ds_read_b128 v[184:187], v137 offset:23568
	s_mov_b32 m0, s2
	s_nop 0
	buffer_load_dwordx4 v133, s[12:15], s60 offen lds
	s_nop 0
	s_mov_b32 m0, s26
	s_nop 0
	buffer_load_dwordx4 v130, s[12:15], s60 offen lds
	s_barrier
	s_waitcnt lgkmcnt(0)
	s_setprio 1
	s_waitcnt lgkmcnt(7)
	v_mfma_f32_16x16x32_bf16 v[60:63], v[140:143], v[156:159], v[60:63]
	v_mfma_f32_16x16x32_bf16 v[56:59], v[148:151], v[156:159], v[56:59]
	s_waitcnt lgkmcnt(5)
	v_mfma_f32_16x16x32_bf16 v[44:47], v[140:143], v[164:167], v[44:47]
	v_mfma_f32_16x16x32_bf16 v[40:43], v[148:151], v[164:167], v[40:43]
	s_waitcnt lgkmcnt(3)
	v_mfma_f32_16x16x32_bf16 v[28:31], v[140:143], v[172:175], v[28:31]
	v_mfma_f32_16x16x32_bf16 v[24:27], v[148:151], v[172:175], v[24:27]
	s_waitcnt lgkmcnt(1)
	v_mfma_f32_16x16x32_bf16 v[12:15], v[140:143], v[180:183], v[12:15]
	v_mfma_f32_16x16x32_bf16 v[8:11], v[148:151], v[180:183], v[8:11]
	v_mfma_f32_16x16x32_bf16 v[60:63], v[144:147], v[160:163], v[60:63]
	v_mfma_f32_16x16x32_bf16 v[56:59], v[152:155], v[160:163], v[56:59]
	v_mfma_f32_16x16x32_bf16 v[44:47], v[144:147], v[168:171], v[44:47]
	v_mfma_f32_16x16x32_bf16 v[40:43], v[152:155], v[168:171], v[40:43]
	v_mfma_f32_16x16x32_bf16 v[28:31], v[144:147], v[176:179], v[28:31]
	v_mfma_f32_16x16x32_bf16 v[24:27], v[152:155], v[176:179], v[24:27]
	s_waitcnt lgkmcnt(0)
	v_mfma_f32_16x16x32_bf16 v[12:15], v[144:147], v[184:187], v[12:15]
	v_mfma_f32_16x16x32_bf16 v[8:11], v[152:155], v[184:187], v[8:11]
	s_setprio 0
	s_barrier
; #define G_WAIT_V(n) asm volatile("s_waitcnt vmcnt(" #n ")" ::: "memory")
; #define G_BAR() __builtin_amdgcn_s_barrier()
; #define G_SCHED() __builtin_amdgcn_sched_barrier(0)
; #define D_STAGE_A(slot, half, kt) D_STAGE(rsA, voffA, slot, half, kt)
; #define D_STAGE_B(slot, half, kt) D_STAGE(rsB, voffB, slot, half, kt)
; #define D_LDA(dst, slot) do { _Pragma("unroll") for (int m = 0; m < 4; ++m) _Pragma("unroll") for (int k = 0; k < 2; ++k) \
;     dst[m][k] = *(const LDS_AS bf16x8*)(lds + (slot) + aoff + m * 2048 + k * 1024); } while (0)
; #define D_LDB(dst, slot) do { _Pragma("unroll") for (int n = 0; n < 2; ++n) _Pragma("unroll") for (int k = 0; k < 2; ++k) \
;     dst[n][k] = *(const LDS_AS bf16x8*)(lds + (slot) + boff + n * 2048 + k * 1024); } while (0)
; #define D_MMA(ai, bj, At, Bf) do { __builtin_amdgcn_s_setprio(1); _Pragma("unroll") for (int m = 0; m < 4; ++m) _Pragma("unroll") for (int n = 0; n < 2; ++n) _Pragma("unroll") for (int k = 0; k < 2; ++k) \
;     acc[ai][bj][m][n] = __builtin_amdgcn_mfma_f32_16x16x32_bf16(Bf[n][k], At[m][k], acc[ai][bj][m][n], 0, 0, 0); __builtin_amdgcn_s_setprio(0); } while (0)
; #define D_WAIT_L(n) asm volatile("s_waitcnt lgkmcnt(" #n ")" ::: "memory")
; #define D_STAGE_A(slot, half, kt) D_STAGE(rsA, voffA, slot, half, kt)
; #define D_STAGE_B(slot, half, kt) do { _Pragma("unroll") for (int _i = 0; _i < 2; ++_i) { const unsigned _m0 = ldsw + (unsigned)((slot) + _i * 8192); const unsigned _so = (unsigned)(kt) * 128u + (half) * bt_half + _i * bt_piece; \
;     asm volatile("s_mov_b32 m0, %0\n\ts_nop 4\n\tbuffer_load_dwordx4 %1, %2, %3 offen lds" :: "s"(_m0), "v"(voffB0), "s"(rsB), "s"(_so) : "m0", "memory"); } } while (0)
; #define D_WAIT_L(n) asm volatile("s_waitcnt lgkmcnt(" #n ")" ::: "memory")
; template <class Cfg>
; DI void gemm256dma_unit(LDS_AS unsigned char* lds, const Cfg& cfg) {
;     ...
;     D_STAGE_B(G_SB(0, 1), 1, t2);
;     G_WAIT_V(6); G_BAR(); G_SCHED(); D_MMA(1, 1, At, B1); G_BAR(); G_SCHED();
;     D_LDB(B0, G_SB(1, 0)); G_SCHED(); D_LDA(At, G_SA(1, 0)); D_STAGE_A(G_SA(0, 1), 1, t2);
;     D_WAIT_L(8); G_BAR(); D_WAIT_L(0); G_SCHED(); D_MMA(0, 0, At, B0); G_BAR(); G_SCHED();
;     D_LDB(B1, G_SB(1, 1)); D_STAGE_B(G_SB(1, 0), 0, t3);
;     G_BAR(); D_WAIT_L(0); G_SCHED(); D_MMA(0, 1, At, B1); G_BAR(); G_SCHED();
	s_mov_b32 m0, s27
	s_nop 0
	buffer_load_dwordx4 v129, s[8:11], s60 offen lds
	s_nop 0
	s_mov_b32 m0, s28
	s_nop 0
	buffer_load_dwordx4 v135, s[8:11], s60 offen lds
	s_waitcnt vmcnt(10)
	s_barrier
	s_setprio 1
	v_mfma_f32_16x16x32_bf16 v[52:55], v[192:195], v[156:159], v[52:55]
	v_mfma_f32_16x16x32_bf16 v[48:51], v[200:203], v[156:159], v[48:51]
	v_mfma_f32_16x16x32_bf16 v[36:39], v[192:195], v[164:167], v[36:39]
	v_mfma_f32_16x16x32_bf16 v[32:35], v[200:203], v[164:167], v[32:35]
	v_mfma_f32_16x16x32_bf16 v[20:23], v[192:195], v[172:175], v[20:23]
	v_mfma_f32_16x16x32_bf16 v[16:19], v[200:203], v[172:175], v[16:19]
	v_mfma_f32_16x16x32_bf16 v[4:7], v[192:195], v[180:183], v[4:7]
	v_mfma_f32_16x16x32_bf16 v[0:3], v[200:203], v[180:183], v[0:3]
	v_mfma_f32_16x16x32_bf16 v[52:55], v[196:199], v[160:163], v[52:55]
	v_mfma_f32_16x16x32_bf16 v[48:51], v[204:207], v[160:163], v[48:51]
	v_mfma_f32_16x16x32_bf16 v[36:39], v[196:199], v[168:171], v[36:39]
	v_mfma_f32_16x16x32_bf16 v[32:35], v[204:207], v[168:171], v[32:35]
	v_mfma_f32_16x16x32_bf16 v[20:23], v[196:199], v[176:179], v[20:23]
	v_mfma_f32_16x16x32_bf16 v[16:19], v[204:207], v[176:179], v[16:19]
	v_mfma_f32_16x16x32_bf16 v[4:7], v[196:199], v[184:187], v[4:7]
	v_mfma_f32_16x16x32_bf16 v[0:3], v[204:207], v[184:187], v[0:3]
	s_setprio 0
	s_barrier
	v_add_u32_e32 v139, 0x18010, v136
	ds_read_b128 v[140:143], v139
	ds_read_b128 v[144:147], v139 offset:1024
	ds_read_b128 v[148:151], v139 offset:2048
	ds_read_b128 v[152:155], v139 offset:3072
	ds_read_b128 v[156:159], v137 offset:32784
	ds_read_b128 v[160:163], v137 offset:33808
	ds_read_b128 v[164:167], v137 offset:34832
	ds_read_b128 v[168:171], v137 offset:35856
	ds_read_b128 v[172:175], v137 offset:36880
	ds_read_b128 v[176:179], v137 offset:37904
	ds_read_b128 v[180:183], v137 offset:38928
	ds_read_b128 v[184:187], v137 offset:39952
	s_mov_b32 m0, s30
	s_nop 0
	buffer_load_dwordx4 v134, s[12:15], s60 offen lds
	s_nop 0
	s_mov_b32 m0, s31
	s_nop 0
	buffer_load_dwordx4 v131, s[12:15], s60 offen lds
	s_waitcnt lgkmcnt(8)
	s_waitcnt vmcnt(10)
	s_barrier
	s_waitcnt lgkmcnt(0)
	s_setprio 1
	s_waitcnt lgkmcnt(7)
	v_mfma_f32_16x16x32_bf16 v[124:127], v[140:143], v[156:159], v[124:127]
	v_mfma_f32_16x16x32_bf16 v[120:123], v[148:151], v[156:159], v[120:123]
	s_waitcnt lgkmcnt(5)
	v_mfma_f32_16x16x32_bf16 v[108:111], v[140:143], v[164:167], v[108:111]
	v_mfma_f32_16x16x32_bf16 v[104:107], v[148:151], v[164:167], v[104:107]
	s_waitcnt lgkmcnt(3)
	v_mfma_f32_16x16x32_bf16 v[92:95], v[140:143], v[172:175], v[92:95]
	v_mfma_f32_16x16x32_bf16 v[88:91], v[148:151], v[172:175], v[88:91]
	s_waitcnt lgkmcnt(1)
	v_mfma_f32_16x16x32_bf16 v[76:79], v[140:143], v[180:183], v[76:79]
	v_mfma_f32_16x16x32_bf16 v[72:75], v[148:151], v[180:183], v[72:75]
	v_mfma_f32_16x16x32_bf16 v[124:127], v[144:147], v[160:163], v[124:127]
	v_mfma_f32_16x16x32_bf16 v[120:123], v[152:155], v[160:163], v[120:123]
	v_mfma_f32_16x16x32_bf16 v[108:111], v[144:147], v[168:171], v[108:111]
	v_mfma_f32_16x16x32_bf16 v[104:107], v[152:155], v[168:171], v[104:107]
	v_mfma_f32_16x16x32_bf16 v[92:95], v[144:147], v[176:179], v[92:95]
	v_mfma_f32_16x16x32_bf16 v[88:91], v[152:155], v[176:179], v[88:91]
	s_waitcnt lgkmcnt(0)
	v_mfma_f32_16x16x32_bf16 v[76:79], v[144:147], v[184:187], v[76:79]
	v_mfma_f32_16x16x32_bf16 v[72:75], v[152:155], v[184:187], v[72:75]
	s_setprio 0
	s_barrier
	v_add_u32_e32 v139, 0x1c010, v136
	ds_read_b128 v[192:195], v139
	ds_read_b128 v[196:199], v139 offset:1024
	ds_read_b128 v[200:203], v139 offset:2048
	ds_read_b128 v[204:207], v139 offset:3072
	s_mov_b32 m0, s33
	s_nop 0
	buffer_load_dwordx4 v132, s[8:11], s55 offen lds
	s_nop 0
	s_mov_b32 m0, s34
	s_nop 0
	buffer_load_dwordx4 v128, s[8:11], s55 offen lds
	s_waitcnt vmcnt(10)
	s_barrier
; #define G_WAIT_V(n) asm volatile("s_waitcnt vmcnt(" #n ")" ::: "memory")
; #define G_BAR() __builtin_amdgcn_s_barrier()
; #define G_SCHED() __builtin_amdgcn_sched_barrier(0)
; #define D_STAGE_A(slot, half, kt) D_STAGE(rsA, voffA, slot, half, kt)
; #define D_STAGE_B(slot, half, kt) D_STAGE(rsB, voffB, slot, half, kt)
; #define D_LDA(dst, slot) do { _Pragma("unroll") for (int m = 0; m < 4; ++m) _Pragma("unroll") for (int k = 0; k < 2; ++k) \
;     dst[m][k] = *(const LDS_AS bf16x8*)(lds + (slot) + aoff + m * 2048 + k * 1024); } while (0)
; #define D_MMA(ai, bj, At, Bf) do { __builtin_amdgcn_s_setprio(1); _Pragma("unroll") for (int m = 0; m < 4; ++m) _Pragma("unroll") for (int n = 0; n < 2; ++n) _Pragma("unroll") for (int k = 0; k < 2; ++k) \
;     acc[ai][bj][m][n] = __builtin_amdgcn_mfma_f32_16x16x32_bf16(Bf[n][k], At[m][k], acc[ai][bj][m][n], 0, 0, 0); __builtin_amdgcn_s_setprio(0); } while (0)
; #define D_WAIT_L(n) asm volatile("s_waitcnt lgkmcnt(" #n ")" ::: "memory")
; #define D_STAGE_A(slot, half, kt) D_STAGE(rsA, voffA, slot, half, kt)
; #define D_STAGE_B(slot, half, kt) do { _Pragma("unroll") for (int _i = 0; _i < 2; ++_i) { const unsigned _m0 = ldsw + (unsigned)((slot) + _i * 8192); const unsigned _so = (unsigned)(kt) * 128u + (half) * bt_half + _i * bt_piece; \
;     asm volatile("s_mov_b32 m0, %0\n\ts_nop 4\n\tbuffer_load_dwordx4 %1, %2, %3 offen lds" :: "s"(_m0), "v"(voffB0), "s"(rsB), "s"(_so) : "m0", "memory"); } } while (0)
; #define D_LDA(dst, slot) do { _Pragma("unroll") for (int m = 0; m < 4; ++m) { \
;     const i32x4 _lo = *(const LDS_AS i32x4*)(lds + (slot) + aoff[0] + m * 2048); const i32x4 _hi = *(const LDS_AS i32x4*)(lds + (slot) + aoff[1] + m * 2048); \
;     dst[m] = __builtin_shufflevector(_lo, _hi, 0, 1, 2, 3, 4, 5, 6, 7); } } while (0)
; #define D_WAIT_L(n) asm volatile("s_waitcnt lgkmcnt(" #n ")" ::: "memory")
; template <class Cfg>
; DI void gemm256dma_unit(LDS_AS unsigned char* lds, const Cfg& cfg) {
;     ...
;     D_LDA(At, G_SA(1, 1)); D_STAGE_A(G_SA(1, 0), 0, t3);
;     G_BAR(); D_WAIT_L(0); G_SCHED(); D_MMA(1, 0, At, B0); G_BAR(); G_SCHED();
;     D_STAGE_B(G_SB(1, 1), 1, t3);
;     G_WAIT_V(6); G_BAR(); G_SCHED(); D_MMA(1, 1, At, B1); G_BAR(); G_SCHED();
;   }
;   G_WAIT_V(0);
;   if (wr == 0) G_BAR();
	s_waitcnt lgkmcnt(0)
	s_setprio 1
	s_waitcnt lgkmcnt(3)
	v_mfma_f32_16x16x32_bf16 v[116:119], v[192:195], v[156:159], v[116:119]
	s_waitcnt lgkmcnt(1)
	v_mfma_f32_16x16x32_bf16 v[112:115], v[200:203], v[156:159], v[112:115]
	v_mfma_f32_16x16x32_bf16 v[100:103], v[192:195], v[164:167], v[100:103]
	v_mfma_f32_16x16x32_bf16 v[96:99], v[200:203], v[164:167], v[96:99]
	v_mfma_f32_16x16x32_bf16 v[84:87], v[192:195], v[172:175], v[84:87]
	v_mfma_f32_16x16x32_bf16 v[80:83], v[200:203], v[172:175], v[80:83]
	v_mfma_f32_16x16x32_bf16 v[68:71], v[192:195], v[180:183], v[68:71]
	v_mfma_f32_16x16x32_bf16 v[64:67], v[200:203], v[180:183], v[64:67]
	v_mfma_f32_16x16x32_bf16 v[116:119], v[196:199], v[160:163], v[116:119]
	s_waitcnt lgkmcnt(0)
	v_mfma_f32_16x16x32_bf16 v[112:115], v[204:207], v[160:163], v[112:115]
	v_mfma_f32_16x16x32_bf16 v[100:103], v[196:199], v[168:171], v[100:103]
	v_mfma_f32_16x16x32_bf16 v[96:99], v[204:207], v[168:171], v[96:99]
	v_mfma_f32_16x16x32_bf16 v[84:87], v[196:199], v[176:179], v[84:87]
	v_mfma_f32_16x16x32_bf16 v[80:83], v[204:207], v[176:179], v[80:83]
	v_mfma_f32_16x16x32_bf16 v[68:71], v[196:199], v[184:187], v[68:71]
	v_mfma_f32_16x16x32_bf16 v[64:67], v[204:207], v[184:187], v[64:67]
	s_setprio 0
	s_barrier
	ds_read_b128 v[156:159], v137 offset:49168
	ds_read_b128 v[160:163], v137 offset:50192
	ds_read_b128 v[164:167], v137 offset:51216
	ds_read_b128 v[168:171], v137 offset:52240
	ds_read_b128 v[172:175], v137 offset:53264
	ds_read_b128 v[176:179], v137 offset:54288
	ds_read_b128 v[180:183], v137 offset:55312
	ds_read_b128 v[184:187], v137 offset:56336
	s_mov_b32 m0, s35
	s_nop 0
	buffer_load_dwordx4 v133, s[12:15], s55 offen lds
	s_nop 0
	s_mov_b32 m0, s36
	s_nop 0
	buffer_load_dwordx4 v130, s[12:15], s55 offen lds
	s_barrier
	s_waitcnt lgkmcnt(0)
	s_setprio 1
	s_waitcnt lgkmcnt(7)
	v_mfma_f32_16x16x32_bf16 v[60:63], v[140:143], v[156:159], v[60:63]
	v_mfma_f32_16x16x32_bf16 v[56:59], v[148:151], v[156:159], v[56:59]
	s_waitcnt lgkmcnt(5)
	v_mfma_f32_16x16x32_bf16 v[44:47], v[140:143], v[164:167], v[44:47]
	v_mfma_f32_16x16x32_bf16 v[40:43], v[148:151], v[164:167], v[40:43]
	s_waitcnt lgkmcnt(3)
	v_mfma_f32_16x16x32_bf16 v[28:31], v[140:143], v[172:175], v[28:31]
	v_mfma_f32_16x16x32_bf16 v[24:27], v[148:151], v[172:175], v[24:27]
	s_waitcnt lgkmcnt(1)
	v_mfma_f32_16x16x32_bf16 v[12:15], v[140:143], v[180:183], v[12:15]
	v_mfma_f32_16x16x32_bf16 v[8:11], v[148:151], v[180:183], v[8:11]
	v_mfma_f32_16x16x32_bf16 v[60:63], v[144:147], v[160:163], v[60:63]
	v_mfma_f32_16x16x32_bf16 v[56:59], v[152:155], v[160:163], v[56:59]
	v_mfma_f32_16x16x32_bf16 v[44:47], v[144:147], v[168:171], v[44:47]
	v_mfma_f32_16x16x32_bf16 v[40:43], v[152:155], v[168:171], v[40:43]
	v_mfma_f32_16x16x32_bf16 v[28:31], v[144:147], v[176:179], v[28:31]
	v_mfma_f32_16x16x32_bf16 v[24:27], v[152:155], v[176:179], v[24:27]
	s_waitcnt lgkmcnt(0)
	v_mfma_f32_16x16x32_bf16 v[12:15], v[144:147], v[184:187], v[12:15]
	v_mfma_f32_16x16x32_bf16 v[8:11], v[152:155], v[184:187], v[8:11]
	s_setprio 0
	s_barrier
	s_mov_b32 m0, s37
	s_nop 0
	buffer_load_dwordx4 v129, s[8:11], s55 offen lds
	s_nop 0
	s_mov_b32 m0, s39
	s_nop 0
	buffer_load_dwordx4 v135, s[8:11], s55 offen lds
	s_waitcnt vmcnt(10)
	s_barrier
	s_setprio 1
	v_mfma_f32_16x16x32_bf16 v[52:55], v[192:195], v[156:159], v[52:55]
	v_mfma_f32_16x16x32_bf16 v[48:51], v[200:203], v[156:159], v[48:51]
	v_mfma_f32_16x16x32_bf16 v[36:39], v[192:195], v[164:167], v[36:39]
	v_mfma_f32_16x16x32_bf16 v[32:35], v[200:203], v[164:167], v[32:35]
	v_mfma_f32_16x16x32_bf16 v[20:23], v[192:195], v[172:175], v[20:23]
	v_mfma_f32_16x16x32_bf16 v[16:19], v[200:203], v[172:175], v[16:19]
	v_mfma_f32_16x16x32_bf16 v[4:7], v[192:195], v[180:183], v[4:7]
	v_mfma_f32_16x16x32_bf16 v[0:3], v[200:203], v[180:183], v[0:3]
	v_mfma_f32_16x16x32_bf16 v[52:55], v[196:199], v[160:163], v[52:55]
	v_mfma_f32_16x16x32_bf16 v[48:51], v[204:207], v[160:163], v[48:51]
	v_mfma_f32_16x16x32_bf16 v[36:39], v[196:199], v[168:171], v[36:39]
	v_mfma_f32_16x16x32_bf16 v[32:35], v[204:207], v[168:171], v[32:35]
	v_mfma_f32_16x16x32_bf16 v[20:23], v[196:199], v[176:179], v[20:23]
	v_mfma_f32_16x16x32_bf16 v[16:19], v[204:207], v[176:179], v[16:19]
	v_mfma_f32_16x16x32_bf16 v[4:7], v[196:199], v[184:187], v[4:7]
	v_mfma_f32_16x16x32_bf16 v[0:3], v[204:207], v[184:187], v[0:3]
	s_setprio 0
	s_barrier
	s_mov_b32 s47, s54
	s_cbranch_scc0 .LBB0_830
	s_waitcnt vmcnt(0)
	s_cmpk_lt_u32 s16, 0x100
	s_cbranch_scc0 .LBB0_833
	s_barrier

; #define G_BAR() __builtin_amdgcn_s_barrier()
; #define G_SCHED() __builtin_amdgcn_sched_barrier(0)
; #define D_STAGE_A(slot, half, kt) D_STAGE(rsA, voffA, slot, half, kt)
; #define D_STAGE_B(slot, half, kt) D_STAGE(rsB, voffB, slot, half, kt)
; #define D_LDA(dst, slot) do { _Pragma("unroll") for (int m = 0; m < 4; ++m) _Pragma("unroll") for (int k = 0; k < 2; ++k) \
;     dst[m][k] = *(const LDS_AS bf16x8*)(lds + (slot) + aoff + m * 2048 + k * 1024); } while (0)
; #define D_LDB(dst, slot) do { _Pragma("unroll") for (int n = 0; n < 2; ++n) _Pragma("unroll") for (int k = 0; k < 2; ++k) \
;     dst[n][k] = *(const LDS_AS bf16x8*)(lds + (slot) + boff + n * 2048 + k * 1024); } while (0)
; #define D_MMA(ai, bj, At, Bf) do { __builtin_amdgcn_s_setprio(1); _Pragma("unroll") for (int m = 0; m < 4; ++m) _Pragma("unroll") for (int n = 0; n < 2; ++n) _Pragma("unroll") for (int k = 0; k < 2; ++k) \
;     acc[ai][bj][m][n] = __builtin_amdgcn_mfma_f32_16x16x32_bf16(Bf[n][k], At[m][k], acc[ai][bj][m][n], 0, 0, 0); __builtin_amdgcn_s_setprio(0); } while (0)
; #define D_WAIT_L(n) asm volatile("s_waitcnt lgkmcnt(" #n ")" ::: "memory")
; #define D_STAGE_A(slot, half, kt) D_STAGE(rsA, voffA, slot, half, kt)
; #define D_STAGE_B(slot, half, kt) do { _Pragma("unroll") for (int _i = 0; _i < 2; ++_i) { const unsigned _m0 = ldsw + (unsigned)((slot) + _i * 8192); const unsigned _so = (unsigned)(kt) * 128u + (half) * bt_half + _i * bt_piece; \
;     asm volatile("s_mov_b32 m0, %0\n\ts_nop 4\n\tbuffer_load_dwordx4 %1, %2, %3 offen lds" :: "s"(_m0), "v"(voffB0), "s"(rsB), "s"(_so) : "m0", "memory"); } } while (0)
; template <class Cfg>
; DI void gemm256dma_unit(LDS_AS unsigned char* lds, const Cfg& cfg) {
;     ...
;   for (int t = 0; t < nt; t += 2) {
;     const int t1 = t + 1;
;     const int t2 = (t + 2 < nt) ? t + 2 : 0;
;     const int t3 = (t + 2 < nt) ? t + 3 : 1;
;     D_LDB(B0, G_SB(0, 0)); G_SCHED(); D_LDA(At, G_SA(0, 0)); D_STAGE_A(G_SA(1, 1), 1, t1);
;     D_WAIT_L(8); G_BAR(); D_WAIT_L(0); G_SCHED(); D_MMA(0, 0, At, B0); G_BAR(); G_SCHED();
;     D_LDB(B1, G_SB(0, 1)); D_STAGE_B(G_SB(0, 0), 0, t2);
;     G_BAR(); D_WAIT_L(0); G_SCHED(); D_MMA(0, 1, At, B1); G_BAR(); G_SCHED();
;     D_LDA(At, G_SA(0, 1)); D_STAGE_A(G_SA(0, 0), 0, t2);
;     G_BAR(); D_WAIT_L(0); G_SCHED(); D_MMA(1, 0, At, B0); G_BAR(); G_SCHED();
.LBB0_1266:
	ds_read_b128 v[142:145], v137
	ds_read_b128 v[146:149], v137 offset:1024
	ds_read_b128 v[150:153], v137 offset:2048
	ds_read_b128 v[154:157], v137 offset:3072
	s_add_i32 s34, s33, 2
	s_add_i32 s36, s31, 0xffffff00
	s_add_i32 s35, s31, 0xffffff80
	s_cmp_lt_u32 s33, 30
	s_cselect_b32 s37, s35, 0
	s_cselect_b32 s35, s31, 0x80
	s_addk_i32 s31, 0x100
	s_cmp_gt_u32 s33, 29
	ds_read_b128 v[158:161], v138 offset:16
	ds_read_b128 v[162:165], v138 offset:1040
	ds_read_b128 v[166:169], v138 offset:2064
	ds_read_b128 v[170:173], v138 offset:3088
	ds_read_b128 v[174:177], v138 offset:4112
	ds_read_b128 v[178:181], v138 offset:5136
	ds_read_b128 v[182:185], v138 offset:6160
	ds_read_b128 v[186:189], v138 offset:7184
	s_mov_b32 m0, s29
	s_nop 0
	buffer_load_dwordx4 v129, s[0:3], s36 offen lds
	s_nop 0
	s_mov_b32 m0, s30
	s_nop 0
	buffer_load_dwordx4 v134, s[0:3], s36 offen lds
	s_waitcnt lgkmcnt(8)
	s_waitcnt vmcnt(10)
	s_barrier
	s_waitcnt lgkmcnt(0)
	s_setprio 1
	s_waitcnt lgkmcnt(7)
	v_mfma_f32_16x16x32_bf16 v[124:127], v[142:145], v[158:161], v[124:127]
	v_mfma_f32_16x16x32_bf16 v[120:123], v[150:153], v[158:161], v[120:123]
	s_waitcnt lgkmcnt(5)
	v_mfma_f32_16x16x32_bf16 v[108:111], v[142:145], v[166:169], v[108:111]
	v_mfma_f32_16x16x32_bf16 v[104:107], v[150:153], v[166:169], v[104:107]
	s_waitcnt lgkmcnt(3)
	v_mfma_f32_16x16x32_bf16 v[92:95], v[142:145], v[174:177], v[92:95]
	v_mfma_f32_16x16x32_bf16 v[88:91], v[150:153], v[174:177], v[88:91]
	s_waitcnt lgkmcnt(1)
	v_mfma_f32_16x16x32_bf16 v[76:79], v[142:145], v[182:185], v[76:79]
	v_mfma_f32_16x16x32_bf16 v[72:75], v[150:153], v[182:185], v[72:75]
	v_mfma_f32_16x16x32_bf16 v[124:127], v[146:149], v[162:165], v[124:127]
	v_mfma_f32_16x16x32_bf16 v[120:123], v[154:157], v[162:165], v[120:123]
	v_mfma_f32_16x16x32_bf16 v[108:111], v[146:149], v[170:173], v[108:111]
	v_mfma_f32_16x16x32_bf16 v[104:107], v[154:157], v[170:173], v[104:107]
	v_mfma_f32_16x16x32_bf16 v[92:95], v[146:149], v[178:181], v[92:95]
	v_mfma_f32_16x16x32_bf16 v[88:91], v[154:157], v[178:181], v[88:91]
	s_waitcnt lgkmcnt(0)
	v_mfma_f32_16x16x32_bf16 v[76:79], v[146:149], v[186:189], v[76:79]
	v_mfma_f32_16x16x32_bf16 v[72:75], v[154:157], v[186:189], v[72:75]
	s_setprio 0
	s_barrier
	ds_read_b128 v[192:195], v139
	ds_read_b128 v[196:199], v139 offset:1024
	ds_read_b128 v[200:203], v139 offset:2048
	ds_read_b128 v[204:207], v139 offset:3072
	s_mov_b32 m0, s13
	s_nop 0
	buffer_load_dwordx4 v130, s[44:47], s37 offen lds
	s_nop 0
	s_mov_b32 m0, s14
	s_nop 0
	buffer_load_dwordx4 v135, s[44:47], s37 offen lds
	s_waitcnt vmcnt(10)
	s_barrier
	s_waitcnt lgkmcnt(0)
	s_setprio 1
	s_waitcnt lgkmcnt(3)
	v_mfma_f32_16x16x32_bf16 v[116:119], v[192:195], v[158:161], v[116:119]
	s_waitcnt lgkmcnt(1)
	v_mfma_f32_16x16x32_bf16 v[112:115], v[200:203], v[158:161], v[112:115]
	v_mfma_f32_16x16x32_bf16 v[100:103], v[192:195], v[166:169], v[100:103]
	v_mfma_f32_16x16x32_bf16 v[96:99], v[200:203], v[166:169], v[96:99]
	v_mfma_f32_16x16x32_bf16 v[84:87], v[192:195], v[174:177], v[84:87]
	v_mfma_f32_16x16x32_bf16 v[80:83], v[200:203], v[174:177], v[80:83]
	v_mfma_f32_16x16x32_bf16 v[68:71], v[192:195], v[182:185], v[68:71]
	v_mfma_f32_16x16x32_bf16 v[64:67], v[200:203], v[182:185], v[64:67]
	v_mfma_f32_16x16x32_bf16 v[116:119], v[196:199], v[162:165], v[116:119]
	s_waitcnt lgkmcnt(0)
	v_mfma_f32_16x16x32_bf16 v[112:115], v[204:207], v[162:165], v[112:115]
	v_mfma_f32_16x16x32_bf16 v[100:103], v[196:199], v[170:173], v[100:103]
	v_mfma_f32_16x16x32_bf16 v[96:99], v[204:207], v[170:173], v[96:99]
	v_mfma_f32_16x16x32_bf16 v[84:87], v[196:199], v[178:181], v[84:87]
	v_mfma_f32_16x16x32_bf16 v[80:83], v[204:207], v[178:181], v[80:83]
	v_mfma_f32_16x16x32_bf16 v[68:71], v[196:199], v[186:189], v[68:71]
	v_mfma_f32_16x16x32_bf16 v[64:67], v[204:207], v[186:189], v[64:67]
	s_setprio 0
	s_barrier
	ds_read_b128 v[158:161], v138 offset:16400
	ds_read_b128 v[162:165], v138 offset:17424
	ds_read_b128 v[166:169], v138 offset:18448
	ds_read_b128 v[170:173], v138 offset:19472
	ds_read_b128 v[174:177], v138 offset:20496
	ds_read_b128 v[178:181], v138 offset:21520
	ds_read_b128 v[182:185], v138 offset:22544
	ds_read_b128 v[186:189], v138 offset:23568
	s_mov_b32 m0, s15
	s_nop 0
	buffer_load_dwordx4 v128, s[0:3], s37 offen lds
	s_nop 0
	s_mov_b32 m0, s16
	s_nop 0
	buffer_load_dwordx4 v133, s[0:3], s37 offen lds
	s_barrier
	s_waitcnt lgkmcnt(0)
	s_setprio 1
	s_waitcnt lgkmcnt(7)
	v_mfma_f32_16x16x32_bf16 v[60:63], v[142:145], v[158:161], v[60:63]
	v_mfma_f32_16x16x32_bf16 v[56:59], v[150:153], v[158:161], v[56:59]
	s_waitcnt lgkmcnt(5)
	v_mfma_f32_16x16x32_bf16 v[44:47], v[142:145], v[166:169], v[44:47]
	v_mfma_f32_16x16x32_bf16 v[40:43], v[150:153], v[166:169], v[40:43]
	s_waitcnt lgkmcnt(3)
	v_mfma_f32_16x16x32_bf16 v[28:31], v[142:145], v[174:177], v[28:31]
	v_mfma_f32_16x16x32_bf16 v[24:27], v[150:153], v[174:177], v[24:27]
	s_waitcnt lgkmcnt(1)
	v_mfma_f32_16x16x32_bf16 v[12:15], v[142:145], v[182:185], v[12:15]
	v_mfma_f32_16x16x32_bf16 v[8:11], v[150:153], v[182:185], v[8:11]
	v_mfma_f32_16x16x32_bf16 v[60:63], v[146:149], v[162:165], v[60:63]
	v_mfma_f32_16x16x32_bf16 v[56:59], v[154:157], v[162:165], v[56:59]
	v_mfma_f32_16x16x32_bf16 v[44:47], v[146:149], v[170:173], v[44:47]
	v_mfma_f32_16x16x32_bf16 v[40:43], v[154:157], v[170:173], v[40:43]
	v_mfma_f32_16x16x32_bf16 v[28:31], v[146:149], v[178:181], v[28:31]
	v_mfma_f32_16x16x32_bf16 v[24:27], v[154:157], v[178:181], v[24:27]
	s_waitcnt lgkmcnt(0)
	v_mfma_f32_16x16x32_bf16 v[12:15], v[146:149], v[186:189], v[12:15]
	v_mfma_f32_16x16x32_bf16 v[8:11], v[154:157], v[186:189], v[8:11]
	s_setprio 0
	s_barrier
; #define G_WAIT_V(n) asm volatile("s_waitcnt vmcnt(" #n ")" ::: "memory")
; #define G_BAR() __builtin_amdgcn_s_barrier()
; #define G_SCHED() __builtin_amdgcn_sched_barrier(0)
; #define D_STAGE_A(slot, half, kt) D_STAGE(rsA, voffA, slot, half, kt)
; #define D_STAGE_B(slot, half, kt) D_STAGE(rsB, voffB, slot, half, kt)
; #define D_LDA(dst, slot) do { _Pragma("unroll") for (int m = 0; m < 4; ++m) _Pragma("unroll") for (int k = 0; k < 2; ++k) \
;     dst[m][k] = *(const LDS_AS bf16x8*)(lds + (slot) + aoff + m * 2048 + k * 1024); } while (0)
; #define D_LDB(dst, slot) do { _Pragma("unroll") for (int n = 0; n < 2; ++n) _Pragma("unroll") for (int k = 0; k < 2; ++k) \
;     dst[n][k] = *(const LDS_AS bf16x8*)(lds + (slot) + boff + n * 2048 + k * 1024); } while (0)
; #define D_MMA(ai, bj, At, Bf) do { __builtin_amdgcn_s_setprio(1); _Pragma("unroll") for (int m = 0; m < 4; ++m) _Pragma("unroll") for (int n = 0; n < 2; ++n) _Pragma("unroll") for (int k = 0; k < 2; ++k) \
;     acc[ai][bj][m][n] = __builtin_amdgcn_mfma_f32_16x16x32_bf16(Bf[n][k], At[m][k], acc[ai][bj][m][n], 0, 0, 0); __builtin_amdgcn_s_setprio(0); } while (0)
; #define D_WAIT_L(n) asm volatile("s_waitcnt lgkmcnt(" #n ")" ::: "memory")
; #define D_STAGE_A(slot, half, kt) D_STAGE(rsA, voffA, slot, half, kt)
; #define D_STAGE_B(slot, half, kt) do { _Pragma("unroll") for (int _i = 0; _i < 2; ++_i) { const unsigned _m0 = ldsw + (unsigned)((slot) + _i * 8192); const unsigned _so = (unsigned)(kt) * 128u + (half) * bt_half + _i * bt_piece; \
;     asm volatile("s_mov_b32 m0, %0\n\ts_nop 4\n\tbuffer_load_dwordx4 %1, %2, %3 offen lds" :: "s"(_m0), "v"(voffB0), "s"(rsB), "s"(_so) : "m0", "memory"); } } while (0)
; #define D_WAIT_L(n) asm volatile("s_waitcnt lgkmcnt(" #n ")" ::: "memory")
; template <class Cfg>
; DI void gemm256dma_unit(LDS_AS unsigned char* lds, const Cfg& cfg) {
;     ...
;     D_STAGE_B(G_SB(0, 1), 1, t2);
;     G_WAIT_V(6); G_BAR(); G_SCHED(); D_MMA(1, 1, At, B1); G_BAR(); G_SCHED();
;     D_LDB(B0, G_SB(1, 0)); G_SCHED(); D_LDA(At, G_SA(1, 0)); D_STAGE_A(G_SA(0, 1), 1, t2);
;     D_WAIT_L(8); G_BAR(); D_WAIT_L(0); G_SCHED(); D_MMA(0, 0, At, B0); G_BAR(); G_SCHED();
;     D_LDB(B1, G_SB(1, 1)); D_STAGE_B(G_SB(1, 0), 0, t3);
;     G_BAR(); D_WAIT_L(0); G_SCHED(); D_MMA(0, 1, At, B1); G_BAR(); G_SCHED();
	s_mov_b32 m0, s17
	s_nop 0
	buffer_load_dwordx4 v131, s[44:47], s37 offen lds
	s_nop 0
	s_mov_b32 m0, s19
	s_nop 0
	buffer_load_dwordx4 v136, s[44:47], s37 offen lds
	s_waitcnt vmcnt(10)
	s_barrier
	s_setprio 1
	v_mfma_f32_16x16x32_bf16 v[52:55], v[192:195], v[158:161], v[52:55]
	v_mfma_f32_16x16x32_bf16 v[48:51], v[200:203], v[158:161], v[48:51]
	v_mfma_f32_16x16x32_bf16 v[36:39], v[192:195], v[166:169], v[36:39]
	v_mfma_f32_16x16x32_bf16 v[32:35], v[200:203], v[166:169], v[32:35]
	v_mfma_f32_16x16x32_bf16 v[20:23], v[192:195], v[174:177], v[20:23]
	v_mfma_f32_16x16x32_bf16 v[16:19], v[200:203], v[174:177], v[16:19]
	v_mfma_f32_16x16x32_bf16 v[4:7], v[192:195], v[182:185], v[4:7]
	v_mfma_f32_16x16x32_bf16 v[0:3], v[200:203], v[182:185], v[0:3]
	v_mfma_f32_16x16x32_bf16 v[52:55], v[196:199], v[162:165], v[52:55]
	v_mfma_f32_16x16x32_bf16 v[48:51], v[204:207], v[162:165], v[48:51]
	v_mfma_f32_16x16x32_bf16 v[36:39], v[196:199], v[170:173], v[36:39]
	v_mfma_f32_16x16x32_bf16 v[32:35], v[204:207], v[170:173], v[32:35]
	v_mfma_f32_16x16x32_bf16 v[20:23], v[196:199], v[178:181], v[20:23]
	v_mfma_f32_16x16x32_bf16 v[16:19], v[204:207], v[178:181], v[16:19]
	v_mfma_f32_16x16x32_bf16 v[4:7], v[196:199], v[186:189], v[4:7]
	v_mfma_f32_16x16x32_bf16 v[0:3], v[204:207], v[186:189], v[0:3]
	s_setprio 0
	s_barrier
	ds_read_b128 v[142:145], v140
	ds_read_b128 v[146:149], v140 offset:1024
	ds_read_b128 v[150:153], v140 offset:2048
	ds_read_b128 v[154:157], v140 offset:3072
	ds_read_b128 v[158:161], v138 offset:32784
	ds_read_b128 v[162:165], v138 offset:33808
	ds_read_b128 v[166:169], v138 offset:34832
	ds_read_b128 v[170:173], v138 offset:35856
	ds_read_b128 v[174:177], v138 offset:36880
	ds_read_b128 v[178:181], v138 offset:37904
	ds_read_b128 v[182:185], v138 offset:38928
	ds_read_b128 v[186:189], v138 offset:39952
	s_mov_b32 m0, s20
	s_nop 0
	buffer_load_dwordx4 v129, s[0:3], s37 offen lds
	s_nop 0
	s_mov_b32 m0, s22
	s_nop 0
	buffer_load_dwordx4 v134, s[0:3], s37 offen lds
	s_waitcnt lgkmcnt(8)
	s_waitcnt vmcnt(10)
	s_barrier
	s_waitcnt lgkmcnt(0)
	s_setprio 1
	s_waitcnt lgkmcnt(7)
	v_mfma_f32_16x16x32_bf16 v[124:127], v[142:145], v[158:161], v[124:127]
	v_mfma_f32_16x16x32_bf16 v[120:123], v[150:153], v[158:161], v[120:123]
	s_waitcnt lgkmcnt(5)
	v_mfma_f32_16x16x32_bf16 v[108:111], v[142:145], v[166:169], v[108:111]
	v_mfma_f32_16x16x32_bf16 v[104:107], v[150:153], v[166:169], v[104:107]
	s_waitcnt lgkmcnt(3)
	v_mfma_f32_16x16x32_bf16 v[92:95], v[142:145], v[174:177], v[92:95]
	v_mfma_f32_16x16x32_bf16 v[88:91], v[150:153], v[174:177], v[88:91]
	s_waitcnt lgkmcnt(1)
	v_mfma_f32_16x16x32_bf16 v[76:79], v[142:145], v[182:185], v[76:79]
	v_mfma_f32_16x16x32_bf16 v[72:75], v[150:153], v[182:185], v[72:75]
	v_mfma_f32_16x16x32_bf16 v[124:127], v[146:149], v[162:165], v[124:127]
	v_mfma_f32_16x16x32_bf16 v[120:123], v[154:157], v[162:165], v[120:123]
	v_mfma_f32_16x16x32_bf16 v[108:111], v[146:149], v[170:173], v[108:111]
	v_mfma_f32_16x16x32_bf16 v[104:107], v[154:157], v[170:173], v[104:107]
	v_mfma_f32_16x16x32_bf16 v[92:95], v[146:149], v[178:181], v[92:95]
	v_mfma_f32_16x16x32_bf16 v[88:91], v[154:157], v[178:181], v[88:91]
	s_waitcnt lgkmcnt(0)
	v_mfma_f32_16x16x32_bf16 v[76:79], v[146:149], v[186:189], v[76:79]
	v_mfma_f32_16x16x32_bf16 v[72:75], v[154:157], v[186:189], v[72:75]
	s_setprio 0
	s_barrier
	ds_read_b128 v[192:195], v141
	ds_read_b128 v[196:199], v141 offset:1024
	ds_read_b128 v[200:203], v141 offset:2048
	ds_read_b128 v[204:207], v141 offset:3072
	s_mov_b32 m0, s23
	s_nop 0
	buffer_load_dwordx4 v130, s[44:47], s35 offen lds
	s_nop 0
	s_mov_b32 m0, s24
	s_nop 0
	buffer_load_dwordx4 v135, s[44:47], s35 offen lds
	s_waitcnt vmcnt(10)
	s_barrier
; #define G_WAIT_V(n) asm volatile("s_waitcnt vmcnt(" #n ")" ::: "memory")
; #define G_BAR() __builtin_amdgcn_s_barrier()
; #define G_SCHED() __builtin_amdgcn_sched_barrier(0)
; #define D_STAGE_A(slot, half, kt) D_STAGE(rsA, voffA, slot, half, kt)
; #define D_STAGE_B(slot, half, kt) D_STAGE(rsB, voffB, slot, half, kt)
; #define D_LDA(dst, slot) do { _Pragma("unroll") for (int m = 0; m < 4; ++m) _Pragma("unroll") for (int k = 0; k < 2; ++k) \
;     dst[m][k] = *(const LDS_AS bf16x8*)(lds + (slot) + aoff + m * 2048 + k * 1024); } while (0)
; #define D_MMA(ai, bj, At, Bf) do { __builtin_amdgcn_s_setprio(1); _Pragma("unroll") for (int m = 0; m < 4; ++m) _Pragma("unroll") for (int n = 0; n < 2; ++n) _Pragma("unroll") for (int k = 0; k < 2; ++k) \
;     acc[ai][bj][m][n] = __builtin_amdgcn_mfma_f32_16x16x32_bf16(Bf[n][k], At[m][k], acc[ai][bj][m][n], 0, 0, 0); __builtin_amdgcn_s_setprio(0); } while (0)
; #define D_WAIT_L(n) asm volatile("s_waitcnt lgkmcnt(" #n ")" ::: "memory")
; #define D_STAGE_A(slot, half, kt) D_STAGE(rsA, voffA, slot, half, kt)
; #define D_STAGE_B(slot, half, kt) do { _Pragma("unroll") for (int _i = 0; _i < 2; ++_i) { const unsigned _m0 = ldsw + (unsigned)((slot) + _i * 8192); const unsigned _so = (unsigned)(kt) * 128u + (half) * bt_half + _i * bt_piece; \
;     asm volatile("s_mov_b32 m0, %0\n\ts_nop 4\n\tbuffer_load_dwordx4 %1, %2, %3 offen lds" :: "s"(_m0), "v"(voffB0), "s"(rsB), "s"(_so) : "m0", "memory"); } } while (0)
; #define D_WAIT_L(n) asm volatile("s_waitcnt lgkmcnt(" #n ")" ::: "memory")
; #define DENSE_UNIT(lds, cfg) gemm256dma_unit(lds, cfg)
; #define DENSE_UNIT(lds, cfg) gemm256_unit(lds, cfg)
; template <class Cfg>
; DI void gemm256dma_unit(LDS_AS unsigned char* lds, const Cfg& cfg) {
;     ...
;     D_LDA(At, G_SA(1, 1)); D_STAGE_A(G_SA(1, 0), 0, t3);
;     G_BAR(); D_WAIT_L(0); G_SCHED(); D_MMA(1, 0, At, B0); G_BAR(); G_SCHED();
;     D_STAGE_B(G_SB(1, 1), 1, t3);
;     G_WAIT_V(6); G_BAR(); G_SCHED(); D_MMA(1, 1, At, B1); G_BAR(); G_SCHED();
;   }
;   G_WAIT_V(0);
;   if (wr == 0) G_BAR();
;   for (int u = bid; u < 32 * 8; u += nb) {
;     const int uu = __builtin_amdgcn_readfirstlane(u);
;     CfgWo cfg{p, uu >> 3, uu & 7};
;     if (MODE == 0) DENSE_UNIT(lds, cfg); else gemm256_unit<CfgWo, MODE>(lds, cfg);
	s_waitcnt lgkmcnt(0)
	s_setprio 1
	s_waitcnt lgkmcnt(3)
	v_mfma_f32_16x16x32_bf16 v[116:119], v[192:195], v[158:161], v[116:119]
	s_waitcnt lgkmcnt(1)
	v_mfma_f32_16x16x32_bf16 v[112:115], v[200:203], v[158:161], v[112:115]
	v_mfma_f32_16x16x32_bf16 v[100:103], v[192:195], v[166:169], v[100:103]
	v_mfma_f32_16x16x32_bf16 v[96:99], v[200:203], v[166:169], v[96:99]
	v_mfma_f32_16x16x32_bf16 v[84:87], v[192:195], v[174:177], v[84:87]
	v_mfma_f32_16x16x32_bf16 v[80:83], v[200:203], v[174:177], v[80:83]
	v_mfma_f32_16x16x32_bf16 v[68:71], v[192:195], v[182:185], v[68:71]
	v_mfma_f32_16x16x32_bf16 v[64:67], v[200:203], v[182:185], v[64:67]
	v_mfma_f32_16x16x32_bf16 v[116:119], v[196:199], v[162:165], v[116:119]
	s_waitcnt lgkmcnt(0)
	v_mfma_f32_16x16x32_bf16 v[112:115], v[204:207], v[162:165], v[112:115]
	v_mfma_f32_16x16x32_bf16 v[100:103], v[196:199], v[170:173], v[100:103]
	v_mfma_f32_16x16x32_bf16 v[96:99], v[204:207], v[170:173], v[96:99]
	v_mfma_f32_16x16x32_bf16 v[84:87], v[196:199], v[178:181], v[84:87]
	v_mfma_f32_16x16x32_bf16 v[80:83], v[204:207], v[178:181], v[80:83]
	v_mfma_f32_16x16x32_bf16 v[68:71], v[196:199], v[186:189], v[68:71]
	v_mfma_f32_16x16x32_bf16 v[64:67], v[204:207], v[186:189], v[64:67]
	s_setprio 0
	s_barrier
	ds_read_b128 v[158:161], v138 offset:49168
	ds_read_b128 v[162:165], v138 offset:50192
	ds_read_b128 v[166:169], v138 offset:51216
	ds_read_b128 v[170:173], v138 offset:52240
	ds_read_b128 v[174:177], v138 offset:53264
	ds_read_b128 v[178:181], v138 offset:54288
	ds_read_b128 v[182:185], v138 offset:55312
	ds_read_b128 v[186:189], v138 offset:56336
	s_mov_b32 m0, s25
	s_nop 0
	buffer_load_dwordx4 v128, s[0:3], s35 offen lds
	s_nop 0
	s_mov_b32 m0, s26
	s_nop 0
	buffer_load_dwordx4 v133, s[0:3], s35 offen lds
	s_barrier
	s_waitcnt lgkmcnt(0)
	s_setprio 1
	s_waitcnt lgkmcnt(7)
	v_mfma_f32_16x16x32_bf16 v[60:63], v[142:145], v[158:161], v[60:63]
	v_mfma_f32_16x16x32_bf16 v[56:59], v[150:153], v[158:161], v[56:59]
	s_waitcnt lgkmcnt(5)
	v_mfma_f32_16x16x32_bf16 v[44:47], v[142:145], v[166:169], v[44:47]
	v_mfma_f32_16x16x32_bf16 v[40:43], v[150:153], v[166:169], v[40:43]
	s_waitcnt lgkmcnt(3)
	v_mfma_f32_16x16x32_bf16 v[28:31], v[142:145], v[174:177], v[28:31]
	v_mfma_f32_16x16x32_bf16 v[24:27], v[150:153], v[174:177], v[24:27]
	s_waitcnt lgkmcnt(1)
	v_mfma_f32_16x16x32_bf16 v[12:15], v[142:145], v[182:185], v[12:15]
	v_mfma_f32_16x16x32_bf16 v[8:11], v[150:153], v[182:185], v[8:11]
	v_mfma_f32_16x16x32_bf16 v[60:63], v[146:149], v[162:165], v[60:63]
	v_mfma_f32_16x16x32_bf16 v[56:59], v[154:157], v[162:165], v[56:59]
	v_mfma_f32_16x16x32_bf16 v[44:47], v[146:149], v[170:173], v[44:47]
	v_mfma_f32_16x16x32_bf16 v[40:43], v[154:157], v[170:173], v[40:43]
	v_mfma_f32_16x16x32_bf16 v[28:31], v[146:149], v[178:181], v[28:31]
	v_mfma_f32_16x16x32_bf16 v[24:27], v[154:157], v[178:181], v[24:27]
	s_waitcnt lgkmcnt(0)
	v_mfma_f32_16x16x32_bf16 v[12:15], v[146:149], v[186:189], v[12:15]
	v_mfma_f32_16x16x32_bf16 v[8:11], v[154:157], v[186:189], v[8:11]
	s_setprio 0
	s_barrier
	s_mov_b32 m0, s27
	s_nop 0
	buffer_load_dwordx4 v131, s[44:47], s35 offen lds
	s_nop 0
	s_mov_b32 m0, s28
	s_nop 0
	buffer_load_dwordx4 v136, s[44:47], s35 offen lds
	s_waitcnt vmcnt(10)
	s_barrier
	s_setprio 1
	v_mfma_f32_16x16x32_bf16 v[52:55], v[192:195], v[158:161], v[52:55]
	v_mfma_f32_16x16x32_bf16 v[48:51], v[200:203], v[158:161], v[48:51]
	v_mfma_f32_16x16x32_bf16 v[36:39], v[192:195], v[166:169], v[36:39]
	v_mfma_f32_16x16x32_bf16 v[32:35], v[200:203], v[166:169], v[32:35]
	v_mfma_f32_16x16x32_bf16 v[20:23], v[192:195], v[174:177], v[20:23]
	v_mfma_f32_16x16x32_bf16 v[16:19], v[200:203], v[174:177], v[16:19]
	v_mfma_f32_16x16x32_bf16 v[4:7], v[192:195], v[182:185], v[4:7]
	v_mfma_f32_16x16x32_bf16 v[0:3], v[200:203], v[182:185], v[0:3]
	v_mfma_f32_16x16x32_bf16 v[52:55], v[196:199], v[162:165], v[52:55]
	v_mfma_f32_16x16x32_bf16 v[48:51], v[204:207], v[162:165], v[48:51]
	v_mfma_f32_16x16x32_bf16 v[36:39], v[196:199], v[170:173], v[36:39]
	v_mfma_f32_16x16x32_bf16 v[32:35], v[204:207], v[170:173], v[32:35]
	v_mfma_f32_16x16x32_bf16 v[20:23], v[196:199], v[178:181], v[20:23]
	v_mfma_f32_16x16x32_bf16 v[16:19], v[204:207], v[178:181], v[16:19]
	v_mfma_f32_16x16x32_bf16 v[4:7], v[196:199], v[186:189], v[4:7]
	v_mfma_f32_16x16x32_bf16 v[0:3], v[204:207], v[186:189], v[0:3]
	s_setprio 0
	s_barrier
	s_mov_b32 s33, s34
	s_cbranch_scc0 .LBB0_1266
	s_waitcnt vmcnt(0)
	s_cmpk_lt_u32 s12, 0x100
	s_cbranch_scc0 .LBB0_1262
	s_barrier
	s_branch .LBB0_1262

; #define G_WAIT_V(n) asm volatile("s_waitcnt vmcnt(" #n ")" ::: "memory")
; #define G_BAR() __builtin_amdgcn_s_barrier()
; #define G_SCHED() __builtin_amdgcn_sched_barrier(0)
; #define D_STAGE_A(slot, half, kt) D_STAGE(rsA, voffA, slot, half, kt)
; #define D_STAGE_B(slot, half, kt) D_STAGE(rsB, voffB, slot, half, kt)
; #define D_LDA(dst, slot) do { _Pragma("unroll") for (int m = 0; m < 4; ++m) _Pragma("unroll") for (int k = 0; k < 2; ++k) \
;     dst[m][k] = *(const LDS_AS bf16x8*)(lds + (slot) + aoff + m * 2048 + k * 1024); } while (0)
; #define D_LDB(dst, slot) do { _Pragma("unroll") for (int n = 0; n < 2; ++n) _Pragma("unroll") for (int k = 0; k < 2; ++k) \
;     dst[n][k] = *(const LDS_AS bf16x8*)(lds + (slot) + boff + n * 2048 + k * 1024); } while (0)
; #define D_MMA(ai, bj, At, Bf) do { __builtin_amdgcn_s_setprio(1); _Pragma("unroll") for (int m = 0; m < 4; ++m) _Pragma("unroll") for (int n = 0; n < 2; ++n) _Pragma("unroll") for (int k = 0; k < 2; ++k) \
;     acc[ai][bj][m][n] = __builtin_amdgcn_mfma_f32_16x16x32_bf16(Bf[n][k], At[m][k], acc[ai][bj][m][n], 0, 0, 0); __builtin_amdgcn_s_setprio(0); } while (0)
; #define D_WAIT_L(n) asm volatile("s_waitcnt lgkmcnt(" #n ")" ::: "memory")
; #define D_STAGE_A(slot, half, kt) D_STAGE(rsA, voffA, slot, half, kt)
; #define D_WAIT_L(n) asm volatile("s_waitcnt lgkmcnt(" #n ")" ::: "memory")
;     ...
;   for (int t = 0; t < (F8_PEEL ? nt - 2 : nt); t += 2) {
;     const int t1 = t + 1;
;     const int t2 = (F8_PEEL || t + 2 < nt) ? t + 2 : t;
;     const int t3 = (F8_PEEL || t + 2 < nt) ? t + 3 : t + 1;
;     D_LDB(B0, G_SB(0, 0)); G_SCHED(); D_LDA(At, G_SA(0, 0)); D_STAGE_A(G_SA(1, 1), 1, t1);
;     D_WAIT_L(8); G_BAR(); D_WAIT_L(0); G_SCHED(); D_MMA(0, 0, At, B0); G_BAR(); G_SCHED();
;     D_LDB(B1, G_SB(0, 1)); D_STAGE_B(G_SB(0, 0), 0, t2);
;     G_BAR(); D_WAIT_L(0); G_SCHED(); D_MMA(0, 1, At, B1); G_BAR(); G_SCHED();
;     D_LDA(At, G_SA(0, 1)); D_STAGE_A(G_SA(0, 0), 0, t2);
;     G_BAR(); D_WAIT_L(0); G_SCHED(); D_MMA(1, 0, At, B0); G_BAR(); G_SCHED();
;     D_STAGE_B(G_SB(0, 1), 1, t2);
;     G_WAIT_V(6); G_BAR(); G_SCHED(); D_MMA(1, 1, At, B1); G_BAR(); G_SCHED();
.LBB0_1415:
	s_add_i32 s82, 0, 0x10010
	v_add_u32_e32 v72, s82, v125
	v_add_u32_e32 v73, s82, v126
	ds_read_b128 v[152:155], v72
	ds_read_b128 v[160:163], v72 offset:2048
	ds_read_b128 v[156:159], v73
	ds_read_b128 v[164:167], v73 offset:2048
	s_add_i32 s38, s79, 1
	s_add_i32 s80, s79, 3
	s_add_i32 s78, s79, 2
	s_add_i32 s96, 0, 0x14010
	s_cmp_lt_u32 s79, 14
	s_cselect_b32 s81, s78, s79
	s_cselect_b32 s38, s80, s38
	s_lshl_b32 s86, s81, 7
	s_lshl_b32 s81, s38, 7
	s_add_i32 s97, s86, 0x20000
	s_add_i32 s91, s86, 0x2000
	s_add_i32 s90, s86, 0x22000
	s_add_i32 s87, 0, 0x18010
	s_add_i32 s85, 0, 0x1c010
	s_add_i32 s84, s81, 0x20000
	s_add_i32 s83, s81, 0x2000
	s_add_i32 s82, s81, 0x22000
	s_add_i32 s80, s77, 0x100
	s_cmp_gt_u32 s79, 13
	ds_read_b128 v[168:171], v127 offset:16
	ds_read_b128 v[176:179], v127 offset:2064
	ds_read_b128 v[172:175], v128 offset:16
	ds_read_b128 v[180:183], v128 offset:2064
	ds_read_b128 v[192:195], v127 offset:4112
	ds_read_b128 v[200:203], v127 offset:6160
	ds_read_b128 v[196:199], v128 offset:4112
	ds_read_b128 v[204:207], v128 offset:6160
	s_mov_b32 m0, s75
	s_nop 0
	buffer_load_dwordx4 v121, s[8:11], s77 offen lds
	s_nop 0
	s_mov_b32 m0, s76
	s_nop 0
	buffer_load_dwordx4 v124, s[8:11], s77 offen lds
	s_waitcnt lgkmcnt(8)
	s_waitcnt vmcnt(10)
	s_barrier
	s_waitcnt lgkmcnt(0)
	s_setprio 1
	s_waitcnt lgkmcnt(5)
	v_mfma_scale_f32_16x16x128_f8f6f4 v[134:137], v[160:167], v[168:175], v[136:139], v149, v148 op_sel_hi:[0,0,0]
	s_waitcnt lgkmcnt(0)
	v_mfma_scale_f32_16x16x128_f8f6f4 v[212:215], v[152:159], v[200:207], v[212:215], v149, v148 op_sel_hi:[0,0,0]
	v_mfma_scale_f32_16x16x128_f8f6f4 v[216:219], v[160:167], v[200:207], v[216:219], v149, v148 op_sel_hi:[0,0,0]
	v_mfma_scale_f32_16x16x128_f8f6f4 v[130:133], v[152:159], v[168:175], v[140:143], v149, v148 op_sel_hi:[0,0,0]
	v_mfma_scale_f32_16x16x128_f8f6f4 v[144:147], v[152:159], v[176:183], v[108:111], v149, v148 op_sel_hi:[0,0,0]
	v_mfma_scale_f32_16x16x128_f8f6f4 v[184:187], v[160:167], v[176:183], v[104:107], v149, v148 op_sel_hi:[0,0,0]
	v_mfma_scale_f32_16x16x128_f8f6f4 v[188:191], v[152:159], v[192:199], v[92:95], v149, v148 op_sel_hi:[0,0,0]
	v_mfma_scale_f32_16x16x128_f8f6f4 v[208:211], v[160:167], v[192:199], v[88:91], v149, v148 op_sel_hi:[0,0,0]
	s_setprio 0
	s_barrier
	v_add_u32_e32 v76, s96, v125
	v_add_u32_e32 v80, s96, v126
	ds_read_b128 v[72:75], v76
	s_nop 1
	ds_read_b128 v[88:91], v76 offset:2048
	ds_read_b128 v[76:79], v80
	ds_read_b128 v[92:95], v80 offset:2048
	s_mov_b32 m0, s23
	s_nop 0
	buffer_load_dwordx4 v122, s[4:7], s86 offen lds
	s_nop 0
	s_mov_b32 m0, s39
	s_nop 0
	buffer_load_dwordx4 v122, s[4:7], s97 offen lds
	s_waitcnt vmcnt(10)
	s_barrier
	s_waitcnt lgkmcnt(0)
	s_setprio 1
	s_waitcnt lgkmcnt(1)
	v_mfma_scale_f32_16x16x128_f8f6f4 v[68:71], v[72:79], v[200:207], v[68:71], v149, v148 op_sel_hi:[0,0,0]
	s_waitcnt lgkmcnt(0)
	v_mfma_scale_f32_16x16x128_f8f6f4 v[56:59], v[88:95], v[200:207], v[56:59], v149, v148 op_sel_hi:[0,0,0]
	v_mfma_scale_f32_16x16x128_f8f6f4 v[220:223], v[72:79], v[168:175], v[116:119], v149, v148 op_sel_hi:[0,0,0]
	v_mfma_scale_f32_16x16x128_f8f6f4 v[168:171], v[88:95], v[168:175], v[112:115], v149, v148 op_sel_hi:[0,0,0]
	v_mfma_scale_f32_16x16x128_f8f6f4 v[172:175], v[72:79], v[176:183], v[100:103], v149, v148 op_sel_hi:[0,0,0]
	v_mfma_scale_f32_16x16x128_f8f6f4 v[176:179], v[88:95], v[176:183], v[96:99], v149, v148 op_sel_hi:[0,0,0]
	v_mfma_scale_f32_16x16x128_f8f6f4 v[180:183], v[72:79], v[192:199], v[84:87], v149, v148 op_sel_hi:[0,0,0]
	v_mfma_scale_f32_16x16x128_f8f6f4 v[192:195], v[88:95], v[192:199], v[8:11], v149, v148 op_sel_hi:[0,0,0]
	s_setprio 0
	s_barrier
	ds_read_b128 v[80:83], v127 offset:16400
	s_nop 1
	ds_read_b128 v[96:99], v127 offset:18448
	ds_read_b128 v[84:87], v128 offset:16400
	ds_read_b128 v[100:103], v128 offset:18448
	ds_read_b128 v[104:107], v127 offset:20496
	ds_read_b128 v[112:115], v127 offset:22544
	ds_read_b128 v[108:111], v128 offset:20496
	ds_read_b128 v[116:119], v128 offset:22544
	s_mov_b32 m0, s61
	s_nop 0
	buffer_load_dwordx4 v120, s[8:11], s86 offen lds
	s_nop 0
	s_mov_b32 m0, s62
	s_nop 0
	buffer_load_dwordx4 v123, s[8:11], s86 offen lds
	s_barrier
	s_waitcnt lgkmcnt(0)
	s_setprio 1
	s_waitcnt lgkmcnt(5)
	v_mfma_scale_f32_16x16x128_f8f6f4 v[64:67], v[152:159], v[80:87], v[64:67], v149, v148 op_sel_hi:[0,0,0]
	v_mfma_scale_f32_16x16x128_f8f6f4 v[60:63], v[160:167], v[80:87], v[60:63], v149, v148 op_sel_hi:[0,0,0]
	s_waitcnt lgkmcnt(0)
	v_mfma_scale_f32_16x16x128_f8f6f4 v[236:239], v[160:167], v[112:119], v[236:239], v149, v148 op_sel_hi:[0,0,0]
	v_mfma_scale_f32_16x16x128_f8f6f4 v[200:203], v[152:159], v[96:103], v[44:47], v149, v148 op_sel_hi:[0,0,0]
	v_mfma_scale_f32_16x16x128_f8f6f4 v[204:207], v[160:167], v[96:103], v[40:43], v149, v148 op_sel_hi:[0,0,0]
	v_mfma_scale_f32_16x16x128_f8f6f4 v[224:227], v[152:159], v[104:111], v[28:31], v149, v148 op_sel_hi:[0,0,0]
	v_mfma_scale_f32_16x16x128_f8f6f4 v[228:231], v[160:167], v[104:111], v[24:27], v149, v148 op_sel_hi:[0,0,0]
	v_mfma_scale_f32_16x16x128_f8f6f4 v[232:235], v[152:159], v[112:119], v[12:15], v149, v148 op_sel_hi:[0,0,0]
	s_setprio 0
	s_barrier
	s_mov_b32 m0, s63
	s_nop 0
	buffer_load_dwordx4 v122, s[4:7], s91 offen lds
	s_nop 0
	s_mov_b32 m0, s66
	s_nop 0
	buffer_load_dwordx4 v122, s[4:7], s90 offen lds
	s_waitcnt vmcnt(10)
	s_barrier
; #define G_WAIT_V(n) asm volatile("s_waitcnt vmcnt(" #n ")" ::: "memory")
; #define G_BAR() __builtin_amdgcn_s_barrier()
; #define G_SCHED() __builtin_amdgcn_sched_barrier(0)
; #define D_STAGE_A(slot, half, kt) D_STAGE(rsA, voffA, slot, half, kt)
; #define D_STAGE_B(slot, half, kt) D_STAGE(rsB, voffB, slot, half, kt)
; #define D_LDA(dst, slot) do { _Pragma("unroll") for (int m = 0; m < 4; ++m) _Pragma("unroll") for (int k = 0; k < 2; ++k) \
;     dst[m][k] = *(const LDS_AS bf16x8*)(lds + (slot) + aoff + m * 2048 + k * 1024); } while (0)
; #define D_LDB(dst, slot) do { _Pragma("unroll") for (int n = 0; n < 2; ++n) _Pragma("unroll") for (int k = 0; k < 2; ++k) \
;     dst[n][k] = *(const LDS_AS bf16x8*)(lds + (slot) + boff + n * 2048 + k * 1024); } while (0)
; #define D_MMA(ai, bj, At, Bf) do { __builtin_amdgcn_s_setprio(1); _Pragma("unroll") for (int m = 0; m < 4; ++m) _Pragma("unroll") for (int n = 0; n < 2; ++n) _Pragma("unroll") for (int k = 0; k < 2; ++k) \
;     acc[ai][bj][m][n] = __builtin_amdgcn_mfma_f32_16x16x32_bf16(Bf[n][k], At[m][k], acc[ai][bj][m][n], 0, 0, 0); __builtin_amdgcn_s_setprio(0); } while (0)
; #define D_WAIT_L(n) asm volatile("s_waitcnt lgkmcnt(" #n ")" ::: "memory")
; #define D_STAGE_A(slot, half, kt) D_STAGE(rsA, voffA, slot, half, kt)
; #define D_STAGE_B(slot, half, kt) do { _Pragma("unroll") for (int _i = 0; _i < 2; ++_i) { const unsigned _m0 = ldsw + (unsigned)((slot) + _i * 8192); const unsigned _so = (unsigned)(kt) * 128u + (half) * bt_half + _i * bt_piece; \
;     asm volatile("s_mov_b32 m0, %0\n\ts_nop 4\n\tbuffer_load_dwordx4 %1, %2, %3 offen lds" :: "s"(_m0), "v"(voffB0), "s"(rsB), "s"(_so) : "m0", "memory"); } } while (0)
; #define D_WAIT_L(n) asm volatile("s_waitcnt lgkmcnt(" #n ")" ::: "memory")
;     ...
;     D_LDB(B0, G_SB(1, 0)); G_SCHED(); D_LDA(At, G_SA(1, 0)); D_STAGE_A(G_SA(0, 1), 1, t2);
;     D_WAIT_L(8); G_BAR(); D_WAIT_L(0); G_SCHED(); D_MMA(0, 0, At, B0); G_BAR(); G_SCHED();
;     D_LDB(B1, G_SB(1, 1)); D_STAGE_B(G_SB(1, 0), 0, t3);
;     G_BAR(); D_WAIT_L(0); G_SCHED(); D_MMA(0, 1, At, B1); G_BAR(); G_SCHED();
;     D_LDA(At, G_SA(1, 1)); D_STAGE_A(G_SA(1, 0), 0, t3);
;     G_BAR(); D_WAIT_L(0); G_SCHED(); D_MMA(1, 0, At, B0); G_BAR(); G_SCHED();
;     D_STAGE_B(G_SB(1, 1), 1, t3);
;     G_WAIT_V(6); G_BAR(); G_SCHED(); D_MMA(1, 1, At, B1); G_BAR(); G_SCHED();
;   }
	s_setprio 1
	v_mfma_scale_f32_16x16x128_f8f6f4 v[52:55], v[72:79], v[80:87], v[52:55], v149, v148 op_sel_hi:[0,0,0]
	v_mfma_scale_f32_16x16x128_f8f6f4 v[48:51], v[88:95], v[80:87], v[48:51], v149, v148 op_sel_hi:[0,0,0]
	v_mfma_scale_f32_16x16x128_f8f6f4 v[240:243], v[72:79], v[96:103], v[36:39], v149, v148 op_sel_hi:[0,0,0]
	v_mfma_scale_f32_16x16x128_f8f6f4 v[244:247], v[88:95], v[96:103], v[32:35], v149, v148 op_sel_hi:[0,0,0]
	v_mfma_scale_f32_16x16x128_f8f6f4 v[248:251], v[72:79], v[104:111], v[20:23], v149, v148 op_sel_hi:[0,0,0]
	v_mfma_scale_f32_16x16x128_f8f6f4 v[80:83], v[88:95], v[104:111], v[16:19], v149, v148 op_sel_hi:[0,0,0]
	v_mfma_scale_f32_16x16x128_f8f6f4 v[72:75], v[72:79], v[112:119], v[4:7], v149, v148 op_sel_hi:[0,0,0]
	v_mfma_scale_f32_16x16x128_f8f6f4 v[76:79], v[88:95], v[112:119], v[0:3], v149, v148 op_sel_hi:[0,0,0]
	s_setprio 0
	s_barrier
	s_nop 3
	v_add_u32_e32 v4, s87, v125
	v_add_u32_e32 v8, s87, v126
	ds_read_b128 v[0:3], v4
	ds_read_b128 v[16:19], v4 offset:2048
	ds_read_b128 v[4:7], v8
	ds_read_b128 v[20:23], v8 offset:2048
	ds_read_b128 v[8:11], v127 offset:32784
	ds_read_b128 v[24:27], v127 offset:34832
	ds_read_b128 v[12:15], v128 offset:32784
	ds_read_b128 v[28:31], v128 offset:34832
	ds_read_b128 v[32:35], v127 offset:36880
	ds_read_b128 v[40:43], v127 offset:38928
	ds_read_b128 v[36:39], v128 offset:36880
	ds_read_b128 v[44:47], v128 offset:38928
	s_mov_b32 m0, s67
	s_nop 0
	buffer_load_dwordx4 v121, s[8:11], s86 offen lds
	s_nop 0
	s_mov_b32 m0, s68
	s_nop 0
	buffer_load_dwordx4 v124, s[8:11], s86 offen lds
	s_waitcnt lgkmcnt(8)
	s_waitcnt vmcnt(10)
	s_barrier
	s_waitcnt lgkmcnt(0)
	s_setprio 1
	s_waitcnt lgkmcnt(5)
	v_mfma_scale_f32_16x16x128_f8f6f4 v[140:143], v[0:7], v[8:15], v[130:133], v149, v148 op_sel_hi:[0,0,0]
	v_mfma_scale_f32_16x16x128_f8f6f4 v[136:139], v[16:23], v[8:15], v[134:137], v149, v148 op_sel_hi:[0,0,0]
	s_waitcnt lgkmcnt(4)
	v_mfma_scale_f32_16x16x128_f8f6f4 v[108:111], v[0:7], v[24:31], v[144:147], v149, v148 op_sel_hi:[0,0,0]
	v_mfma_scale_f32_16x16x128_f8f6f4 v[104:107], v[16:23], v[24:31], v[184:187], v149, v148 op_sel_hi:[0,0,0]
	s_waitcnt lgkmcnt(1)
	v_mfma_scale_f32_16x16x128_f8f6f4 v[92:95], v[0:7], v[32:39], v[188:191], v149, v148 op_sel_hi:[0,0,0]
	v_mfma_scale_f32_16x16x128_f8f6f4 v[88:91], v[16:23], v[32:39], v[208:211], v149, v148 op_sel_hi:[0,0,0]
	s_waitcnt lgkmcnt(0)
	v_mfma_scale_f32_16x16x128_f8f6f4 v[212:215], v[0:7], v[40:47], v[212:215], v149, v148 op_sel_hi:[0,0,0]
	v_mfma_scale_f32_16x16x128_f8f6f4 v[216:219], v[16:23], v[40:47], v[216:219], v149, v148 op_sel_hi:[0,0,0]
	s_setprio 0
	s_barrier
	v_add_u32_e32 v84, s85, v125
	v_add_u32_e32 v85, s85, v126
	ds_read_b128 v[152:155], v84
	ds_read_b128 v[160:163], v84 offset:2048
	ds_read_b128 v[156:159], v85
	ds_read_b128 v[164:167], v85 offset:2048
	s_mov_b32 m0, s69
	s_nop 0
	buffer_load_dwordx4 v122, s[4:7], s81 offen lds
	s_nop 0
	s_mov_b32 m0, s70
	s_nop 0
	buffer_load_dwordx4 v122, s[4:7], s84 offen lds
	s_waitcnt vmcnt(10)
	s_barrier
	s_waitcnt lgkmcnt(0)
	s_setprio 1
	s_waitcnt lgkmcnt(1)
	v_mfma_scale_f32_16x16x128_f8f6f4 v[116:119], v[152:159], v[8:15], v[220:223], v149, v148 op_sel_hi:[0,0,0]
	s_waitcnt lgkmcnt(0)
	v_mfma_scale_f32_16x16x128_f8f6f4 v[112:115], v[160:167], v[8:15], v[168:171], v149, v148 op_sel_hi:[0,0,0]
	v_mfma_scale_f32_16x16x128_f8f6f4 v[100:103], v[152:159], v[24:31], v[172:175], v149, v148 op_sel_hi:[0,0,0]
	v_mfma_scale_f32_16x16x128_f8f6f4 v[96:99], v[160:167], v[24:31], v[176:179], v149, v148 op_sel_hi:[0,0,0]
	v_mfma_scale_f32_16x16x128_f8f6f4 v[84:87], v[152:159], v[32:39], v[180:183], v149, v148 op_sel_hi:[0,0,0]
	v_mfma_scale_f32_16x16x128_f8f6f4 v[8:11], v[160:167], v[32:39], v[192:195], v149, v148 op_sel_hi:[0,0,0]
	v_mfma_scale_f32_16x16x128_f8f6f4 v[68:71], v[152:159], v[40:47], v[68:71], v149, v148 op_sel_hi:[0,0,0]
	v_mfma_scale_f32_16x16x128_f8f6f4 v[56:59], v[160:167], v[40:47], v[56:59], v149, v148 op_sel_hi:[0,0,0]
	s_setprio 0
	s_barrier
	ds_read_b128 v[32:35], v127 offset:49168
	ds_read_b128 v[168:171], v127 offset:51216
	ds_read_b128 v[36:39], v128 offset:49168
	ds_read_b128 v[172:175], v128 offset:51216
	ds_read_b128 v[176:179], v127 offset:53264
	ds_read_b128 v[192:195], v127 offset:55312
	ds_read_b128 v[180:183], v128 offset:53264
	ds_read_b128 v[196:199], v128 offset:55312
	s_mov_b32 m0, s71
	s_nop 0
	buffer_load_dwordx4 v120, s[8:11], s81 offen lds
	s_nop 0
	s_mov_b32 m0, s72
	s_nop 0
	buffer_load_dwordx4 v123, s[8:11], s81 offen lds
	s_barrier
	s_waitcnt lgkmcnt(0)
	s_setprio 1
	s_waitcnt lgkmcnt(5)
	v_mfma_scale_f32_16x16x128_f8f6f4 v[64:67], v[0:7], v[32:39], v[64:67], v149, v148 op_sel_hi:[0,0,0]
	v_mfma_scale_f32_16x16x128_f8f6f4 v[60:63], v[16:23], v[32:39], v[60:63], v149, v148 op_sel_hi:[0,0,0]
	s_waitcnt lgkmcnt(4)
	v_mfma_scale_f32_16x16x128_f8f6f4 v[44:47], v[0:7], v[168:175], v[200:203], v149, v148 op_sel_hi:[0,0,0]
	v_mfma_scale_f32_16x16x128_f8f6f4 v[40:43], v[16:23], v[168:175], v[204:207], v149, v148 op_sel_hi:[0,0,0]
	s_waitcnt lgkmcnt(1)
	v_mfma_scale_f32_16x16x128_f8f6f4 v[28:31], v[0:7], v[176:183], v[224:227], v149, v148 op_sel_hi:[0,0,0]
	v_mfma_scale_f32_16x16x128_f8f6f4 v[24:27], v[16:23], v[176:183], v[228:231], v149, v148 op_sel_hi:[0,0,0]
	s_waitcnt lgkmcnt(0)
	v_mfma_scale_f32_16x16x128_f8f6f4 v[12:15], v[0:7], v[192:199], v[232:235], v149, v148 op_sel_hi:[0,0,0]
	v_mfma_scale_f32_16x16x128_f8f6f4 v[236:239], v[16:23], v[192:199], v[236:239], v149, v148 op_sel_hi:[0,0,0]
	s_setprio 0
	s_barrier
	s_mov_b32 m0, s73
	s_nop 0
	buffer_load_dwordx4 v122, s[4:7], s83 offen lds
	s_nop 0
	s_mov_b32 m0, s74
	s_nop 0
	buffer_load_dwordx4 v122, s[4:7], s82 offen lds
	s_waitcnt vmcnt(10)
	s_barrier
	s_setprio 1
	v_mfma_scale_f32_16x16x128_f8f6f4 v[52:55], v[152:159], v[32:39], v[52:55], v149, v148 op_sel_hi:[0,0,0]
	v_mfma_scale_f32_16x16x128_f8f6f4 v[48:51], v[160:167], v[32:39], v[48:51], v149, v148 op_sel_hi:[0,0,0]
	v_mfma_scale_f32_16x16x128_f8f6f4 v[36:39], v[152:159], v[168:175], v[240:243], v149, v148 op_sel_hi:[0,0,0]
	v_mfma_scale_f32_16x16x128_f8f6f4 v[32:35], v[160:167], v[168:175], v[244:247], v149, v148 op_sel_hi:[0,0,0]
	v_mfma_scale_f32_16x16x128_f8f6f4 v[20:23], v[152:159], v[176:183], v[248:251], v149, v148 op_sel_hi:[0,0,0]
	v_mfma_scale_f32_16x16x128_f8f6f4 v[16:19], v[160:167], v[176:183], v[80:83], v149, v148 op_sel_hi:[0,0,0]
	v_mfma_scale_f32_16x16x128_f8f6f4 v[4:7], v[152:159], v[192:199], v[72:75], v149, v148 op_sel_hi:[0,0,0]
	v_mfma_scale_f32_16x16x128_f8f6f4 v[0:3], v[160:167], v[192:199], v[76:79], v149, v148 op_sel_hi:[0,0,0]
	s_setprio 0
	s_barrier
	s_mov_b32 s77, s80
	s_mov_b32 s79, s78
	s_cbranch_scc0 .LBB0_1415
	s_waitcnt vmcnt(0)
	s_cmpk_lt_u32 s15, 0x100
	s_cbranch_scc0 .LBB0_1418
	s_barrier

; #define G_WAIT_V(n) asm volatile("s_waitcnt vmcnt(" #n ")" ::: "memory")
; #define G_BAR() __builtin_amdgcn_s_barrier()
; #define G_SCHED() __builtin_amdgcn_sched_barrier(0)
; #define D_STAGE_A(slot, half, kt) D_STAGE(rsA, voffA, slot, half, kt)
; #define D_STAGE_B(slot, half, kt) D_STAGE(rsB, voffB, slot, half, kt)
; #define D_LDA(dst, slot) do { _Pragma("unroll") for (int m = 0; m < 4; ++m) _Pragma("unroll") for (int k = 0; k < 2; ++k) \
;     dst[m][k] = *(const LDS_AS bf16x8*)(lds + (slot) + aoff + m * 2048 + k * 1024); } while (0)
; #define D_LDB(dst, slot) do { _Pragma("unroll") for (int n = 0; n < 2; ++n) _Pragma("unroll") for (int k = 0; k < 2; ++k) \
;     dst[n][k] = *(const LDS_AS bf16x8*)(lds + (slot) + boff + n * 2048 + k * 1024); } while (0)
; #define D_MMA(ai, bj, At, Bf) do { __builtin_amdgcn_s_setprio(1); _Pragma("unroll") for (int m = 0; m < 4; ++m) _Pragma("unroll") for (int n = 0; n < 2; ++n) _Pragma("unroll") for (int k = 0; k < 2; ++k) \
;     acc[ai][bj][m][n] = __builtin_amdgcn_mfma_f32_16x16x32_bf16(Bf[n][k], At[m][k], acc[ai][bj][m][n], 0, 0, 0); __builtin_amdgcn_s_setprio(0); } while (0)
; #define D_WAIT_L(n) asm volatile("s_waitcnt lgkmcnt(" #n ")" ::: "memory")
; #define D_STAGE_A(slot, half, kt) D_STAGE(rsA, voffA, slot, half, kt)
; #define D_WAIT_L(n) asm volatile("s_waitcnt lgkmcnt(" #n ")" ::: "memory")
;     ...
;   for (int t = 0; t < (F8_PEEL ? nt - 2 : nt); t += 2) {
;     const int t1 = t + 1;
;     const int t2 = (F8_PEEL || t + 2 < nt) ? t + 2 : t;
;     const int t3 = (F8_PEEL || t + 2 < nt) ? t + 3 : t + 1;
;     D_LDB(B0, G_SB(0, 0)); G_SCHED(); D_LDA(At, G_SA(0, 0)); D_STAGE_A(G_SA(1, 1), 1, t1);
;     D_WAIT_L(8); G_BAR(); D_WAIT_L(0); G_SCHED(); D_MMA(0, 0, At, B0); G_BAR(); G_SCHED();
;     D_LDB(B1, G_SB(0, 1)); D_STAGE_B(G_SB(0, 0), 0, t2);
;     G_BAR(); D_WAIT_L(0); G_SCHED(); D_MMA(0, 1, At, B1); G_BAR(); G_SCHED();
;     D_LDA(At, G_SA(0, 1)); D_STAGE_A(G_SA(0, 0), 0, t2);
;     G_BAR(); D_WAIT_L(0); G_SCHED(); D_MMA(1, 0, At, B0); G_BAR(); G_SCHED();
;     D_STAGE_B(G_SB(0, 1), 1, t2);
;     G_WAIT_V(6); G_BAR(); G_SCHED(); D_MMA(1, 1, At, B1); G_BAR(); G_SCHED();
.LBB0_1443:
	s_add_i32 s81, 0, 0x10010
	v_add_u32_e32 v73, s81, v69
	v_add_u32_e32 v86, s81, v70
	ds_read_b128 v[74:77], v73
	ds_read_b128 v[82:85], v73 offset:2048
	ds_read_b128 v[78:81], v86
	ds_read_b128 v[86:89], v86 offset:2048
	s_add_i32 s38, s79, 1
	s_add_i32 s78, s79, 3
	s_add_i32 s76, s79, 2
	s_add_i32 s86, 0, 0x14010
	s_cmp_lt_u32 s79, 14
	s_cselect_b32 s80, s76, s79
	s_cselect_b32 s38, s78, s38
	s_lshl_b32 s85, s80, 7
	s_lshl_b32 s80, s38, 7
	s_add_i32 s87, s85, 0x20000
	s_add_i32 s90, s85, 0x2000
	s_add_i32 s91, s85, 0x22000
	s_add_i32 s96, 0, 0x18010
	s_add_i32 s84, 0, 0x1c010
	s_add_i32 s83, s80, 0x20000
	s_add_i32 s82, s80, 0x2000
	s_add_i32 s81, s80, 0x22000
	s_add_i32 s78, s77, 0x100
	s_cmp_gt_u32 s79, 13
	ds_read_b128 v[90:93], v71 offset:16
	ds_read_b128 v[98:101], v71 offset:2064
	ds_read_b128 v[94:97], v72 offset:16
	ds_read_b128 v[102:105], v72 offset:2064
	ds_read_b128 v[106:109], v71 offset:4112
	ds_read_b128 v[114:117], v71 offset:6160
	ds_read_b128 v[110:113], v72 offset:4112
	ds_read_b128 v[118:121], v72 offset:6160
	s_mov_b32 m0, s74
	s_nop 0
	buffer_load_dwordx4 v65, s[8:11], s77 offen lds
	s_nop 0
	s_mov_b32 m0, s75
	s_nop 0
	buffer_load_dwordx4 v68, s[8:11], s77 offen lds
	s_waitcnt lgkmcnt(8)
	s_waitcnt vmcnt(10)
	s_barrier
	s_waitcnt lgkmcnt(0)
	s_setprio 1
	s_waitcnt lgkmcnt(5)
	v_mfma_scale_f32_16x16x128_f8f6f4 v[56:59], v[74:81], v[90:97], v[56:59], v149, v148 op_sel_hi:[0,0,0]
	v_mfma_scale_f32_16x16x128_f8f6f4 v[60:63], v[82:89], v[90:97], v[60:63], v149, v148 op_sel_hi:[0,0,0]
	s_waitcnt lgkmcnt(4)
	v_mfma_scale_f32_16x16x128_f8f6f4 v[44:47], v[74:81], v[98:105], v[44:47], v149, v148 op_sel_hi:[0,0,0]
	v_mfma_scale_f32_16x16x128_f8f6f4 v[40:43], v[82:89], v[98:105], v[40:43], v149, v148 op_sel_hi:[0,0,0]
	s_waitcnt lgkmcnt(1)
	v_mfma_scale_f32_16x16x128_f8f6f4 v[122:125], v[74:81], v[106:113], v[28:31], v149, v148 op_sel_hi:[0,0,0]
	v_mfma_scale_f32_16x16x128_f8f6f4 v[126:129], v[82:89], v[106:113], v[24:27], v149, v148 op_sel_hi:[0,0,0]
	s_waitcnt lgkmcnt(0)
	v_mfma_scale_f32_16x16x128_f8f6f4 v[130:133], v[74:81], v[114:121], v[12:15], v149, v148 op_sel_hi:[0,0,0]
	v_mfma_scale_f32_16x16x128_f8f6f4 v[134:137], v[82:89], v[114:121], v[8:11], v149, v148 op_sel_hi:[0,0,0]
	s_setprio 0
	s_barrier
	s_nop 3
	v_add_u32_e32 v12, s86, v69
	v_add_u32_e32 v28, s86, v70
	ds_read_b128 v[8:11], v12
	ds_read_b128 v[24:27], v12 offset:2048
	ds_read_b128 v[12:15], v28
	ds_read_b128 v[28:31], v28 offset:2048
	s_mov_b32 m0, s21
	s_nop 0
	buffer_load_dwordx4 v66, s[4:7], s85 offen lds
	s_nop 0
	s_mov_b32 m0, s39
	s_nop 0
	buffer_load_dwordx4 v66, s[4:7], s87 offen lds
	s_waitcnt vmcnt(10)
	s_barrier
	s_waitcnt lgkmcnt(0)
	s_setprio 1
	s_waitcnt lgkmcnt(1)
	v_mfma_scale_f32_16x16x128_f8f6f4 v[52:55], v[8:15], v[90:97], v[52:55], v149, v148 op_sel_hi:[0,0,0]
	s_waitcnt lgkmcnt(0)
	v_mfma_scale_f32_16x16x128_f8f6f4 v[48:51], v[24:31], v[90:97], v[48:51], v149, v148 op_sel_hi:[0,0,0]
	v_mfma_scale_f32_16x16x128_f8f6f4 v[138:141], v[8:15], v[98:105], v[36:39], v149, v148 op_sel_hi:[0,0,0]
	v_mfma_scale_f32_16x16x128_f8f6f4 v[142:145], v[24:31], v[98:105], v[32:35], v149, v148 op_sel_hi:[0,0,0]
	v_mfma_scale_f32_16x16x128_f8f6f4 v[152:155], v[8:15], v[106:113], v[20:23], v149, v148 op_sel_hi:[0,0,0]
	v_mfma_scale_f32_16x16x128_f8f6f4 v[106:109], v[24:31], v[106:113], v[16:19], v149, v148 op_sel_hi:[0,0,0]
	v_mfma_scale_f32_16x16x128_f8f6f4 v[110:113], v[8:15], v[114:121], v[4:7], v149, v148 op_sel_hi:[0,0,0]
	v_mfma_scale_f32_16x16x128_f8f6f4 v[114:117], v[24:31], v[114:121], v[0:3], v149, v148 op_sel_hi:[0,0,0]
	s_setprio 0
	s_barrier
	s_mov_b32 m0, s60
	s_nop 0
	buffer_load_dwordx4 v64, s[8:11], s85 offen lds
	s_nop 0
	s_mov_b32 m0, s61
	s_nop 0
	buffer_load_dwordx4 v67, s[8:11], s85 offen lds
	s_barrier
	s_waitcnt lgkmcnt(0)
	s_barrier
; #define G_WAIT_V(n) asm volatile("s_waitcnt vmcnt(" #n ")" ::: "memory")
; #define G_BAR() __builtin_amdgcn_s_barrier()
; #define G_SCHED() __builtin_amdgcn_sched_barrier(0)
; #define D_STAGE_A(slot, half, kt) D_STAGE(rsA, voffA, slot, half, kt)
; #define D_STAGE_B(slot, half, kt) D_STAGE(rsB, voffB, slot, half, kt)
; #define D_LDA(dst, slot) do { _Pragma("unroll") for (int m = 0; m < 4; ++m) _Pragma("unroll") for (int k = 0; k < 2; ++k) \
;     dst[m][k] = *(const LDS_AS bf16x8*)(lds + (slot) + aoff + m * 2048 + k * 1024); } while (0)
; #define D_LDB(dst, slot) do { _Pragma("unroll") for (int n = 0; n < 2; ++n) _Pragma("unroll") for (int k = 0; k < 2; ++k) \
;     dst[n][k] = *(const LDS_AS bf16x8*)(lds + (slot) + boff + n * 2048 + k * 1024); } while (0)
; #define D_MMA(ai, bj, At, Bf) do { __builtin_amdgcn_s_setprio(1); _Pragma("unroll") for (int m = 0; m < 4; ++m) _Pragma("unroll") for (int n = 0; n < 2; ++n) _Pragma("unroll") for (int k = 0; k < 2; ++k) \
;     acc[ai][bj][m][n] = __builtin_amdgcn_mfma_f32_16x16x32_bf16(Bf[n][k], At[m][k], acc[ai][bj][m][n], 0, 0, 0); __builtin_amdgcn_s_setprio(0); } while (0)
; #define D_WAIT_L(n) asm volatile("s_waitcnt lgkmcnt(" #n ")" ::: "memory")
; #define D_STAGE_A(slot, half, kt) D_STAGE(rsA, voffA, slot, half, kt)
; #define D_STAGE_B(slot, half, kt) do { _Pragma("unroll") for (int _i = 0; _i < 2; ++_i) { const unsigned _m0 = ldsw + (unsigned)((slot) + _i * 8192); const unsigned _so = (unsigned)(kt) * 128u + (half) * bt_half + _i * bt_piece; \
;     asm volatile("s_mov_b32 m0, %0\n\ts_nop 4\n\tbuffer_load_dwordx4 %1, %2, %3 offen lds" :: "s"(_m0), "v"(voffB0), "s"(rsB), "s"(_so) : "m0", "memory"); } } while (0)
;     ...
;     D_STAGE_B(G_SB(0, 1), 1, t2);
;     G_WAIT_V(6); G_BAR(); G_SCHED(); D_MMA(1, 1, At, B1); G_BAR(); G_SCHED();
;     D_LDB(B0, G_SB(1, 0)); G_SCHED(); D_LDA(At, G_SA(1, 0)); D_STAGE_A(G_SA(0, 1), 1, t2);
;     D_WAIT_L(8); G_BAR(); D_WAIT_L(0); G_SCHED(); D_MMA(0, 0, At, B0); G_BAR(); G_SCHED();
;     D_LDB(B1, G_SB(1, 1)); D_STAGE_B(G_SB(1, 0), 0, t3);
;     G_BAR(); D_WAIT_L(0); G_SCHED(); D_MMA(0, 1, At, B1); G_BAR(); G_SCHED();
;     D_LDA(At, G_SA(1, 1)); D_STAGE_A(G_SA(1, 0), 0, t3);
;     G_BAR(); D_WAIT_L(0); G_SCHED(); D_MMA(1, 0, At, B0); G_BAR(); G_SCHED();
;     D_STAGE_B(G_SB(1, 1), 1, t3);
;     G_WAIT_V(6); G_BAR(); G_SCHED(); D_MMA(1, 1, At, B1); G_BAR(); G_SCHED();
;   }
	s_mov_b32 m0, s62
	s_nop 0
	buffer_load_dwordx4 v66, s[4:7], s90 offen lds
	s_nop 0
	s_mov_b32 m0, s63
	s_nop 0
	buffer_load_dwordx4 v66, s[4:7], s91 offen lds
	s_waitcnt vmcnt(10)
	s_barrier
	s_barrier
	v_add_u32_e32 v4, s96, v69
	v_add_u32_e32 v8, s96, v70
	ds_read_b128 v[0:3], v4
	ds_read_b128 v[16:19], v4 offset:2048
	ds_read_b128 v[4:7], v8
	ds_read_b128 v[20:23], v8 offset:2048
	ds_read_b128 v[32:35], v71 offset:32784
	ds_read_b128 v[74:77], v71 offset:34832
	ds_read_b128 v[36:39], v72 offset:32784
	ds_read_b128 v[78:81], v72 offset:34832
	ds_read_b128 v[82:85], v71 offset:36880
	ds_read_b128 v[90:93], v71 offset:38928
	ds_read_b128 v[86:89], v72 offset:36880
	ds_read_b128 v[94:97], v72 offset:38928
	s_mov_b32 m0, s66
	s_nop 0
	buffer_load_dwordx4 v65, s[8:11], s85 offen lds
	s_nop 0
	s_mov_b32 m0, s67
	s_nop 0
	buffer_load_dwordx4 v68, s[8:11], s85 offen lds
	s_waitcnt lgkmcnt(8)
	s_waitcnt vmcnt(10)
	s_barrier
	s_waitcnt lgkmcnt(0)
	s_setprio 1
	s_waitcnt lgkmcnt(5)
	v_mfma_scale_f32_16x16x128_f8f6f4 v[56:59], v[0:7], v[32:39], v[56:59], v149, v148 op_sel_hi:[0,0,0]
	v_mfma_scale_f32_16x16x128_f8f6f4 v[60:63], v[16:23], v[32:39], v[60:63], v149, v148 op_sel_hi:[0,0,0]
	s_waitcnt lgkmcnt(4)
	v_mfma_scale_f32_16x16x128_f8f6f4 v[44:47], v[0:7], v[74:81], v[44:47], v149, v148 op_sel_hi:[0,0,0]
	v_mfma_scale_f32_16x16x128_f8f6f4 v[40:43], v[16:23], v[74:81], v[40:43], v149, v148 op_sel_hi:[0,0,0]
	s_waitcnt lgkmcnt(1)
	v_mfma_scale_f32_16x16x128_f8f6f4 v[28:31], v[0:7], v[82:89], v[122:125], v149, v148 op_sel_hi:[0,0,0]
	v_mfma_scale_f32_16x16x128_f8f6f4 v[24:27], v[16:23], v[82:89], v[126:129], v149, v148 op_sel_hi:[0,0,0]
	s_waitcnt lgkmcnt(0)
	v_mfma_scale_f32_16x16x128_f8f6f4 v[12:15], v[0:7], v[90:97], v[130:133], v149, v148 op_sel_hi:[0,0,0]
	v_mfma_scale_f32_16x16x128_f8f6f4 v[8:11], v[16:23], v[90:97], v[134:137], v149, v148 op_sel_hi:[0,0,0]
	s_setprio 0
	s_barrier
	v_add_u32_e32 v4, s84, v69
	v_add_u32_e32 v16, s84, v70
	ds_read_b128 v[0:3], v4
	ds_read_b128 v[98:101], v4 offset:2048
	ds_read_b128 v[4:7], v16
	ds_read_b128 v[102:105], v16 offset:2048
	s_mov_b32 m0, s68
	s_nop 0
	buffer_load_dwordx4 v66, s[4:7], s80 offen lds
	s_nop 0
	s_mov_b32 m0, s69
	s_nop 0
	buffer_load_dwordx4 v66, s[4:7], s83 offen lds
	s_waitcnt vmcnt(10)
	s_barrier
	s_waitcnt lgkmcnt(0)
	s_setprio 1
	s_waitcnt lgkmcnt(1)
	v_mfma_scale_f32_16x16x128_f8f6f4 v[52:55], v[0:7], v[32:39], v[52:55], v149, v148 op_sel_hi:[0,0,0]
	s_waitcnt lgkmcnt(0)
	v_mfma_scale_f32_16x16x128_f8f6f4 v[48:51], v[98:105], v[32:39], v[48:51], v149, v148 op_sel_hi:[0,0,0]
	v_mfma_scale_f32_16x16x128_f8f6f4 v[36:39], v[0:7], v[74:81], v[138:141], v149, v148 op_sel_hi:[0,0,0]
	v_mfma_scale_f32_16x16x128_f8f6f4 v[32:35], v[98:105], v[74:81], v[142:145], v149, v148 op_sel_hi:[0,0,0]
	v_mfma_scale_f32_16x16x128_f8f6f4 v[20:23], v[0:7], v[82:89], v[152:155], v149, v148 op_sel_hi:[0,0,0]
	v_mfma_scale_f32_16x16x128_f8f6f4 v[16:19], v[98:105], v[82:89], v[106:109], v149, v148 op_sel_hi:[0,0,0]
	v_mfma_scale_f32_16x16x128_f8f6f4 v[4:7], v[0:7], v[90:97], v[110:113], v149, v148 op_sel_hi:[0,0,0]
	v_mfma_scale_f32_16x16x128_f8f6f4 v[0:3], v[98:105], v[90:97], v[114:117], v149, v148 op_sel_hi:[0,0,0]
	s_setprio 0
	s_barrier
	s_mov_b32 m0, s70
	s_nop 0
	buffer_load_dwordx4 v64, s[8:11], s80 offen lds
	s_nop 0
	s_mov_b32 m0, s71
	s_nop 0
	buffer_load_dwordx4 v67, s[8:11], s80 offen lds
	s_barrier
	s_waitcnt lgkmcnt(0)
	s_barrier
	s_mov_b32 m0, s72
	s_nop 0
	buffer_load_dwordx4 v66, s[4:7], s82 offen lds
	s_nop 0
	s_mov_b32 m0, s73
	s_nop 0
	buffer_load_dwordx4 v66, s[4:7], s81 offen lds
	s_waitcnt vmcnt(10)
	s_barrier
	s_barrier
	s_mov_b32 s77, s78
	s_mov_b32 s79, s76
	s_cbranch_scc0 .LBB0_1443
	s_waitcnt vmcnt(0)
	s_cmpk_lt_u32 s15, 0x100
	s_cbranch_scc0 .LBB0_1446
	s_barrier

; #define G_WAIT_V(n) asm volatile("s_waitcnt vmcnt(" #n ")" ::: "memory")
; #define G_BAR() __builtin_amdgcn_s_barrier()
; #define G_SCHED() __builtin_amdgcn_sched_barrier(0)
; #define D_STAGE_A(slot, half, kt) D_STAGE(rsA, voffA, slot, half, kt)
; #define D_STAGE_B(slot, half, kt) D_STAGE(rsB, voffB, slot, half, kt)
; #define D_LDA(dst, slot) do { _Pragma("unroll") for (int m = 0; m < 4; ++m) _Pragma("unroll") for (int k = 0; k < 2; ++k) \
;     dst[m][k] = *(const LDS_AS bf16x8*)(lds + (slot) + aoff + m * 2048 + k * 1024); } while (0)
; #define D_LDB(dst, slot) do { _Pragma("unroll") for (int n = 0; n < 2; ++n) _Pragma("unroll") for (int k = 0; k < 2; ++k) \
;     dst[n][k] = *(const LDS_AS bf16x8*)(lds + (slot) + boff + n * 2048 + k * 1024); } while (0)
; #define D_MMA(ai, bj, At, Bf) do { __builtin_amdgcn_s_setprio(1); _Pragma("unroll") for (int m = 0; m < 4; ++m) _Pragma("unroll") for (int n = 0; n < 2; ++n) _Pragma("unroll") for (int k = 0; k < 2; ++k) \
;     acc[ai][bj][m][n] = __builtin_amdgcn_mfma_f32_16x16x32_bf16(Bf[n][k], At[m][k], acc[ai][bj][m][n], 0, 0, 0); __builtin_amdgcn_s_setprio(0); } while (0)
; #define D_WAIT_L(n) asm volatile("s_waitcnt lgkmcnt(" #n ")" ::: "memory")
; #define D_STAGE_A(slot, half, kt) D_STAGE(rsA, voffA, slot, half, kt)
; #define D_WAIT_L(n) asm volatile("s_waitcnt lgkmcnt(" #n ")" ::: "memory")
;     ...
;   for (int t = 0; t < (F8_PEEL ? nt - 2 : nt); t += 2) {
;     const int t1 = t + 1;
;     const int t2 = (F8_PEEL || t + 2 < nt) ? t + 2 : t;
;     const int t3 = (F8_PEEL || t + 2 < nt) ? t + 3 : t + 1;
;     D_LDB(B0, G_SB(0, 0)); G_SCHED(); D_LDA(At, G_SA(0, 0)); D_STAGE_A(G_SA(1, 1), 1, t1);
;     D_WAIT_L(8); G_BAR(); D_WAIT_L(0); G_SCHED(); D_MMA(0, 0, At, B0); G_BAR(); G_SCHED();
;     D_LDB(B1, G_SB(0, 1)); D_STAGE_B(G_SB(0, 0), 0, t2);
;     G_BAR(); D_WAIT_L(0); G_SCHED(); D_MMA(0, 1, At, B1); G_BAR(); G_SCHED();
;     D_LDA(At, G_SA(0, 1)); D_STAGE_A(G_SA(0, 0), 0, t2);
;     G_BAR(); D_WAIT_L(0); G_SCHED(); D_MMA(1, 0, At, B0); G_BAR(); G_SCHED();
;     D_STAGE_B(G_SB(0, 1), 1, t2);
;     G_WAIT_V(6); G_BAR(); G_SCHED(); D_MMA(1, 1, At, B1); G_BAR(); G_SCHED();
.LBB0_1483:
	s_add_i32 s77, 0, 0x10010
	v_add_u32_e32 v72, s77, v124
	v_add_u32_e32 v73, s77, v125
	ds_read_b128 v[152:155], v72
	ds_read_b128 v[160:163], v72 offset:2048
	ds_read_b128 v[156:159], v73
	ds_read_b128 v[164:167], v73 offset:2048
	s_add_i32 s38, s73, 1
	s_add_i32 s75, s73, 3
	s_add_i32 s74, s73, 2
	s_add_i32 s85, 0, 0x14010
	s_cmp_lt_u32 s73, 14
	s_cselect_b32 s76, s74, s73
	s_cselect_b32 s38, s75, s38
	s_lshl_b32 s81, s76, 7
	s_lshl_b32 s76, s38, 7
	s_add_i32 s86, s81, 0x20000
	s_add_i32 s83, s81, 0x2000
	s_add_i32 s84, s81, 0x22000
	s_add_i32 s82, 0, 0x18010
	s_add_i32 s80, 0, 0x1c010
	s_add_i32 s79, s76, 0x20000
	s_add_i32 s77, s76, 0x2000
	s_add_i32 s78, s76, 0x22000
	s_add_i32 s75, s72, 0x100
	s_cmp_gt_u32 s73, 13
	ds_read_b128 v[168:171], v127 offset:16
	ds_read_b128 v[176:179], v127 offset:2064
	ds_read_b128 v[172:175], v128 offset:16
	ds_read_b128 v[180:183], v128 offset:2064
	ds_read_b128 v[192:195], v127 offset:4112
	ds_read_b128 v[200:203], v127 offset:6160
	ds_read_b128 v[196:199], v128 offset:4112
	ds_read_b128 v[204:207], v128 offset:6160
	s_waitcnt lgkmcnt(12)
	s_mov_b32 m0, s26
	s_nop 0
	buffer_load_dwordx4 v122, s[8:11], s72 offen lds
	s_nop 0
	s_mov_b32 m0, s62
	s_nop 0
	buffer_load_dwordx4 v123, s[8:11], s72 offen lds
	s_waitcnt lgkmcnt(8)
	s_waitcnt vmcnt(10)
	s_barrier
	s_waitcnt lgkmcnt(0)
	s_setprio 1
	s_waitcnt lgkmcnt(5)
	v_mfma_scale_f32_16x16x128_f8f6f4 v[134:137], v[160:167], v[168:175], v[136:139], v149, v148 op_sel_hi:[0,0,0]
	s_waitcnt lgkmcnt(0)
	v_mfma_scale_f32_16x16x128_f8f6f4 v[220:223], v[152:159], v[200:207], v[220:223], v149, v148 op_sel_hi:[0,0,0]
	v_mfma_scale_f32_16x16x128_f8f6f4 v[224:227], v[160:167], v[200:207], v[224:227], v149, v148 op_sel_hi:[0,0,0]
	v_mfma_scale_f32_16x16x128_f8f6f4 v[130:133], v[152:159], v[168:175], v[140:143], v149, v148 op_sel_hi:[0,0,0]
	v_mfma_scale_f32_16x16x128_f8f6f4 v[184:187], v[152:159], v[176:183], v[108:111], v149, v148 op_sel_hi:[0,0,0]
	v_mfma_scale_f32_16x16x128_f8f6f4 v[208:211], v[160:167], v[176:183], v[104:107], v149, v148 op_sel_hi:[0,0,0]
	v_mfma_scale_f32_16x16x128_f8f6f4 v[212:215], v[152:159], v[192:199], v[92:95], v149, v148 op_sel_hi:[0,0,0]
	v_mfma_scale_f32_16x16x128_f8f6f4 v[216:219], v[160:167], v[192:199], v[88:91], v149, v148 op_sel_hi:[0,0,0]
	s_setprio 0
	s_barrier
	v_add_u32_e32 v76, s85, v124
	v_add_u32_e32 v80, s85, v125
	ds_read_b128 v[72:75], v76
	s_nop 1
	ds_read_b128 v[88:91], v76 offset:2048
	ds_read_b128 v[76:79], v80
	ds_read_b128 v[92:95], v80 offset:2048
	s_mov_b32 m0, s27
	s_nop 0
	buffer_load_dwordx4 v126, s[4:7], s81 offen lds
	s_nop 0
	s_mov_b32 m0, s63
	s_nop 0
	buffer_load_dwordx4 v126, s[4:7], s86 offen lds
	s_waitcnt vmcnt(10)
	s_barrier
	s_waitcnt lgkmcnt(0)
	s_setprio 1
	s_waitcnt lgkmcnt(1)
	v_mfma_scale_f32_16x16x128_f8f6f4 v[68:71], v[72:79], v[200:207], v[68:71], v149, v148 op_sel_hi:[0,0,0]
	s_waitcnt lgkmcnt(0)
	v_mfma_scale_f32_16x16x128_f8f6f4 v[56:59], v[88:95], v[200:207], v[56:59], v149, v148 op_sel_hi:[0,0,0]
	v_mfma_scale_f32_16x16x128_f8f6f4 v[228:231], v[72:79], v[168:175], v[116:119], v149, v148 op_sel_hi:[0,0,0]
	v_mfma_scale_f32_16x16x128_f8f6f4 v[168:171], v[88:95], v[168:175], v[112:115], v149, v148 op_sel_hi:[0,0,0]
	v_mfma_scale_f32_16x16x128_f8f6f4 v[172:175], v[72:79], v[176:183], v[100:103], v149, v148 op_sel_hi:[0,0,0]
	v_mfma_scale_f32_16x16x128_f8f6f4 v[176:179], v[88:95], v[176:183], v[96:99], v149, v148 op_sel_hi:[0,0,0]
	v_mfma_scale_f32_16x16x128_f8f6f4 v[180:183], v[72:79], v[192:199], v[84:87], v149, v148 op_sel_hi:[0,0,0]
	v_mfma_scale_f32_16x16x128_f8f6f4 v[192:195], v[88:95], v[192:199], v[8:11], v149, v148 op_sel_hi:[0,0,0]
	s_setprio 0
	s_barrier
	ds_read_b128 v[80:83], v127 offset:16400
	s_nop 1
	ds_read_b128 v[96:99], v127 offset:18448
	ds_read_b128 v[84:87], v128 offset:16400
	ds_read_b128 v[100:103], v128 offset:18448
	ds_read_b128 v[104:107], v127 offset:20496
	ds_read_b128 v[112:115], v127 offset:22544
	ds_read_b128 v[108:111], v128 offset:20496
	ds_read_b128 v[116:119], v128 offset:22544
	s_mov_b32 m0, s17
	s_nop 0
	buffer_load_dwordx4 v120, s[8:11], s81 offen lds
	s_nop 0
	s_mov_b32 m0, s66
	s_nop 0
	buffer_load_dwordx4 v121, s[8:11], s81 offen lds
	s_barrier
	s_waitcnt lgkmcnt(0)
	s_setprio 1
	s_waitcnt lgkmcnt(5)
	v_mfma_scale_f32_16x16x128_f8f6f4 v[64:67], v[152:159], v[80:87], v[64:67], v149, v148 op_sel_hi:[0,0,0]
	v_mfma_scale_f32_16x16x128_f8f6f4 v[60:63], v[160:167], v[80:87], v[60:63], v149, v148 op_sel_hi:[0,0,0]
	s_waitcnt lgkmcnt(0)
	v_mfma_scale_f32_16x16x128_f8f6f4 v[244:247], v[160:167], v[112:119], v[244:247], v149, v148 op_sel_hi:[0,0,0]
	v_mfma_scale_f32_16x16x128_f8f6f4 v[200:203], v[152:159], v[96:103], v[44:47], v149, v148 op_sel_hi:[0,0,0]
	v_mfma_scale_f32_16x16x128_f8f6f4 v[204:207], v[160:167], v[96:103], v[40:43], v149, v148 op_sel_hi:[0,0,0]
	v_mfma_scale_f32_16x16x128_f8f6f4 v[232:235], v[152:159], v[104:111], v[28:31], v149, v148 op_sel_hi:[0,0,0]
	v_mfma_scale_f32_16x16x128_f8f6f4 v[236:239], v[160:167], v[104:111], v[24:27], v149, v148 op_sel_hi:[0,0,0]
	v_mfma_scale_f32_16x16x128_f8f6f4 v[240:243], v[152:159], v[112:119], v[12:15], v149, v148 op_sel_hi:[0,0,0]
	s_setprio 0
	s_barrier
	s_mov_b32 m0, s28
	s_nop 0
	buffer_load_dwordx4 v126, s[4:7], s83 offen lds
	s_nop 0
	s_mov_b32 m0, s67
	s_nop 0
	buffer_load_dwordx4 v126, s[4:7], s84 offen lds
	s_waitcnt vmcnt(10)
	s_barrier
; #define G_WAIT_V(n) asm volatile("s_waitcnt vmcnt(" #n ")" ::: "memory")
; #define G_BAR() __builtin_amdgcn_s_barrier()
; #define G_SCHED() __builtin_amdgcn_sched_barrier(0)
; #define D_STAGE_A(slot, half, kt) D_STAGE(rsA, voffA, slot, half, kt)
; #define D_STAGE_B(slot, half, kt) D_STAGE(rsB, voffB, slot, half, kt)
; #define D_LDA(dst, slot) do { _Pragma("unroll") for (int m = 0; m < 4; ++m) _Pragma("unroll") for (int k = 0; k < 2; ++k) \
;     dst[m][k] = *(const LDS_AS bf16x8*)(lds + (slot) + aoff + m * 2048 + k * 1024); } while (0)
; #define D_LDB(dst, slot) do { _Pragma("unroll") for (int n = 0; n < 2; ++n) _Pragma("unroll") for (int k = 0; k < 2; ++k) \
;     dst[n][k] = *(const LDS_AS bf16x8*)(lds + (slot) + boff + n * 2048 + k * 1024); } while (0)
; #define D_MMA(ai, bj, At, Bf) do { __builtin_amdgcn_s_setprio(1); _Pragma("unroll") for (int m = 0; m < 4; ++m) _Pragma("unroll") for (int n = 0; n < 2; ++n) _Pragma("unroll") for (int k = 0; k < 2; ++k) \
;     acc[ai][bj][m][n] = __builtin_amdgcn_mfma_f32_16x16x32_bf16(Bf[n][k], At[m][k], acc[ai][bj][m][n], 0, 0, 0); __builtin_amdgcn_s_setprio(0); } while (0)
; #define D_WAIT_L(n) asm volatile("s_waitcnt lgkmcnt(" #n ")" ::: "memory")
; #define D_STAGE_A(slot, half, kt) D_STAGE(rsA, voffA, slot, half, kt)
; #define D_STAGE_B(slot, half, kt) do { _Pragma("unroll") for (int _i = 0; _i < 2; ++_i) { const unsigned _m0 = ldsw + (unsigned)((slot) + _i * 8192); const unsigned _so = (unsigned)(kt) * 128u + (half) * bt_half + _i * bt_piece; \
;     asm volatile("s_mov_b32 m0, %0\n\ts_nop 4\n\tbuffer_load_dwordx4 %1, %2, %3 offen lds" :: "s"(_m0), "v"(voffB0), "s"(rsB), "s"(_so) : "m0", "memory"); } } while (0)
; #define D_WAIT_L(n) asm volatile("s_waitcnt lgkmcnt(" #n ")" ::: "memory")
;     ...
;     D_LDB(B0, G_SB(1, 0)); G_SCHED(); D_LDA(At, G_SA(1, 0)); D_STAGE_A(G_SA(0, 1), 1, t2);
;     D_WAIT_L(8); G_BAR(); D_WAIT_L(0); G_SCHED(); D_MMA(0, 0, At, B0); G_BAR(); G_SCHED();
;     D_LDB(B1, G_SB(1, 1)); D_STAGE_B(G_SB(1, 0), 0, t3);
;     G_BAR(); D_WAIT_L(0); G_SCHED(); D_MMA(0, 1, At, B1); G_BAR(); G_SCHED();
;     D_LDA(At, G_SA(1, 1)); D_STAGE_A(G_SA(1, 0), 0, t3);
;     G_BAR(); D_WAIT_L(0); G_SCHED(); D_MMA(1, 0, At, B0); G_BAR(); G_SCHED();
;     D_STAGE_B(G_SB(1, 1), 1, t3);
;     G_WAIT_V(6); G_BAR(); G_SCHED(); D_MMA(1, 1, At, B1); G_BAR(); G_SCHED();
;   }
	s_setprio 1
	v_mfma_scale_f32_16x16x128_f8f6f4 v[52:55], v[72:79], v[80:87], v[52:55], v149, v148 op_sel_hi:[0,0,0]
	v_mfma_scale_f32_16x16x128_f8f6f4 v[48:51], v[88:95], v[80:87], v[48:51], v149, v148 op_sel_hi:[0,0,0]
	v_mfma_scale_f32_16x16x128_f8f6f4 v[248:251], v[72:79], v[96:103], v[36:39], v149, v148 op_sel_hi:[0,0,0]
	v_mfma_scale_f32_16x16x128_f8f6f4 v[188:191], v[88:95], v[96:103], v[32:35], v149, v148 op_sel_hi:[0,0,0]
	v_mfma_scale_f32_16x16x128_f8f6f4 v[144:147], v[72:79], v[104:111], v[20:23], v149, v148 op_sel_hi:[0,0,0]
	v_mfma_scale_f32_16x16x128_f8f6f4 v[80:83], v[88:95], v[104:111], v[16:19], v149, v148 op_sel_hi:[0,0,0]
	v_mfma_scale_f32_16x16x128_f8f6f4 v[72:75], v[72:79], v[112:119], v[4:7], v149, v148 op_sel_hi:[0,0,0]
	v_mfma_scale_f32_16x16x128_f8f6f4 v[76:79], v[88:95], v[112:119], v[0:3], v149, v148 op_sel_hi:[0,0,0]
	s_setprio 0
	s_barrier
	s_nop 3
	v_add_u32_e32 v4, s82, v124
	v_add_u32_e32 v8, s82, v125
	ds_read_b128 v[0:3], v4
	ds_read_b128 v[16:19], v4 offset:2048
	ds_read_b128 v[4:7], v8
	ds_read_b128 v[20:23], v8 offset:2048
	ds_read_b128 v[8:11], v127 offset:32784
	ds_read_b128 v[24:27], v127 offset:34832
	ds_read_b128 v[12:15], v128 offset:32784
	ds_read_b128 v[28:31], v128 offset:34832
	ds_read_b128 v[32:35], v127 offset:36880
	ds_read_b128 v[40:43], v127 offset:38928
	ds_read_b128 v[36:39], v128 offset:36880
	ds_read_b128 v[44:47], v128 offset:38928
	s_mov_b32 m0, s29
	s_nop 0
	buffer_load_dwordx4 v122, s[8:11], s81 offen lds
	s_nop 0
	s_mov_b32 m0, s68
	s_nop 0
	buffer_load_dwordx4 v123, s[8:11], s81 offen lds
	s_waitcnt lgkmcnt(8)
	s_waitcnt vmcnt(10)
	s_barrier
	s_waitcnt lgkmcnt(0)
	s_setprio 1
	s_waitcnt lgkmcnt(5)
	v_mfma_scale_f32_16x16x128_f8f6f4 v[140:143], v[0:7], v[8:15], v[130:133], v149, v148 op_sel_hi:[0,0,0]
	v_mfma_scale_f32_16x16x128_f8f6f4 v[136:139], v[16:23], v[8:15], v[134:137], v149, v148 op_sel_hi:[0,0,0]
	s_waitcnt lgkmcnt(4)
	v_mfma_scale_f32_16x16x128_f8f6f4 v[108:111], v[0:7], v[24:31], v[184:187], v149, v148 op_sel_hi:[0,0,0]
	v_mfma_scale_f32_16x16x128_f8f6f4 v[104:107], v[16:23], v[24:31], v[208:211], v149, v148 op_sel_hi:[0,0,0]
	s_waitcnt lgkmcnt(1)
	v_mfma_scale_f32_16x16x128_f8f6f4 v[92:95], v[0:7], v[32:39], v[212:215], v149, v148 op_sel_hi:[0,0,0]
	v_mfma_scale_f32_16x16x128_f8f6f4 v[88:91], v[16:23], v[32:39], v[216:219], v149, v148 op_sel_hi:[0,0,0]
	s_waitcnt lgkmcnt(0)
	v_mfma_scale_f32_16x16x128_f8f6f4 v[220:223], v[0:7], v[40:47], v[220:223], v149, v148 op_sel_hi:[0,0,0]
	v_mfma_scale_f32_16x16x128_f8f6f4 v[224:227], v[16:23], v[40:47], v[224:227], v149, v148 op_sel_hi:[0,0,0]
	s_setprio 0
	s_barrier
	v_add_u32_e32 v84, s80, v124
	v_add_u32_e32 v85, s80, v125
	ds_read_b128 v[152:155], v84
	ds_read_b128 v[160:163], v84 offset:2048
	ds_read_b128 v[156:159], v85
	ds_read_b128 v[164:167], v85 offset:2048
	s_mov_b32 m0, s39
	s_nop 0
	buffer_load_dwordx4 v126, s[4:7], s76 offen lds
	s_nop 0
	s_mov_b32 m0, s69
	s_nop 0
	buffer_load_dwordx4 v126, s[4:7], s79 offen lds
	s_waitcnt vmcnt(10)
	s_barrier
	s_waitcnt lgkmcnt(0)
	s_setprio 1
	s_waitcnt lgkmcnt(1)
	v_mfma_scale_f32_16x16x128_f8f6f4 v[116:119], v[152:159], v[8:15], v[228:231], v149, v148 op_sel_hi:[0,0,0]
	s_waitcnt lgkmcnt(0)
	v_mfma_scale_f32_16x16x128_f8f6f4 v[112:115], v[160:167], v[8:15], v[168:171], v149, v148 op_sel_hi:[0,0,0]
	v_mfma_scale_f32_16x16x128_f8f6f4 v[100:103], v[152:159], v[24:31], v[172:175], v149, v148 op_sel_hi:[0,0,0]
	v_mfma_scale_f32_16x16x128_f8f6f4 v[96:99], v[160:167], v[24:31], v[176:179], v149, v148 op_sel_hi:[0,0,0]
	v_mfma_scale_f32_16x16x128_f8f6f4 v[84:87], v[152:159], v[32:39], v[180:183], v149, v148 op_sel_hi:[0,0,0]
	v_mfma_scale_f32_16x16x128_f8f6f4 v[8:11], v[160:167], v[32:39], v[192:195], v149, v148 op_sel_hi:[0,0,0]
	v_mfma_scale_f32_16x16x128_f8f6f4 v[68:71], v[152:159], v[40:47], v[68:71], v149, v148 op_sel_hi:[0,0,0]
	v_mfma_scale_f32_16x16x128_f8f6f4 v[56:59], v[160:167], v[40:47], v[56:59], v149, v148 op_sel_hi:[0,0,0]
	s_setprio 0
	s_barrier
	ds_read_b128 v[32:35], v127 offset:49168
	ds_read_b128 v[168:171], v127 offset:51216
	ds_read_b128 v[36:39], v128 offset:49168
	ds_read_b128 v[172:175], v128 offset:51216
	ds_read_b128 v[176:179], v127 offset:53264
	ds_read_b128 v[192:195], v127 offset:55312
	ds_read_b128 v[180:183], v128 offset:53264
	ds_read_b128 v[196:199], v128 offset:55312
	s_mov_b32 m0, s60
	s_nop 0
	buffer_load_dwordx4 v120, s[8:11], s76 offen lds
	s_nop 0
	s_mov_b32 m0, s70
	s_nop 0
	buffer_load_dwordx4 v121, s[8:11], s76 offen lds
	s_barrier
	s_waitcnt lgkmcnt(0)
	s_setprio 1
	s_waitcnt lgkmcnt(5)
	v_mfma_scale_f32_16x16x128_f8f6f4 v[64:67], v[0:7], v[32:39], v[64:67], v149, v148 op_sel_hi:[0,0,0]
	v_mfma_scale_f32_16x16x128_f8f6f4 v[60:63], v[16:23], v[32:39], v[60:63], v149, v148 op_sel_hi:[0,0,0]
	s_waitcnt lgkmcnt(4)
	v_mfma_scale_f32_16x16x128_f8f6f4 v[44:47], v[0:7], v[168:175], v[200:203], v149, v148 op_sel_hi:[0,0,0]
	v_mfma_scale_f32_16x16x128_f8f6f4 v[40:43], v[16:23], v[168:175], v[204:207], v149, v148 op_sel_hi:[0,0,0]
	s_waitcnt lgkmcnt(1)
	v_mfma_scale_f32_16x16x128_f8f6f4 v[28:31], v[0:7], v[176:183], v[232:235], v149, v148 op_sel_hi:[0,0,0]
	v_mfma_scale_f32_16x16x128_f8f6f4 v[24:27], v[16:23], v[176:183], v[236:239], v149, v148 op_sel_hi:[0,0,0]
	s_waitcnt lgkmcnt(0)
	v_mfma_scale_f32_16x16x128_f8f6f4 v[12:15], v[0:7], v[192:199], v[240:243], v149, v148 op_sel_hi:[0,0,0]
	v_mfma_scale_f32_16x16x128_f8f6f4 v[244:247], v[16:23], v[192:199], v[244:247], v149, v148 op_sel_hi:[0,0,0]
	s_setprio 0
	s_barrier
	s_mov_b32 m0, s61
	s_nop 0
	buffer_load_dwordx4 v126, s[4:7], s77 offen lds
	s_nop 0
	s_mov_b32 m0, s71
	s_nop 0
	buffer_load_dwordx4 v126, s[4:7], s78 offen lds
	s_waitcnt vmcnt(10)
	s_barrier
	s_setprio 1
	v_mfma_scale_f32_16x16x128_f8f6f4 v[52:55], v[152:159], v[32:39], v[52:55], v149, v148 op_sel_hi:[0,0,0]
	v_mfma_scale_f32_16x16x128_f8f6f4 v[48:51], v[160:167], v[32:39], v[48:51], v149, v148 op_sel_hi:[0,0,0]
	v_mfma_scale_f32_16x16x128_f8f6f4 v[36:39], v[152:159], v[168:175], v[248:251], v149, v148 op_sel_hi:[0,0,0]
	v_mfma_scale_f32_16x16x128_f8f6f4 v[32:35], v[160:167], v[168:175], v[188:191], v149, v148 op_sel_hi:[0,0,0]
	v_mfma_scale_f32_16x16x128_f8f6f4 v[20:23], v[152:159], v[176:183], v[144:147], v149, v148 op_sel_hi:[0,0,0]
	v_mfma_scale_f32_16x16x128_f8f6f4 v[16:19], v[160:167], v[176:183], v[80:83], v149, v148 op_sel_hi:[0,0,0]
	v_mfma_scale_f32_16x16x128_f8f6f4 v[4:7], v[152:159], v[192:199], v[72:75], v149, v148 op_sel_hi:[0,0,0]
	v_mfma_scale_f32_16x16x128_f8f6f4 v[0:3], v[160:167], v[192:199], v[76:79], v149, v148 op_sel_hi:[0,0,0]
	s_setprio 0
	s_barrier
	s_mov_b32 s72, s75
	s_mov_b32 s73, s74
	s_cbranch_scc0 .LBB0_1483
	s_waitcnt vmcnt(0)
	s_cmpk_lt_u32 s15, 0x100
	s_cbranch_scc0 .LBB0_1486
	s_barrier

; #define G_BAR() __builtin_amdgcn_s_barrier()
; #define G_SCHED() __builtin_amdgcn_sched_barrier(0)
; #define D_STAGE_A(slot, half, kt) D_STAGE(rsA, voffA, slot, half, kt)
; #define D_STAGE_B(slot, half, kt) D_STAGE(rsB, voffB, slot, half, kt)
; #define D_LDA(dst, slot) do { _Pragma("unroll") for (int m = 0; m < 4; ++m) _Pragma("unroll") for (int k = 0; k < 2; ++k) \
;     dst[m][k] = *(const LDS_AS bf16x8*)(lds + (slot) + aoff + m * 2048 + k * 1024); } while (0)
; #define D_LDB(dst, slot) do { _Pragma("unroll") for (int n = 0; n < 2; ++n) _Pragma("unroll") for (int k = 0; k < 2; ++k) \
;     dst[n][k] = *(const LDS_AS bf16x8*)(lds + (slot) + boff + n * 2048 + k * 1024); } while (0)
; #define D_MMA(ai, bj, At, Bf) do { __builtin_amdgcn_s_setprio(1); _Pragma("unroll") for (int m = 0; m < 4; ++m) _Pragma("unroll") for (int n = 0; n < 2; ++n) _Pragma("unroll") for (int k = 0; k < 2; ++k) \
;     acc[ai][bj][m][n] = __builtin_amdgcn_mfma_f32_16x16x32_bf16(Bf[n][k], At[m][k], acc[ai][bj][m][n], 0, 0, 0); __builtin_amdgcn_s_setprio(0); } while (0)
; #define D_WAIT_L(n) asm volatile("s_waitcnt lgkmcnt(" #n ")" ::: "memory")
; #define D_STAGE_A(slot, half, kt) D_STAGE(rsA, voffA, slot, half, kt)
; #define D_STAGE_B(slot, half, kt) do { _Pragma("unroll") for (int _i = 0; _i < 2; ++_i) { const unsigned _m0 = ldsw + (unsigned)((slot) + _i * 8192); const unsigned _so = (unsigned)(kt) * 128u + (half) * bt_half + _i * bt_piece; \
;     asm volatile("s_mov_b32 m0, %0\n\ts_nop 4\n\tbuffer_load_dwordx4 %1, %2, %3 offen lds" :: "s"(_m0), "v"(voffB0), "s"(rsB), "s"(_so) : "m0", "memory"); } } while (0)
; #define D_WAIT_L(n) asm volatile("s_waitcnt lgkmcnt(" #n ")" ::: "memory")
;     ...
;   for (int t = 0; t < (F8_PEEL ? nt - 2 : nt); t += 2) {
;     const int t1 = t + 1;
;     const int t2 = (F8_PEEL || t + 2 < nt) ? t + 2 : t;
;     const int t3 = (F8_PEEL || t + 2 < nt) ? t + 3 : t + 1;
;     D_LDB(B0, G_SB(0, 0)); G_SCHED(); D_LDA(At, G_SA(0, 0)); D_STAGE_A(G_SA(1, 1), 1, t1);
;     D_WAIT_L(8); G_BAR(); D_WAIT_L(0); G_SCHED(); D_MMA(0, 0, At, B0); G_BAR(); G_SCHED();
;     D_LDB(B1, G_SB(0, 1)); D_STAGE_B(G_SB(0, 0), 0, t2);
;     G_BAR(); D_WAIT_L(0); G_SCHED(); D_MMA(0, 1, At, B1); G_BAR(); G_SCHED();
.LBB0_1510:
	s_add_i32 s77, 0, 0x10010
	s_waitcnt vmcnt(62)
	v_add_u32_e32 v73, s77, v68
	s_waitcnt vmcnt(49)
	v_add_u32_e32 v86, s77, v69
	ds_read_b128 v[74:77], v73
	ds_read_b128 v[82:85], v73 offset:2048
	ds_read_b128 v[78:81], v86
	s_waitcnt vmcnt(46)
	ds_read_b128 v[86:89], v86 offset:2048
	s_add_i32 s38, s75, 1
	s_add_i32 s74, s75, 3
	s_add_i32 s73, s75, 2
	s_add_i32 s82, 0, 0x14010
	s_cmp_lt_u32 s75, 14
	s_cselect_b32 s76, s73, s75
	s_cselect_b32 s38, s74, s38
	s_lshl_b32 s81, s76, 7
	s_lshl_b32 s76, s38, 7
	s_add_i32 s83, s81, 0x20000
	s_add_i32 s84, s81, 0x2000
	s_add_i32 s85, s81, 0x22000
	s_add_i32 s86, 0, 0x18010
	s_add_i32 s80, 0, 0x1c010
	s_add_i32 s79, s76, 0x20000
	s_add_i32 s77, s76, 0x2000
	s_add_i32 s78, s76, 0x22000
	s_add_i32 s74, s72, 0x100
	s_cmp_gt_u32 s75, 13
	s_waitcnt vmcnt(42)
	ds_read_b128 v[90:93], v71 offset:16
	s_waitcnt vmcnt(34)
	ds_read_b128 v[98:101], v71 offset:2064
	ds_read_b128 v[94:97], v72 offset:16
	s_waitcnt vmcnt(30)
	ds_read_b128 v[102:105], v72 offset:2064
	s_waitcnt vmcnt(26)
	ds_read_b128 v[106:109], v71 offset:4112
	s_waitcnt vmcnt(18)
	ds_read_b128 v[114:117], v71 offset:6160
	ds_read_b128 v[110:113], v72 offset:4112
	s_waitcnt vmcnt(2)
	ds_read_b128 v[118:121], v72 offset:6160
	s_waitcnt lgkmcnt(12)
	s_mov_b32 m0, s26
	s_nop 0
	buffer_load_dwordx4 v66, s[8:11], s72 offen lds
	s_nop 0
	s_mov_b32 m0, s62
	s_nop 0
	buffer_load_dwordx4 v67, s[8:11], s72 offen lds
	s_waitcnt lgkmcnt(8)
	s_waitcnt vmcnt(10)
	s_barrier
	s_waitcnt lgkmcnt(0)
	s_setprio 1
	s_waitcnt lgkmcnt(5)
	v_mfma_scale_f32_16x16x128_f8f6f4 v[56:59], v[74:81], v[90:97], v[56:59], v149, v148 op_sel_hi:[0,0,0]
	v_mfma_scale_f32_16x16x128_f8f6f4 v[60:63], v[82:89], v[90:97], v[60:63], v149, v148 op_sel_hi:[0,0,0]
	s_waitcnt lgkmcnt(4)
	v_mfma_scale_f32_16x16x128_f8f6f4 v[44:47], v[74:81], v[98:105], v[44:47], v149, v148 op_sel_hi:[0,0,0]
	v_mfma_scale_f32_16x16x128_f8f6f4 v[40:43], v[82:89], v[98:105], v[40:43], v149, v148 op_sel_hi:[0,0,0]
	s_waitcnt vmcnt(0) lgkmcnt(1)
	v_mfma_scale_f32_16x16x128_f8f6f4 v[122:125], v[74:81], v[106:113], v[28:31], v149, v148 op_sel_hi:[0,0,0]
	v_mfma_scale_f32_16x16x128_f8f6f4 v[126:129], v[82:89], v[106:113], v[24:27], v149, v148 op_sel_hi:[0,0,0]
	s_waitcnt lgkmcnt(0)
	v_mfma_scale_f32_16x16x128_f8f6f4 v[130:133], v[74:81], v[114:121], v[12:15], v149, v148 op_sel_hi:[0,0,0]
	v_mfma_scale_f32_16x16x128_f8f6f4 v[134:137], v[82:89], v[114:121], v[8:11], v149, v148 op_sel_hi:[0,0,0]
	s_setprio 0
	s_barrier
	s_nop 3
	v_add_u32_e32 v12, s82, v68
	v_add_u32_e32 v28, s82, v69
	ds_read_b128 v[8:11], v12
	ds_read_b128 v[24:27], v12 offset:2048
	ds_read_b128 v[12:15], v28
	ds_read_b128 v[28:31], v28 offset:2048
	s_mov_b32 m0, s27
	s_nop 0
	buffer_load_dwordx4 v70, s[4:7], s81 offen lds
	s_nop 0
	s_mov_b32 m0, s63
	s_nop 0
	buffer_load_dwordx4 v70, s[4:7], s83 offen lds
	s_waitcnt vmcnt(10)
	s_barrier
	s_waitcnt lgkmcnt(0)
	s_setprio 1
	s_waitcnt lgkmcnt(1)
	v_mfma_scale_f32_16x16x128_f8f6f4 v[52:55], v[8:15], v[90:97], v[52:55], v149, v148 op_sel_hi:[0,0,0]
	s_waitcnt lgkmcnt(0)
	v_mfma_scale_f32_16x16x128_f8f6f4 v[48:51], v[24:31], v[90:97], v[48:51], v149, v148 op_sel_hi:[0,0,0]
	v_mfma_scale_f32_16x16x128_f8f6f4 v[138:141], v[8:15], v[98:105], v[36:39], v149, v148 op_sel_hi:[0,0,0]
	v_mfma_scale_f32_16x16x128_f8f6f4 v[152:155], v[24:31], v[98:105], v[32:35], v149, v148 op_sel_hi:[0,0,0]
	v_mfma_scale_f32_16x16x128_f8f6f4 v[156:159], v[8:15], v[106:113], v[20:23], v149, v148 op_sel_hi:[0,0,0]
	v_mfma_scale_f32_16x16x128_f8f6f4 v[106:109], v[24:31], v[106:113], v[16:19], v149, v148 op_sel_hi:[0,0,0]
	v_mfma_scale_f32_16x16x128_f8f6f4 v[110:113], v[8:15], v[114:121], v[4:7], v149, v148 op_sel_hi:[0,0,0]
	v_mfma_scale_f32_16x16x128_f8f6f4 v[114:117], v[24:31], v[114:121], v[0:3], v149, v148 op_sel_hi:[0,0,0]
	s_setprio 0
	s_barrier
; #define G_WAIT_V(n) asm volatile("s_waitcnt vmcnt(" #n ")" ::: "memory")
; #define G_BAR() __builtin_amdgcn_s_barrier()
; #define G_SCHED() __builtin_amdgcn_sched_barrier(0)
; #define D_STAGE_A(slot, half, kt) D_STAGE(rsA, voffA, slot, half, kt)
; #define D_STAGE_B(slot, half, kt) D_STAGE(rsB, voffB, slot, half, kt)
; #define D_LDA(dst, slot) do { _Pragma("unroll") for (int m = 0; m < 4; ++m) _Pragma("unroll") for (int k = 0; k < 2; ++k) \
;     dst[m][k] = *(const LDS_AS bf16x8*)(lds + (slot) + aoff + m * 2048 + k * 1024); } while (0)
; #define D_LDB(dst, slot) do { _Pragma("unroll") for (int n = 0; n < 2; ++n) _Pragma("unroll") for (int k = 0; k < 2; ++k) \
;     dst[n][k] = *(const LDS_AS bf16x8*)(lds + (slot) + boff + n * 2048 + k * 1024); } while (0)
; #define D_MMA(ai, bj, At, Bf) do { __builtin_amdgcn_s_setprio(1); _Pragma("unroll") for (int m = 0; m < 4; ++m) _Pragma("unroll") for (int n = 0; n < 2; ++n) _Pragma("unroll") for (int k = 0; k < 2; ++k) \
;     acc[ai][bj][m][n] = __builtin_amdgcn_mfma_f32_16x16x32_bf16(Bf[n][k], At[m][k], acc[ai][bj][m][n], 0, 0, 0); __builtin_amdgcn_s_setprio(0); } while (0)
; #define D_WAIT_L(n) asm volatile("s_waitcnt lgkmcnt(" #n ")" ::: "memory")
; #define D_STAGE_A(slot, half, kt) D_STAGE(rsA, voffA, slot, half, kt)
; #define D_WAIT_L(n) asm volatile("s_waitcnt lgkmcnt(" #n ")" ::: "memory")
;     ...
;     D_LDA(At, G_SA(0, 1)); D_STAGE_A(G_SA(0, 0), 0, t2);
;     G_BAR(); D_WAIT_L(0); G_SCHED(); D_MMA(1, 0, At, B0); G_BAR(); G_SCHED();
;     D_STAGE_B(G_SB(0, 1), 1, t2);
;     G_WAIT_V(6); G_BAR(); G_SCHED(); D_MMA(1, 1, At, B1); G_BAR(); G_SCHED();
;     D_LDB(B0, G_SB(1, 0)); G_SCHED(); D_LDA(At, G_SA(1, 0)); D_STAGE_A(G_SA(0, 1), 1, t2);
;     D_WAIT_L(8); G_BAR(); D_WAIT_L(0); G_SCHED(); D_MMA(0, 0, At, B0); G_BAR(); G_SCHED();
;     D_LDB(B1, G_SB(1, 1)); D_STAGE_B(G_SB(1, 0), 0, t3);
;     G_BAR(); D_WAIT_L(0); G_SCHED(); D_MMA(0, 1, At, B1); G_BAR(); G_SCHED();
;     D_LDA(At, G_SA(1, 1)); D_STAGE_A(G_SA(1, 0), 0, t3);
;     G_BAR(); D_WAIT_L(0); G_SCHED(); D_MMA(1, 0, At, B0); G_BAR(); G_SCHED();
;     D_STAGE_B(G_SB(1, 1), 1, t3);
;     G_WAIT_V(6); G_BAR(); G_SCHED(); D_MMA(1, 1, At, B1); G_BAR(); G_SCHED();
;   }
	s_mov_b32 m0, s17
	s_nop 0
	buffer_load_dwordx4 v64, s[8:11], s81 offen lds
	s_nop 0
	s_mov_b32 m0, s66
	s_nop 0
	buffer_load_dwordx4 v65, s[8:11], s81 offen lds
	s_barrier
	s_waitcnt lgkmcnt(0)
	s_barrier
	s_mov_b32 m0, s28
	s_nop 0
	buffer_load_dwordx4 v70, s[4:7], s84 offen lds
	s_nop 0
	s_mov_b32 m0, s67
	s_nop 0
	buffer_load_dwordx4 v70, s[4:7], s85 offen lds
	s_waitcnt vmcnt(10)
	s_barrier
	s_barrier
	v_add_u32_e32 v4, s86, v68
	v_add_u32_e32 v8, s86, v69
	ds_read_b128 v[0:3], v4
	ds_read_b128 v[16:19], v4 offset:2048
	ds_read_b128 v[4:7], v8
	ds_read_b128 v[20:23], v8 offset:2048
	ds_read_b128 v[32:35], v71 offset:32784
	ds_read_b128 v[74:77], v71 offset:34832
	ds_read_b128 v[36:39], v72 offset:32784
	ds_read_b128 v[78:81], v72 offset:34832
	ds_read_b128 v[82:85], v71 offset:36880
	ds_read_b128 v[90:93], v71 offset:38928
	ds_read_b128 v[86:89], v72 offset:36880
	ds_read_b128 v[94:97], v72 offset:38928
	s_mov_b32 m0, s29
	s_nop 0
	buffer_load_dwordx4 v66, s[8:11], s81 offen lds
	s_nop 0
	s_mov_b32 m0, s68
	s_nop 0
	buffer_load_dwordx4 v67, s[8:11], s81 offen lds
	s_waitcnt lgkmcnt(8)
	s_waitcnt vmcnt(10)
	s_barrier
	s_waitcnt lgkmcnt(0)
	s_setprio 1
	s_waitcnt lgkmcnt(5)
	v_mfma_scale_f32_16x16x128_f8f6f4 v[56:59], v[0:7], v[32:39], v[56:59], v149, v148 op_sel_hi:[0,0,0]
	v_mfma_scale_f32_16x16x128_f8f6f4 v[60:63], v[16:23], v[32:39], v[60:63], v149, v148 op_sel_hi:[0,0,0]
	s_waitcnt lgkmcnt(4)
	v_mfma_scale_f32_16x16x128_f8f6f4 v[44:47], v[0:7], v[74:81], v[44:47], v149, v148 op_sel_hi:[0,0,0]
	v_mfma_scale_f32_16x16x128_f8f6f4 v[40:43], v[16:23], v[74:81], v[40:43], v149, v148 op_sel_hi:[0,0,0]
	s_waitcnt lgkmcnt(1)
	v_mfma_scale_f32_16x16x128_f8f6f4 v[28:31], v[0:7], v[82:89], v[122:125], v149, v148 op_sel_hi:[0,0,0]
	v_mfma_scale_f32_16x16x128_f8f6f4 v[24:27], v[16:23], v[82:89], v[126:129], v149, v148 op_sel_hi:[0,0,0]
	s_waitcnt lgkmcnt(0)
	v_mfma_scale_f32_16x16x128_f8f6f4 v[12:15], v[0:7], v[90:97], v[130:133], v149, v148 op_sel_hi:[0,0,0]
	v_mfma_scale_f32_16x16x128_f8f6f4 v[8:11], v[16:23], v[90:97], v[134:137], v149, v148 op_sel_hi:[0,0,0]
	s_setprio 0
	s_barrier
	v_add_u32_e32 v4, s80, v68
	v_add_u32_e32 v16, s80, v69
	ds_read_b128 v[0:3], v4
	ds_read_b128 v[98:101], v4 offset:2048
	ds_read_b128 v[4:7], v16
	ds_read_b128 v[102:105], v16 offset:2048
	s_mov_b32 m0, s39
	s_nop 0
	buffer_load_dwordx4 v70, s[4:7], s76 offen lds
	s_nop 0
	s_mov_b32 m0, s69
	s_nop 0
	buffer_load_dwordx4 v70, s[4:7], s79 offen lds
	s_waitcnt vmcnt(10)
	s_barrier
	s_waitcnt lgkmcnt(0)
	s_setprio 1
	s_waitcnt lgkmcnt(1)
	v_mfma_scale_f32_16x16x128_f8f6f4 v[52:55], v[0:7], v[32:39], v[52:55], v149, v148 op_sel_hi:[0,0,0]
	s_waitcnt lgkmcnt(0)
	v_mfma_scale_f32_16x16x128_f8f6f4 v[48:51], v[98:105], v[32:39], v[48:51], v149, v148 op_sel_hi:[0,0,0]
	v_mfma_scale_f32_16x16x128_f8f6f4 v[36:39], v[0:7], v[74:81], v[138:141], v149, v148 op_sel_hi:[0,0,0]
	v_mfma_scale_f32_16x16x128_f8f6f4 v[32:35], v[98:105], v[74:81], v[152:155], v149, v148 op_sel_hi:[0,0,0]
	v_mfma_scale_f32_16x16x128_f8f6f4 v[20:23], v[0:7], v[82:89], v[156:159], v149, v148 op_sel_hi:[0,0,0]
	v_mfma_scale_f32_16x16x128_f8f6f4 v[16:19], v[98:105], v[82:89], v[106:109], v149, v148 op_sel_hi:[0,0,0]
	v_mfma_scale_f32_16x16x128_f8f6f4 v[4:7], v[0:7], v[90:97], v[110:113], v149, v148 op_sel_hi:[0,0,0]
	v_mfma_scale_f32_16x16x128_f8f6f4 v[0:3], v[98:105], v[90:97], v[114:117], v149, v148 op_sel_hi:[0,0,0]
	s_setprio 0
	s_barrier
	s_mov_b32 m0, s60
	s_nop 0
	buffer_load_dwordx4 v64, s[8:11], s76 offen lds
	s_nop 0
	s_mov_b32 m0, s70
	s_nop 0
	buffer_load_dwordx4 v65, s[8:11], s76 offen lds
	s_barrier
	s_waitcnt lgkmcnt(0)
	s_barrier
	s_mov_b32 m0, s61
	s_nop 0
	buffer_load_dwordx4 v70, s[4:7], s77 offen lds
	s_nop 0
	s_mov_b32 m0, s71
	s_nop 0
	buffer_load_dwordx4 v70, s[4:7], s78 offen lds
	s_waitcnt vmcnt(10)
	s_barrier
	s_barrier
	s_mov_b32 s72, s74
	s_mov_b32 s75, s73
	s_cbranch_scc0 .LBB0_1510
	s_waitcnt vmcnt(0)
	s_cmpk_lt_u32 s15, 0x100
	s_cbranch_scc0 .LBB0_1513
	s_barrier

; #define G_WAIT_V(n) asm volatile("s_waitcnt vmcnt(" #n ")" ::: "memory")
; #define G_BAR() __builtin_amdgcn_s_barrier()
; #define G_SCHED() __builtin_amdgcn_sched_barrier(0)
; #define D_STAGE_A(slot, half, kt) D_STAGE(rsA, voffA, slot, half, kt)
; #define D_STAGE_B(slot, half, kt) D_STAGE(rsB, voffB, slot, half, kt)
; #define D_LDA(dst, slot) do { _Pragma("unroll") for (int m = 0; m < 4; ++m) _Pragma("unroll") for (int k = 0; k < 2; ++k) \
;     dst[m][k] = *(const LDS_AS bf16x8*)(lds + (slot) + aoff + m * 2048 + k * 1024); } while (0)
; #define D_LDB(dst, slot) do { _Pragma("unroll") for (int n = 0; n < 2; ++n) _Pragma("unroll") for (int k = 0; k < 2; ++k) \
;     dst[n][k] = *(const LDS_AS bf16x8*)(lds + (slot) + boff + n * 2048 + k * 1024); } while (0)
; #define D_MMA(ai, bj, At, Bf) do { __builtin_amdgcn_s_setprio(1); _Pragma("unroll") for (int m = 0; m < 4; ++m) _Pragma("unroll") for (int n = 0; n < 2; ++n) _Pragma("unroll") for (int k = 0; k < 2; ++k) \
;     acc[ai][bj][m][n] = __builtin_amdgcn_mfma_f32_16x16x32_bf16(Bf[n][k], At[m][k], acc[ai][bj][m][n], 0, 0, 0); __builtin_amdgcn_s_setprio(0); } while (0)
; #define D_WAIT_L(n) asm volatile("s_waitcnt lgkmcnt(" #n ")" ::: "memory")
; #define D_STAGE_A(slot, half, kt) D_STAGE(rsA, voffA, slot, half, kt)
; #define D_WAIT_L(n) asm volatile("s_waitcnt lgkmcnt(" #n ")" ::: "memory")
;     ...
;   for (int t = 0; t < (F8_PEEL ? nt - 2 : nt); t += 2) {
;     const int t1 = t + 1;
;     const int t2 = (F8_PEEL || t + 2 < nt) ? t + 2 : t;
;     const int t3 = (F8_PEEL || t + 2 < nt) ? t + 3 : t + 1;
;     D_LDB(B0, G_SB(0, 0)); G_SCHED(); D_LDA(At, G_SA(0, 0)); D_STAGE_A(G_SA(1, 1), 1, t1);
;     D_WAIT_L(8); G_BAR(); D_WAIT_L(0); G_SCHED(); D_MMA(0, 0, At, B0); G_BAR(); G_SCHED();
;     D_LDB(B1, G_SB(0, 1)); D_STAGE_B(G_SB(0, 0), 0, t2);
;     G_BAR(); D_WAIT_L(0); G_SCHED(); D_MMA(0, 1, At, B1); G_BAR(); G_SCHED();
;     D_LDA(At, G_SA(0, 1)); D_STAGE_A(G_SA(0, 0), 0, t2);
;     G_BAR(); D_WAIT_L(0); G_SCHED(); D_MMA(1, 0, At, B0); G_BAR(); G_SCHED();
;     D_STAGE_B(G_SB(0, 1), 1, t2);
;     G_WAIT_V(6); G_BAR(); G_SCHED(); D_MMA(1, 1, At, B1); G_BAR(); G_SCHED();
.LBB0_1606:
	s_add_i32 s74, 0, 0x10010
	v_add_u32_e32 v68, s74, v133
	v_add_u32_e32 v69, s74, v134
	ds_read_b128 v[146:149], v68
	ds_read_b128 v[154:157], v68 offset:2048
	ds_read_b128 v[150:153], v69
	ds_read_b128 v[158:161], v69 offset:2048
	s_add_i32 s38, s71, 1
	s_add_i32 s72, s71, 3
	s_add_i32 s70, s71, 2
	s_add_i32 s82, 0, 0x14010
	s_cmp_lt_u32 s71, 14
	s_cselect_b32 s73, s70, s71
	s_cselect_b32 s38, s72, s38
	s_lshl_b32 s78, s73, 7
	s_lshl_b32 s73, s38, 7
	s_add_i32 s83, s78, 0x20000
	s_add_i32 s81, s78, 0x40000
	s_add_i32 s80, s78, 0x60000
	s_add_i32 s79, 0, 0x18010
	s_add_i32 s77, 0, 0x1c010
	s_add_i32 s76, s73, 0x20000
	s_add_i32 s75, s73, 0x40000
	s_add_i32 s74, s73, 0x60000
	s_add_i32 s72, s69, 0x100
	s_cmp_gt_u32 s71, 13
	ds_read_b128 v[168:171], v135 offset:16
	ds_read_b128 v[176:179], v135 offset:2064
	ds_read_b128 v[172:175], v136 offset:16
	ds_read_b128 v[180:183], v136 offset:2064
	ds_read_b128 v[192:195], v135 offset:4112
	ds_read_b128 v[200:203], v135 offset:6160
	ds_read_b128 v[196:199], v136 offset:4112
	ds_read_b128 v[204:207], v136 offset:6160
	s_mov_b32 m0, s67
	s_nop 0
	buffer_load_dwordx4 v129, s[8:11], s69 offen lds
	s_nop 0
	s_mov_b32 m0, s68
	s_nop 0
	buffer_load_dwordx4 v132, s[8:11], s69 offen lds
	s_waitcnt lgkmcnt(8)
	s_waitcnt vmcnt(10)
	s_barrier
	s_waitcnt lgkmcnt(0)
	s_setprio 1
	s_waitcnt lgkmcnt(0)
	v_mfma_scale_f32_16x16x128_f8f6f4 v[216:219], v[146:153], v[200:207], v[216:219], v165, v164 op_sel_hi:[0,0,0]
	v_mfma_scale_f32_16x16x128_f8f6f4 v[48:51], v[154:161], v[200:207], v[48:51], v165, v164 op_sel_hi:[0,0,0]
	v_mfma_scale_f32_16x16x128_f8f6f4 v[138:141], v[146:153], v[168:175], v[124:127], v165, v164 op_sel_hi:[0,0,0]
	v_mfma_scale_f32_16x16x128_f8f6f4 v[142:145], v[154:161], v[168:175], v[120:123], v165, v164 op_sel_hi:[0,0,0]
	v_mfma_scale_f32_16x16x128_f8f6f4 v[184:187], v[146:153], v[176:183], v[108:111], v165, v164 op_sel_hi:[0,0,0]
	v_mfma_scale_f32_16x16x128_f8f6f4 v[188:191], v[154:161], v[176:183], v[100:103], v165, v164 op_sel_hi:[0,0,0]
	v_mfma_scale_f32_16x16x128_f8f6f4 v[208:211], v[146:153], v[192:199], v[84:87], v165, v164 op_sel_hi:[0,0,0]
	v_mfma_scale_f32_16x16x128_f8f6f4 v[212:215], v[154:161], v[192:199], v[80:83], v165, v164 op_sel_hi:[0,0,0]
	s_setprio 0
	s_barrier
	v_add_u32_e32 v68, s82, v133
	v_add_u32_e32 v69, s82, v134
	s_nop 2
	ds_read_b128 v[80:83], v68
	ds_read_b128 v[120:123], v68 offset:2048
	ds_read_b128 v[84:87], v69
	ds_read_b128 v[124:127], v69 offset:2048
	s_mov_b32 m0, s39
	s_nop 0
	buffer_load_dwordx4 v130, s[4:7], s78 offen lds
	s_nop 0
	s_mov_b32 m0, s50
	s_nop 0
	buffer_load_dwordx4 v130, s[4:7], s83 offen lds
	s_waitcnt vmcnt(10)
	s_barrier
	s_waitcnt lgkmcnt(0)
	s_setprio 1
	s_waitcnt lgkmcnt(1)
	v_mfma_scale_f32_16x16x128_f8f6f4 v[116:119], v[80:87], v[168:175], v[116:119], v165, v164 op_sel_hi:[0,0,0]
	s_waitcnt lgkmcnt(0)
	v_mfma_scale_f32_16x16x128_f8f6f4 v[112:115], v[120:127], v[168:175], v[112:115], v165, v164 op_sel_hi:[0,0,0]
	v_mfma_scale_f32_16x16x128_f8f6f4 v[76:79], v[80:87], v[200:207], v[76:79], v165, v164 op_sel_hi:[0,0,0]
	v_mfma_scale_f32_16x16x128_f8f6f4 v[166:169], v[80:87], v[176:183], v[104:107], v165, v164 op_sel_hi:[0,0,0]
	v_mfma_scale_f32_16x16x128_f8f6f4 v[170:173], v[120:127], v[176:183], v[96:99], v165, v164 op_sel_hi:[0,0,0]
	v_mfma_scale_f32_16x16x128_f8f6f4 v[174:177], v[80:87], v[192:199], v[92:95], v165, v164 op_sel_hi:[0,0,0]
	v_mfma_scale_f32_16x16x128_f8f6f4 v[178:181], v[120:127], v[192:199], v[88:91], v165, v164 op_sel_hi:[0,0,0]
	v_mfma_scale_f32_16x16x128_f8f6f4 v[192:195], v[120:127], v[200:207], v[16:19], v165, v164 op_sel_hi:[0,0,0]
	s_setprio 0
	s_barrier
	ds_read_b128 v[68:71], v135 offset:16400
	s_nop 2
	ds_read_b128 v[88:91], v135 offset:18448
	ds_read_b128 v[72:75], v136 offset:16400
	ds_read_b128 v[92:95], v136 offset:18448
	ds_read_b128 v[96:99], v135 offset:20496
	ds_read_b128 v[104:107], v135 offset:22544
	ds_read_b128 v[100:103], v136 offset:20496
	ds_read_b128 v[108:111], v136 offset:22544
	s_mov_b32 m0, s51
	s_nop 0
	buffer_load_dwordx4 v128, s[8:11], s78 offen lds
	s_nop 0
	s_mov_b32 m0, s54
	s_nop 0
	buffer_load_dwordx4 v131, s[8:11], s78 offen lds
	s_barrier
	s_waitcnt lgkmcnt(0)
	s_setprio 1
	s_waitcnt lgkmcnt(5)
	v_mfma_scale_f32_16x16x128_f8f6f4 v[56:59], v[146:153], v[68:75], v[56:59], v165, v164 op_sel_hi:[0,0,0]
	v_mfma_scale_f32_16x16x128_f8f6f4 v[52:55], v[154:161], v[68:75], v[52:55], v165, v164 op_sel_hi:[0,0,0]
	s_waitcnt lgkmcnt(1)
	v_mfma_scale_f32_16x16x128_f8f6f4 v[224:227], v[154:161], v[96:103], v[224:227], v165, v164 op_sel_hi:[0,0,0]
	v_mfma_scale_f32_16x16x128_f8f6f4 v[200:203], v[146:153], v[88:95], v[36:39], v165, v164 op_sel_hi:[0,0,0]
	v_mfma_scale_f32_16x16x128_f8f6f4 v[204:207], v[154:161], v[88:95], v[32:35], v165, v164 op_sel_hi:[0,0,0]
	v_mfma_scale_f32_16x16x128_f8f6f4 v[220:223], v[146:153], v[96:103], v[20:23], v165, v164 op_sel_hi:[0,0,0]
	s_waitcnt lgkmcnt(0)
	v_mfma_scale_f32_16x16x128_f8f6f4 v[228:231], v[146:153], v[104:111], v[4:7], v165, v164 op_sel_hi:[0,0,0]
	v_mfma_scale_f32_16x16x128_f8f6f4 v[232:235], v[154:161], v[104:111], v[0:3], v165, v164 op_sel_hi:[0,0,0]
	s_setprio 0
	s_barrier
	s_mov_b32 m0, s55
	s_nop 0
	buffer_load_dwordx4 v130, s[4:7], s81 offen lds
	s_nop 0
	s_mov_b32 m0, s58
	s_nop 0
	buffer_load_dwordx4 v130, s[4:7], s80 offen lds
	s_waitcnt vmcnt(10)
	s_barrier
; #define G_WAIT_V(n) asm volatile("s_waitcnt vmcnt(" #n ")" ::: "memory")
; #define G_BAR() __builtin_amdgcn_s_barrier()
; #define G_SCHED() __builtin_amdgcn_sched_barrier(0)
; #define D_STAGE_A(slot, half, kt) D_STAGE(rsA, voffA, slot, half, kt)
; #define D_STAGE_B(slot, half, kt) D_STAGE(rsB, voffB, slot, half, kt)
; #define D_LDA(dst, slot) do { _Pragma("unroll") for (int m = 0; m < 4; ++m) _Pragma("unroll") for (int k = 0; k < 2; ++k) \
;     dst[m][k] = *(const LDS_AS bf16x8*)(lds + (slot) + aoff + m * 2048 + k * 1024); } while (0)
; #define D_LDB(dst, slot) do { _Pragma("unroll") for (int n = 0; n < 2; ++n) _Pragma("unroll") for (int k = 0; k < 2; ++k) \
;     dst[n][k] = *(const LDS_AS bf16x8*)(lds + (slot) + boff + n * 2048 + k * 1024); } while (0)
; #define D_MMA(ai, bj, At, Bf) do { __builtin_amdgcn_s_setprio(1); _Pragma("unroll") for (int m = 0; m < 4; ++m) _Pragma("unroll") for (int n = 0; n < 2; ++n) _Pragma("unroll") for (int k = 0; k < 2; ++k) \
;     acc[ai][bj][m][n] = __builtin_amdgcn_mfma_f32_16x16x32_bf16(Bf[n][k], At[m][k], acc[ai][bj][m][n], 0, 0, 0); __builtin_amdgcn_s_setprio(0); } while (0)
; #define D_WAIT_L(n) asm volatile("s_waitcnt lgkmcnt(" #n ")" ::: "memory")
; #define D_STAGE_A(slot, half, kt) D_STAGE(rsA, voffA, slot, half, kt)
; #define D_STAGE_B(slot, half, kt) do { _Pragma("unroll") for (int _i = 0; _i < 2; ++_i) { const unsigned _m0 = ldsw + (unsigned)((slot) + _i * 8192); const unsigned _so = (unsigned)(kt) * 128u + (half) * bt_half + _i * bt_piece; \
;     asm volatile("s_mov_b32 m0, %0\n\ts_nop 4\n\tbuffer_load_dwordx4 %1, %2, %3 offen lds" :: "s"(_m0), "v"(voffB0), "s"(rsB), "s"(_so) : "m0", "memory"); } } while (0)
; #define D_WAIT_L(n) asm volatile("s_waitcnt lgkmcnt(" #n ")" ::: "memory")
;     ...
;     D_LDB(B0, G_SB(1, 0)); G_SCHED(); D_LDA(At, G_SA(1, 0)); D_STAGE_A(G_SA(0, 1), 1, t2);
;     D_WAIT_L(8); G_BAR(); D_WAIT_L(0); G_SCHED(); D_MMA(0, 0, At, B0); G_BAR(); G_SCHED();
;     D_LDB(B1, G_SB(1, 1)); D_STAGE_B(G_SB(1, 0), 0, t3);
;     G_BAR(); D_WAIT_L(0); G_SCHED(); D_MMA(0, 1, At, B1); G_BAR(); G_SCHED();
;     D_LDA(At, G_SA(1, 1)); D_STAGE_A(G_SA(1, 0), 0, t3);
;     G_BAR(); D_WAIT_L(0); G_SCHED(); D_MMA(1, 0, At, B0); G_BAR(); G_SCHED();
;     D_STAGE_B(G_SB(1, 1), 1, t3);
;     G_WAIT_V(6); G_BAR(); G_SCHED(); D_MMA(1, 1, At, B1); G_BAR(); G_SCHED();
;   }
	s_setprio 1
	v_mfma_scale_f32_16x16x128_f8f6f4 v[64:67], v[80:87], v[68:75], v[64:67], v165, v164 op_sel_hi:[0,0,0]
	v_mfma_scale_f32_16x16x128_f8f6f4 v[60:63], v[120:127], v[68:75], v[60:63], v165, v164 op_sel_hi:[0,0,0]
	v_mfma_scale_f32_16x16x128_f8f6f4 v[236:239], v[80:87], v[88:95], v[44:47], v165, v164 op_sel_hi:[0,0,0]
	v_mfma_scale_f32_16x16x128_f8f6f4 v[240:243], v[120:127], v[88:95], v[40:43], v165, v164 op_sel_hi:[0,0,0]
	v_mfma_scale_f32_16x16x128_f8f6f4 v[244:247], v[80:87], v[96:103], v[28:31], v165, v164 op_sel_hi:[0,0,0]
	v_mfma_scale_f32_16x16x128_f8f6f4 v[248:251], v[120:127], v[96:103], v[24:27], v165, v164 op_sel_hi:[0,0,0]
	v_mfma_scale_f32_16x16x128_f8f6f4 v[68:71], v[80:87], v[104:111], v[12:15], v165, v164 op_sel_hi:[0,0,0]
	v_mfma_scale_f32_16x16x128_f8f6f4 v[72:75], v[120:127], v[104:111], v[8:11], v165, v164 op_sel_hi:[0,0,0]
	s_setprio 0
	s_barrier
	v_add_u32_e32 v4, s79, v133
	s_nop 2
	v_add_u32_e32 v12, s79, v134
	ds_read_b128 v[0:3], v4
	ds_read_b128 v[8:11], v4 offset:2048
	ds_read_b128 v[4:7], v12
	ds_read_b128 v[12:15], v12 offset:2048
	ds_read_b128 v[16:19], v135 offset:32784
	ds_read_b128 v[24:27], v135 offset:34832
	ds_read_b128 v[20:23], v136 offset:32784
	ds_read_b128 v[28:31], v136 offset:34832
	ds_read_b128 v[32:35], v135 offset:36880
	ds_read_b128 v[40:43], v135 offset:38928
	ds_read_b128 v[36:39], v136 offset:36880
	ds_read_b128 v[44:47], v136 offset:38928
	s_mov_b32 m0, s59
	s_nop 0
	buffer_load_dwordx4 v129, s[8:11], s78 offen lds
	s_nop 0
	s_mov_b32 m0, s60
	s_nop 0
	buffer_load_dwordx4 v132, s[8:11], s78 offen lds
	s_waitcnt lgkmcnt(8)
	s_waitcnt vmcnt(10)
	s_barrier
	s_waitcnt lgkmcnt(0)
	s_setprio 1
	s_waitcnt lgkmcnt(5)
	v_mfma_scale_f32_16x16x128_f8f6f4 v[124:127], v[0:7], v[16:23], v[138:141], v165, v164 op_sel_hi:[0,0,0]
	v_mfma_scale_f32_16x16x128_f8f6f4 v[120:123], v[8:15], v[16:23], v[142:145], v165, v164 op_sel_hi:[0,0,0]
	s_waitcnt lgkmcnt(4)
	v_mfma_scale_f32_16x16x128_f8f6f4 v[108:111], v[0:7], v[24:31], v[184:187], v165, v164 op_sel_hi:[0,0,0]
	v_mfma_scale_f32_16x16x128_f8f6f4 v[100:103], v[8:15], v[24:31], v[188:191], v165, v164 op_sel_hi:[0,0,0]
	s_waitcnt lgkmcnt(1)
	v_mfma_scale_f32_16x16x128_f8f6f4 v[84:87], v[0:7], v[32:39], v[208:211], v165, v164 op_sel_hi:[0,0,0]
	v_mfma_scale_f32_16x16x128_f8f6f4 v[80:83], v[8:15], v[32:39], v[212:215], v165, v164 op_sel_hi:[0,0,0]
	s_waitcnt lgkmcnt(0)
	v_mfma_scale_f32_16x16x128_f8f6f4 v[216:219], v[0:7], v[40:47], v[216:219], v165, v164 op_sel_hi:[0,0,0]
	v_mfma_scale_f32_16x16x128_f8f6f4 v[48:51], v[8:15], v[40:47], v[48:51], v165, v164 op_sel_hi:[0,0,0]
	s_setprio 0
	s_barrier
	v_add_u32_e32 v88, s77, v133
	v_add_u32_e32 v89, s77, v134
	ds_read_b128 v[146:149], v88
	ds_read_b128 v[154:157], v88 offset:2048
	ds_read_b128 v[150:153], v89
	ds_read_b128 v[158:161], v89 offset:2048
	s_mov_b32 m0, s61
	s_nop 0
	buffer_load_dwordx4 v130, s[4:7], s73 offen lds
	s_nop 0
	s_mov_b32 m0, s62
	s_nop 0
	buffer_load_dwordx4 v130, s[4:7], s76 offen lds
	s_waitcnt vmcnt(10)
	s_barrier
	s_waitcnt lgkmcnt(0)
	s_setprio 1
	s_waitcnt lgkmcnt(1)
	v_mfma_scale_f32_16x16x128_f8f6f4 v[116:119], v[146:153], v[16:23], v[116:119], v165, v164 op_sel_hi:[0,0,0]
	s_waitcnt lgkmcnt(0)
	v_mfma_scale_f32_16x16x128_f8f6f4 v[112:115], v[154:161], v[16:23], v[112:115], v165, v164 op_sel_hi:[0,0,0]
	v_mfma_scale_f32_16x16x128_f8f6f4 v[104:107], v[146:153], v[24:31], v[166:169], v165, v164 op_sel_hi:[0,0,0]
	v_mfma_scale_f32_16x16x128_f8f6f4 v[96:99], v[154:161], v[24:31], v[170:173], v165, v164 op_sel_hi:[0,0,0]
	v_mfma_scale_f32_16x16x128_f8f6f4 v[92:95], v[146:153], v[32:39], v[174:177], v165, v164 op_sel_hi:[0,0,0]
	v_mfma_scale_f32_16x16x128_f8f6f4 v[88:91], v[154:161], v[32:39], v[178:181], v165, v164 op_sel_hi:[0,0,0]
	v_mfma_scale_f32_16x16x128_f8f6f4 v[76:79], v[146:153], v[40:47], v[76:79], v165, v164 op_sel_hi:[0,0,0]
	v_mfma_scale_f32_16x16x128_f8f6f4 v[16:19], v[154:161], v[40:47], v[192:195], v165, v164 op_sel_hi:[0,0,0]
	s_setprio 0
	s_barrier
	ds_read_b128 v[24:27], v135 offset:49168
	ds_read_b128 v[168:171], v135 offset:51216
	ds_read_b128 v[28:31], v136 offset:49168
	ds_read_b128 v[172:175], v136 offset:51216
	ds_read_b128 v[176:179], v135 offset:53264
	ds_read_b128 v[192:195], v135 offset:55312
	ds_read_b128 v[180:183], v136 offset:53264
	ds_read_b128 v[196:199], v136 offset:55312
	s_mov_b32 m0, s63
	s_nop 0
	buffer_load_dwordx4 v128, s[8:11], s73 offen lds
	s_nop 0
	s_mov_b32 m0, s64
	s_nop 0
	buffer_load_dwordx4 v131, s[8:11], s73 offen lds
	s_barrier
	s_waitcnt lgkmcnt(0)
	s_setprio 1
	s_waitcnt lgkmcnt(5)
	v_mfma_scale_f32_16x16x128_f8f6f4 v[56:59], v[0:7], v[24:31], v[56:59], v165, v164 op_sel_hi:[0,0,0]
	v_mfma_scale_f32_16x16x128_f8f6f4 v[52:55], v[8:15], v[24:31], v[52:55], v165, v164 op_sel_hi:[0,0,0]
	s_waitcnt lgkmcnt(4)
	v_mfma_scale_f32_16x16x128_f8f6f4 v[36:39], v[0:7], v[168:175], v[200:203], v165, v164 op_sel_hi:[0,0,0]
	v_mfma_scale_f32_16x16x128_f8f6f4 v[32:35], v[8:15], v[168:175], v[204:207], v165, v164 op_sel_hi:[0,0,0]
	s_waitcnt lgkmcnt(1)
	v_mfma_scale_f32_16x16x128_f8f6f4 v[20:23], v[0:7], v[176:183], v[220:223], v165, v164 op_sel_hi:[0,0,0]
	v_mfma_scale_f32_16x16x128_f8f6f4 v[224:227], v[8:15], v[176:183], v[224:227], v165, v164 op_sel_hi:[0,0,0]
	s_waitcnt lgkmcnt(0)
	v_mfma_scale_f32_16x16x128_f8f6f4 v[4:7], v[0:7], v[192:199], v[228:231], v165, v164 op_sel_hi:[0,0,0]
	v_mfma_scale_f32_16x16x128_f8f6f4 v[0:3], v[8:15], v[192:199], v[232:235], v165, v164 op_sel_hi:[0,0,0]
	s_setprio 0
	s_barrier
	s_mov_b32 m0, s65
	s_nop 0
	buffer_load_dwordx4 v130, s[4:7], s75 offen lds
	s_nop 0
	s_mov_b32 m0, s66
	s_nop 0
	buffer_load_dwordx4 v130, s[4:7], s74 offen lds
	s_waitcnt vmcnt(10)
	s_barrier
	s_setprio 1
	v_mfma_scale_f32_16x16x128_f8f6f4 v[64:67], v[146:153], v[24:31], v[64:67], v165, v164 op_sel_hi:[0,0,0]
	v_mfma_scale_f32_16x16x128_f8f6f4 v[60:63], v[154:161], v[24:31], v[60:63], v165, v164 op_sel_hi:[0,0,0]
	v_mfma_scale_f32_16x16x128_f8f6f4 v[44:47], v[146:153], v[168:175], v[236:239], v165, v164 op_sel_hi:[0,0,0]
	v_mfma_scale_f32_16x16x128_f8f6f4 v[40:43], v[154:161], v[168:175], v[240:243], v165, v164 op_sel_hi:[0,0,0]
	v_mfma_scale_f32_16x16x128_f8f6f4 v[28:31], v[146:153], v[176:183], v[244:247], v165, v164 op_sel_hi:[0,0,0]
	v_mfma_scale_f32_16x16x128_f8f6f4 v[24:27], v[154:161], v[176:183], v[248:251], v165, v164 op_sel_hi:[0,0,0]
	v_mfma_scale_f32_16x16x128_f8f6f4 v[12:15], v[146:153], v[192:199], v[68:71], v165, v164 op_sel_hi:[0,0,0]
	v_mfma_scale_f32_16x16x128_f8f6f4 v[8:11], v[154:161], v[192:199], v[72:75], v165, v164 op_sel_hi:[0,0,0]
	s_setprio 0
	s_barrier
	s_mov_b32 s69, s72
	s_mov_b32 s71, s70
	s_cbranch_scc0 .LBB0_1606
	s_waitcnt vmcnt(0)
	s_cmpk_lt_u32 s13, 0x100
	s_cbranch_scc0 .LBB0_1609
	s_barrier

; #define G_WAIT_V(n) asm volatile("s_waitcnt vmcnt(" #n ")" ::: "memory")
; #define G_BAR() __builtin_amdgcn_s_barrier()
; #define G_SCHED() __builtin_amdgcn_sched_barrier(0)
; #define D_STAGE_A(slot, half, kt) D_STAGE(rsA, voffA, slot, half, kt)
; #define D_STAGE_B(slot, half, kt) D_STAGE(rsB, voffB, slot, half, kt)
; #define D_LDA(dst, slot) do { _Pragma("unroll") for (int m = 0; m < 4; ++m) _Pragma("unroll") for (int k = 0; k < 2; ++k) \
;     dst[m][k] = *(const LDS_AS bf16x8*)(lds + (slot) + aoff + m * 2048 + k * 1024); } while (0)
; #define D_LDB(dst, slot) do { _Pragma("unroll") for (int n = 0; n < 2; ++n) _Pragma("unroll") for (int k = 0; k < 2; ++k) \
;     dst[n][k] = *(const LDS_AS bf16x8*)(lds + (slot) + boff + n * 2048 + k * 1024); } while (0)
; #define D_MMA(ai, bj, At, Bf) do { __builtin_amdgcn_s_setprio(1); _Pragma("unroll") for (int m = 0; m < 4; ++m) _Pragma("unroll") for (int n = 0; n < 2; ++n) _Pragma("unroll") for (int k = 0; k < 2; ++k) \
;     acc[ai][bj][m][n] = __builtin_amdgcn_mfma_f32_16x16x32_bf16(Bf[n][k], At[m][k], acc[ai][bj][m][n], 0, 0, 0); __builtin_amdgcn_s_setprio(0); } while (0)
; #define D_WAIT_L(n) asm volatile("s_waitcnt lgkmcnt(" #n ")" ::: "memory")
; #define D_STAGE_A(slot, half, kt) D_STAGE(rsA, voffA, slot, half, kt)
; #define D_WAIT_L(n) asm volatile("s_waitcnt lgkmcnt(" #n ")" ::: "memory")
;     ...
;   for (int t = 0; t < (F8_PEEL ? nt - 2 : nt); t += 2) {
;     const int t1 = t + 1;
;     const int t2 = (F8_PEEL || t + 2 < nt) ? t + 2 : t;
;     const int t3 = (F8_PEEL || t + 2 < nt) ? t + 3 : t + 1;
;     D_LDB(B0, G_SB(0, 0)); G_SCHED(); D_LDA(At, G_SA(0, 0)); D_STAGE_A(G_SA(1, 1), 1, t1);
;     D_WAIT_L(8); G_BAR(); D_WAIT_L(0); G_SCHED(); D_MMA(0, 0, At, B0); G_BAR(); G_SCHED();
;     D_LDB(B1, G_SB(0, 1)); D_STAGE_B(G_SB(0, 0), 0, t2);
;     G_BAR(); D_WAIT_L(0); G_SCHED(); D_MMA(0, 1, At, B1); G_BAR(); G_SCHED();
;     D_LDA(At, G_SA(0, 1)); D_STAGE_A(G_SA(0, 0), 0, t2);
;     G_BAR(); D_WAIT_L(0); G_SCHED(); D_MMA(1, 0, At, B0); G_BAR(); G_SCHED();
;     D_STAGE_B(G_SB(0, 1), 1, t2);
;     G_WAIT_V(6); G_BAR(); G_SCHED(); D_MMA(1, 1, At, B1); G_BAR(); G_SCHED();
.LBB0_1634:
	s_add_i32 s73, 0, 0x10010
	v_add_u32_e32 v73, s73, v69
	v_add_u32_e32 v86, s73, v70
	ds_read_b128 v[74:77], v73
	ds_read_b128 v[82:85], v73 offset:2048
	ds_read_b128 v[78:81], v86
	ds_read_b128 v[86:89], v86 offset:2048
	s_add_i32 s38, s71, 1
	s_add_i32 s70, s71, 3
	s_add_i32 s68, s71, 2
	s_add_i32 s78, 0, 0x14010
	s_cmp_lt_u32 s71, 14
	s_cselect_b32 s72, s68, s71
	s_cselect_b32 s38, s70, s38
	s_lshl_b32 s77, s72, 7
	s_lshl_b32 s72, s38, 7
	s_add_i32 s79, s77, 0x20000
	s_add_i32 s80, s77, 0x40000
	s_add_i32 s81, s77, 0x60000
	s_add_i32 s82, 0, 0x18010
	s_add_i32 s76, 0, 0x1c010
	s_add_i32 s75, s72, 0x20000
	s_add_i32 s74, s72, 0x40000
	s_add_i32 s73, s72, 0x60000
	s_add_i32 s70, s69, 0x100
	s_cmp_gt_u32 s71, 13
	ds_read_b128 v[90:93], v71 offset:16
	ds_read_b128 v[98:101], v71 offset:2064
	ds_read_b128 v[94:97], v72 offset:16
	ds_read_b128 v[102:105], v72 offset:2064
	ds_read_b128 v[106:109], v71 offset:4112
	ds_read_b128 v[114:117], v71 offset:6160
	ds_read_b128 v[110:113], v72 offset:4112
	ds_read_b128 v[118:121], v72 offset:6160
	s_mov_b32 m0, s66
	s_nop 0
	buffer_load_dwordx4 v65, s[8:11], s69 offen lds
	s_nop 0
	s_mov_b32 m0, s67
	s_nop 0
	buffer_load_dwordx4 v68, s[8:11], s69 offen lds
	s_waitcnt lgkmcnt(8)
	s_waitcnt vmcnt(10)
	s_barrier
	s_waitcnt lgkmcnt(0)
	s_setprio 1
	s_waitcnt lgkmcnt(4)
	v_mfma_scale_f32_16x16x128_f8f6f4 v[40:43], v[74:81], v[98:105], v[40:43], v165, v164 op_sel_hi:[0,0,0]
	v_mfma_scale_f32_16x16x128_f8f6f4 v[32:35], v[82:89], v[98:105], v[32:35], v165, v164 op_sel_hi:[0,0,0]
	s_waitcnt lgkmcnt(1)
	v_mfma_scale_f32_16x16x128_f8f6f4 v[24:27], v[74:81], v[106:113], v[24:27], v165, v164 op_sel_hi:[0,0,0]
	v_mfma_scale_f32_16x16x128_f8f6f4 v[16:19], v[82:89], v[106:113], v[16:19], v165, v164 op_sel_hi:[0,0,0]
	s_waitcnt lgkmcnt(0)
	v_mfma_scale_f32_16x16x128_f8f6f4 v[8:11], v[74:81], v[114:121], v[8:11], v165, v164 op_sel_hi:[0,0,0]
	v_mfma_scale_f32_16x16x128_f8f6f4 v[122:125], v[74:81], v[90:97], v[48:51], v165, v164 op_sel_hi:[0,0,0]
	v_mfma_scale_f32_16x16x128_f8f6f4 v[126:129], v[82:89], v[90:97], v[52:55], v165, v164 op_sel_hi:[0,0,0]
	v_mfma_scale_f32_16x16x128_f8f6f4 v[130:133], v[82:89], v[114:121], v[0:3], v165, v164 op_sel_hi:[0,0,0]
	s_setprio 0
	s_barrier
	s_nop 4
	v_add_u32_e32 v0, s78, v69
	v_add_u32_e32 v1, s78, v70
	ds_read_b128 v[48:51], v0
	ds_read_b128 v[74:77], v0 offset:2048
	ds_read_b128 v[52:55], v1
	ds_read_b128 v[78:81], v1 offset:2048
	s_mov_b32 m0, s39
	s_nop 0
	buffer_load_dwordx4 v66, s[4:7], s77 offen lds
	s_nop 0
	s_mov_b32 m0, s49
	s_nop 0
	buffer_load_dwordx4 v66, s[4:7], s79 offen lds
	s_waitcnt vmcnt(10)
	s_barrier
	s_waitcnt lgkmcnt(0)
	s_setprio 1
	s_waitcnt lgkmcnt(1)
	v_mfma_scale_f32_16x16x128_f8f6f4 v[44:47], v[48:55], v[98:105], v[44:47], v165, v164 op_sel_hi:[0,0,0]
	s_waitcnt lgkmcnt(0)
	v_mfma_scale_f32_16x16x128_f8f6f4 v[36:39], v[74:81], v[98:105], v[36:39], v165, v164 op_sel_hi:[0,0,0]
	v_mfma_scale_f32_16x16x128_f8f6f4 v[28:31], v[48:55], v[106:113], v[28:31], v165, v164 op_sel_hi:[0,0,0]
	v_mfma_scale_f32_16x16x128_f8f6f4 v[20:23], v[74:81], v[106:113], v[20:23], v165, v164 op_sel_hi:[0,0,0]
	v_mfma_scale_f32_16x16x128_f8f6f4 v[12:15], v[48:55], v[114:121], v[12:15], v165, v164 op_sel_hi:[0,0,0]
	v_mfma_scale_f32_16x16x128_f8f6f4 v[134:137], v[48:55], v[90:97], v[60:63], v165, v164 op_sel_hi:[0,0,0]
	v_mfma_scale_f32_16x16x128_f8f6f4 v[138:141], v[74:81], v[90:97], v[56:59], v165, v164 op_sel_hi:[0,0,0]
	v_mfma_scale_f32_16x16x128_f8f6f4 v[142:145], v[74:81], v[114:121], v[4:7], v165, v164 op_sel_hi:[0,0,0]
	s_setprio 0
	s_barrier
	s_mov_b32 m0, s50
	s_nop 0
	buffer_load_dwordx4 v64, s[8:11], s77 offen lds
	s_nop 0
	s_mov_b32 m0, s51
	s_nop 0
	buffer_load_dwordx4 v67, s[8:11], s77 offen lds
	s_barrier
	s_waitcnt lgkmcnt(0)
	s_barrier
; #define G_WAIT_V(n) asm volatile("s_waitcnt vmcnt(" #n ")" ::: "memory")
; #define G_BAR() __builtin_amdgcn_s_barrier()
; #define G_SCHED() __builtin_amdgcn_sched_barrier(0)
; #define D_STAGE_A(slot, half, kt) D_STAGE(rsA, voffA, slot, half, kt)
; #define D_STAGE_B(slot, half, kt) D_STAGE(rsB, voffB, slot, half, kt)
; #define D_LDA(dst, slot) do { _Pragma("unroll") for (int m = 0; m < 4; ++m) _Pragma("unroll") for (int k = 0; k < 2; ++k) \
;     dst[m][k] = *(const LDS_AS bf16x8*)(lds + (slot) + aoff + m * 2048 + k * 1024); } while (0)
; #define D_LDB(dst, slot) do { _Pragma("unroll") for (int n = 0; n < 2; ++n) _Pragma("unroll") for (int k = 0; k < 2; ++k) \
;     dst[n][k] = *(const LDS_AS bf16x8*)(lds + (slot) + boff + n * 2048 + k * 1024); } while (0)
; #define D_MMA(ai, bj, At, Bf) do { __builtin_amdgcn_s_setprio(1); _Pragma("unroll") for (int m = 0; m < 4; ++m) _Pragma("unroll") for (int n = 0; n < 2; ++n) _Pragma("unroll") for (int k = 0; k < 2; ++k) \
;     acc[ai][bj][m][n] = __builtin_amdgcn_mfma_f32_16x16x32_bf16(Bf[n][k], At[m][k], acc[ai][bj][m][n], 0, 0, 0); __builtin_amdgcn_s_setprio(0); } while (0)
; #define D_WAIT_L(n) asm volatile("s_waitcnt lgkmcnt(" #n ")" ::: "memory")
; #define D_STAGE_A(slot, half, kt) D_STAGE(rsA, voffA, slot, half, kt)
; #define D_STAGE_B(slot, half, kt) do { _Pragma("unroll") for (int _i = 0; _i < 2; ++_i) { const unsigned _m0 = ldsw + (unsigned)((slot) + _i * 8192); const unsigned _so = (unsigned)(kt) * 128u + (half) * bt_half + _i * bt_piece; \
;     asm volatile("s_mov_b32 m0, %0\n\ts_nop 4\n\tbuffer_load_dwordx4 %1, %2, %3 offen lds" :: "s"(_m0), "v"(voffB0), "s"(rsB), "s"(_so) : "m0", "memory"); } } while (0)
;     ...
;     D_STAGE_B(G_SB(0, 1), 1, t2);
;     G_WAIT_V(6); G_BAR(); G_SCHED(); D_MMA(1, 1, At, B1); G_BAR(); G_SCHED();
;     D_LDB(B0, G_SB(1, 0)); G_SCHED(); D_LDA(At, G_SA(1, 0)); D_STAGE_A(G_SA(0, 1), 1, t2);
;     D_WAIT_L(8); G_BAR(); D_WAIT_L(0); G_SCHED(); D_MMA(0, 0, At, B0); G_BAR(); G_SCHED();
;     D_LDB(B1, G_SB(1, 1)); D_STAGE_B(G_SB(1, 0), 0, t3);
;     G_BAR(); D_WAIT_L(0); G_SCHED(); D_MMA(0, 1, At, B1); G_BAR(); G_SCHED();
;     D_LDA(At, G_SA(1, 1)); D_STAGE_A(G_SA(1, 0), 0, t3);
;     G_BAR(); D_WAIT_L(0); G_SCHED(); D_MMA(1, 0, At, B0); G_BAR(); G_SCHED();
;     D_STAGE_B(G_SB(1, 1), 1, t3);
;     G_WAIT_V(6); G_BAR(); G_SCHED(); D_MMA(1, 1, At, B1); G_BAR(); G_SCHED();
;   }
	s_mov_b32 m0, s54
	s_nop 0
	buffer_load_dwordx4 v66, s[4:7], s80 offen lds
	s_nop 0
	s_mov_b32 m0, s55
	s_nop 0
	buffer_load_dwordx4 v66, s[4:7], s81 offen lds
	s_waitcnt vmcnt(10)
	s_barrier
	s_barrier
	v_add_u32_e32 v4, s82, v69
	v_add_u32_e32 v48, s82, v70
	ds_read_b128 v[0:3], v4
	ds_read_b128 v[56:59], v4 offset:2048
	ds_read_b128 v[4:7], v48
	ds_read_b128 v[60:63], v48 offset:2048
	ds_read_b128 v[74:77], v71 offset:32784
	ds_read_b128 v[82:85], v71 offset:34832
	ds_read_b128 v[78:81], v72 offset:32784
	ds_read_b128 v[86:89], v72 offset:34832
	ds_read_b128 v[90:93], v71 offset:36880
	ds_read_b128 v[98:101], v71 offset:38928
	ds_read_b128 v[94:97], v72 offset:36880
	ds_read_b128 v[102:105], v72 offset:38928
	s_mov_b32 m0, s58
	s_nop 0
	buffer_load_dwordx4 v65, s[8:11], s77 offen lds
	s_nop 0
	s_mov_b32 m0, s59
	s_nop 0
	buffer_load_dwordx4 v68, s[8:11], s77 offen lds
	s_waitcnt lgkmcnt(8)
	s_waitcnt vmcnt(10)
	s_barrier
	s_waitcnt lgkmcnt(0)
	s_setprio 1
	s_waitcnt lgkmcnt(5)
	v_mfma_scale_f32_16x16x128_f8f6f4 v[48:51], v[0:7], v[74:81], v[122:125], v165, v164 op_sel_hi:[0,0,0]
	v_mfma_scale_f32_16x16x128_f8f6f4 v[52:55], v[56:63], v[74:81], v[126:129], v165, v164 op_sel_hi:[0,0,0]
	s_waitcnt lgkmcnt(4)
	v_mfma_scale_f32_16x16x128_f8f6f4 v[40:43], v[0:7], v[82:89], v[40:43], v165, v164 op_sel_hi:[0,0,0]
	v_mfma_scale_f32_16x16x128_f8f6f4 v[32:35], v[56:63], v[82:89], v[32:35], v165, v164 op_sel_hi:[0,0,0]
	s_waitcnt lgkmcnt(1)
	v_mfma_scale_f32_16x16x128_f8f6f4 v[24:27], v[0:7], v[90:97], v[24:27], v165, v164 op_sel_hi:[0,0,0]
	v_mfma_scale_f32_16x16x128_f8f6f4 v[16:19], v[56:63], v[90:97], v[16:19], v165, v164 op_sel_hi:[0,0,0]
	s_waitcnt lgkmcnt(0)
	v_mfma_scale_f32_16x16x128_f8f6f4 v[8:11], v[0:7], v[98:105], v[8:11], v165, v164 op_sel_hi:[0,0,0]
	v_mfma_scale_f32_16x16x128_f8f6f4 v[0:3], v[56:63], v[98:105], v[130:133], v165, v164 op_sel_hi:[0,0,0]
	s_setprio 0
	s_barrier
	v_add_u32_e32 v4, s76, v69
	v_add_u32_e32 v5, s76, v70
	ds_read_b128 v[106:109], v4
	ds_read_b128 v[114:117], v4 offset:2048
	ds_read_b128 v[110:113], v5
	ds_read_b128 v[118:121], v5 offset:2048
	s_mov_b32 m0, s60
	s_nop 0
	buffer_load_dwordx4 v66, s[4:7], s72 offen lds
	s_nop 0
	s_mov_b32 m0, s61
	s_nop 0
	buffer_load_dwordx4 v66, s[4:7], s75 offen lds
	s_waitcnt vmcnt(10)
	s_barrier
	s_waitcnt lgkmcnt(0)
	s_setprio 1
	s_waitcnt lgkmcnt(1)
	v_mfma_scale_f32_16x16x128_f8f6f4 v[60:63], v[106:113], v[74:81], v[134:137], v165, v164 op_sel_hi:[0,0,0]
	s_waitcnt lgkmcnt(0)
	v_mfma_scale_f32_16x16x128_f8f6f4 v[56:59], v[114:121], v[74:81], v[138:141], v165, v164 op_sel_hi:[0,0,0]
	v_mfma_scale_f32_16x16x128_f8f6f4 v[44:47], v[106:113], v[82:89], v[44:47], v165, v164 op_sel_hi:[0,0,0]
	v_mfma_scale_f32_16x16x128_f8f6f4 v[36:39], v[114:121], v[82:89], v[36:39], v165, v164 op_sel_hi:[0,0,0]
	v_mfma_scale_f32_16x16x128_f8f6f4 v[28:31], v[106:113], v[90:97], v[28:31], v165, v164 op_sel_hi:[0,0,0]
	v_mfma_scale_f32_16x16x128_f8f6f4 v[20:23], v[114:121], v[90:97], v[20:23], v165, v164 op_sel_hi:[0,0,0]
	v_mfma_scale_f32_16x16x128_f8f6f4 v[12:15], v[106:113], v[98:105], v[12:15], v165, v164 op_sel_hi:[0,0,0]
	v_mfma_scale_f32_16x16x128_f8f6f4 v[4:7], v[114:121], v[98:105], v[142:145], v165, v164 op_sel_hi:[0,0,0]
	s_setprio 0
	s_barrier
	s_mov_b32 m0, s62
	s_nop 0
	buffer_load_dwordx4 v64, s[8:11], s72 offen lds
	s_nop 0
	s_mov_b32 m0, s63
	s_nop 0
	buffer_load_dwordx4 v67, s[8:11], s72 offen lds
	s_barrier
	s_waitcnt lgkmcnt(0)
	s_barrier
	s_mov_b32 m0, s64
	s_nop 0
	buffer_load_dwordx4 v66, s[4:7], s74 offen lds
	s_nop 0
	s_mov_b32 m0, s65
	s_nop 0
	buffer_load_dwordx4 v66, s[4:7], s73 offen lds
	s_waitcnt vmcnt(10)
	s_barrier
	s_barrier
	s_mov_b32 s69, s70
	s_mov_b32 s71, s68
	s_cbranch_scc0 .LBB0_1634
	s_waitcnt vmcnt(0)
	s_cmpk_lt_u32 s13, 0x100
	s_cbranch_scc0 .LBB0_1637
	s_barrier

; #define G_WAIT_V(n) asm volatile("s_waitcnt vmcnt(" #n ")" ::: "memory")
; #define G_BAR() __builtin_amdgcn_s_barrier()
; #define G_SCHED() __builtin_amdgcn_sched_barrier(0)
; #define D_STAGE_A(slot, half, kt) D_STAGE(rsA, voffA, slot, half, kt)
; #define D_STAGE_B(slot, half, kt) D_STAGE(rsB, voffB, slot, half, kt)
; #define D_LDA(dst, slot) do { _Pragma("unroll") for (int m = 0; m < 4; ++m) _Pragma("unroll") for (int k = 0; k < 2; ++k) \
;     dst[m][k] = *(const LDS_AS bf16x8*)(lds + (slot) + aoff + m * 2048 + k * 1024); } while (0)
; #define D_LDB(dst, slot) do { _Pragma("unroll") for (int n = 0; n < 2; ++n) _Pragma("unroll") for (int k = 0; k < 2; ++k) \
;     dst[n][k] = *(const LDS_AS bf16x8*)(lds + (slot) + boff + n * 2048 + k * 1024); } while (0)
; #define D_MMA(ai, bj, At, Bf) do { __builtin_amdgcn_s_setprio(1); _Pragma("unroll") for (int m = 0; m < 4; ++m) _Pragma("unroll") for (int n = 0; n < 2; ++n) _Pragma("unroll") for (int k = 0; k < 2; ++k) \
;     acc[ai][bj][m][n] = __builtin_amdgcn_mfma_f32_16x16x32_bf16(Bf[n][k], At[m][k], acc[ai][bj][m][n], 0, 0, 0); __builtin_amdgcn_s_setprio(0); } while (0)
; #define D_WAIT_L(n) asm volatile("s_waitcnt lgkmcnt(" #n ")" ::: "memory")
; #define D_STAGE_A(slot, half, kt) D_STAGE(rsA, voffA, slot, half, kt)
; #define D_WAIT_L(n) asm volatile("s_waitcnt lgkmcnt(" #n ")" ::: "memory")
;     ...
;   for (int t = 0; t < (F8_PEEL ? nt - 2 : nt); t += 2) {
;     const int t1 = t + 1;
;     const int t2 = (F8_PEEL || t + 2 < nt) ? t + 2 : t;
;     const int t3 = (F8_PEEL || t + 2 < nt) ? t + 3 : t + 1;
;     D_LDB(B0, G_SB(0, 0)); G_SCHED(); D_LDA(At, G_SA(0, 0)); D_STAGE_A(G_SA(1, 1), 1, t1);
;     D_WAIT_L(8); G_BAR(); D_WAIT_L(0); G_SCHED(); D_MMA(0, 0, At, B0); G_BAR(); G_SCHED();
;     D_LDB(B1, G_SB(0, 1)); D_STAGE_B(G_SB(0, 0), 0, t2);
;     G_BAR(); D_WAIT_L(0); G_SCHED(); D_MMA(0, 1, At, B1); G_BAR(); G_SCHED();
;     D_LDA(At, G_SA(0, 1)); D_STAGE_A(G_SA(0, 0), 0, t2);
;     G_BAR(); D_WAIT_L(0); G_SCHED(); D_MMA(1, 0, At, B0); G_BAR(); G_SCHED();
;     D_STAGE_B(G_SB(0, 1), 1, t2);
;     G_WAIT_V(6); G_BAR(); G_SCHED(); D_MMA(1, 1, At, B1); G_BAR(); G_SCHED();
.LBB0_1674:
	s_add_i32 s68, 0, 0x10010
	s_nop 0
	v_add_u32_e32 v68, s68, v132
	v_add_u32_e32 v69, s68, v133
	ds_read_b128 v[146:149], v68
	ds_read_b128 v[154:157], v68 offset:2048
	ds_read_b128 v[150:153], v69
	ds_read_b128 v[158:161], v69 offset:2048
	s_add_i32 s38, s64, 1
	s_add_i32 s66, s64, 3
	s_add_i32 s65, s64, 2
	s_add_i32 s76, 0, 0x14010
	s_cmp_lt_u32 s64, 14
	s_cselect_b32 s67, s65, s64
	s_cselect_b32 s38, s66, s38
	s_lshl_b32 s72, s67, 7
	s_lshl_b32 s67, s38, 7
	s_add_i32 s77, s72, 0x20000
	s_add_i32 s74, s72, 0x40000
	s_add_i32 s75, s72, 0x60000
	s_add_i32 s73, 0, 0x18010
	s_add_i32 s71, 0, 0x1c010
	s_add_i32 s70, s67, 0x20000
	s_add_i32 s68, s67, 0x40000
	s_add_i32 s69, s67, 0x60000
	s_add_i32 s66, s63, 0x100
	s_cmp_gt_u32 s64, 13
	ds_read_b128 v[168:171], v135 offset:16
	ds_read_b128 v[176:179], v135 offset:2064
	ds_read_b128 v[172:175], v136 offset:16
	ds_read_b128 v[180:183], v136 offset:2064
	ds_read_b128 v[192:195], v135 offset:4112
	ds_read_b128 v[200:203], v135 offset:6160
	ds_read_b128 v[196:199], v136 offset:4112
	ds_read_b128 v[204:207], v136 offset:6160
	s_waitcnt lgkmcnt(12)
	s_mov_b32 m0, s24
	s_nop 0
	buffer_load_dwordx4 v166, s[8:11], s63 offen lds
	s_nop 0
	s_mov_b32 m0, s51
	s_nop 0
	buffer_load_dwordx4 v167, s[8:11], s63 offen lds
	s_waitcnt lgkmcnt(8)
	s_waitcnt vmcnt(10)
	s_barrier
	s_waitcnt lgkmcnt(0)
	s_setprio 1
	s_waitcnt lgkmcnt(0)
	v_mfma_scale_f32_16x16x128_f8f6f4 v[220:223], v[146:153], v[200:207], v[220:223], v165, v164 op_sel_hi:[0,0,0]
	v_mfma_scale_f32_16x16x128_f8f6f4 v[48:51], v[154:161], v[200:207], v[48:51], v165, v164 op_sel_hi:[0,0,0]
	v_mfma_scale_f32_16x16x128_f8f6f4 v[138:141], v[146:153], v[168:175], v[124:127], v165, v164 op_sel_hi:[0,0,0]
	v_mfma_scale_f32_16x16x128_f8f6f4 v[184:187], v[154:161], v[168:175], v[120:123], v165, v164 op_sel_hi:[0,0,0]
	v_mfma_scale_f32_16x16x128_f8f6f4 v[188:191], v[146:153], v[176:183], v[108:111], v165, v164 op_sel_hi:[0,0,0]
	v_mfma_scale_f32_16x16x128_f8f6f4 v[208:211], v[154:161], v[176:183], v[100:103], v165, v164 op_sel_hi:[0,0,0]
	v_mfma_scale_f32_16x16x128_f8f6f4 v[212:215], v[146:153], v[192:199], v[84:87], v165, v164 op_sel_hi:[0,0,0]
	v_mfma_scale_f32_16x16x128_f8f6f4 v[216:219], v[154:161], v[192:199], v[80:83], v165, v164 op_sel_hi:[0,0,0]
	s_setprio 0
	s_barrier
	v_add_u32_e32 v68, s76, v132
	v_add_u32_e32 v69, s76, v133
	s_nop 2
	ds_read_b128 v[80:83], v68
	ds_read_b128 v[120:123], v68 offset:2048
	ds_read_b128 v[84:87], v69
	ds_read_b128 v[124:127], v69 offset:2048
	s_mov_b32 m0, s25
	s_nop 0
	buffer_load_dwordx4 v134, s[4:7], s72 offen lds
	s_nop 0
	s_mov_b32 m0, s54
	s_nop 0
	buffer_load_dwordx4 v134, s[4:7], s77 offen lds
	s_waitcnt vmcnt(10)
	s_barrier
	s_waitcnt lgkmcnt(0)
	s_setprio 1
	s_waitcnt lgkmcnt(1)
	v_mfma_scale_f32_16x16x128_f8f6f4 v[116:119], v[80:87], v[168:175], v[116:119], v165, v164 op_sel_hi:[0,0,0]
	s_waitcnt lgkmcnt(0)
	v_mfma_scale_f32_16x16x128_f8f6f4 v[112:115], v[120:127], v[168:175], v[112:115], v165, v164 op_sel_hi:[0,0,0]
	v_mfma_scale_f32_16x16x128_f8f6f4 v[76:79], v[80:87], v[200:207], v[76:79], v165, v164 op_sel_hi:[0,0,0]
	v_mfma_scale_f32_16x16x128_f8f6f4 v[168:171], v[80:87], v[176:183], v[104:107], v165, v164 op_sel_hi:[0,0,0]
	v_mfma_scale_f32_16x16x128_f8f6f4 v[172:175], v[120:127], v[176:183], v[96:99], v165, v164 op_sel_hi:[0,0,0]
	v_mfma_scale_f32_16x16x128_f8f6f4 v[176:179], v[80:87], v[192:199], v[92:95], v165, v164 op_sel_hi:[0,0,0]
	v_mfma_scale_f32_16x16x128_f8f6f4 v[180:183], v[120:127], v[192:199], v[88:91], v165, v164 op_sel_hi:[0,0,0]
	v_mfma_scale_f32_16x16x128_f8f6f4 v[192:195], v[120:127], v[200:207], v[72:75], v165, v164 op_sel_hi:[0,0,0]
	s_setprio 0
	s_barrier
	ds_read_b128 v[68:71], v135 offset:16400
	s_nop 2
	ds_read_b128 v[88:91], v135 offset:18448
	ds_read_b128 v[72:75], v136 offset:16400
	ds_read_b128 v[92:95], v136 offset:18448
	ds_read_b128 v[96:99], v135 offset:20496
	ds_read_b128 v[104:107], v135 offset:22544
	ds_read_b128 v[100:103], v136 offset:20496
	ds_read_b128 v[108:111], v136 offset:22544
	s_mov_b32 m0, s15
	s_nop 0
	buffer_load_dwordx4 v162, s[8:11], s72 offen lds
	s_nop 0
	s_mov_b32 m0, s55
	s_nop 0
	buffer_load_dwordx4 v163, s[8:11], s72 offen lds
	s_barrier
	s_waitcnt lgkmcnt(0)
	s_setprio 1
	s_waitcnt lgkmcnt(5)
	v_mfma_scale_f32_16x16x128_f8f6f4 v[56:59], v[146:153], v[68:75], v[56:59], v165, v164 op_sel_hi:[0,0,0]
	v_mfma_scale_f32_16x16x128_f8f6f4 v[52:55], v[154:161], v[68:75], v[52:55], v165, v164 op_sel_hi:[0,0,0]
	s_waitcnt lgkmcnt(4)
	v_mfma_scale_f32_16x16x128_f8f6f4 v[200:203], v[146:153], v[88:95], v[36:39], v165, v164 op_sel_hi:[0,0,0]
	v_mfma_scale_f32_16x16x128_f8f6f4 v[204:207], v[154:161], v[88:95], v[32:35], v165, v164 op_sel_hi:[0,0,0]
	s_waitcnt lgkmcnt(1)
	v_mfma_scale_f32_16x16x128_f8f6f4 v[224:227], v[146:153], v[96:103], v[20:23], v165, v164 op_sel_hi:[0,0,0]
	v_mfma_scale_f32_16x16x128_f8f6f4 v[228:231], v[154:161], v[96:103], v[16:19], v165, v164 op_sel_hi:[0,0,0]
	s_waitcnt lgkmcnt(0)
	v_mfma_scale_f32_16x16x128_f8f6f4 v[232:235], v[146:153], v[104:111], v[4:7], v165, v164 op_sel_hi:[0,0,0]
	v_mfma_scale_f32_16x16x128_f8f6f4 v[236:239], v[154:161], v[104:111], v[0:3], v165, v164 op_sel_hi:[0,0,0]
	s_setprio 0
	s_barrier
	s_mov_b32 m0, s26
	s_nop 0
	buffer_load_dwordx4 v134, s[4:7], s74 offen lds
	s_nop 0
	s_mov_b32 m0, s58
	s_nop 0
	buffer_load_dwordx4 v134, s[4:7], s75 offen lds
	s_waitcnt vmcnt(10)
	s_barrier
; #define G_WAIT_V(n) asm volatile("s_waitcnt vmcnt(" #n ")" ::: "memory")
; #define G_BAR() __builtin_amdgcn_s_barrier()
; #define G_SCHED() __builtin_amdgcn_sched_barrier(0)
; #define D_STAGE_A(slot, half, kt) D_STAGE(rsA, voffA, slot, half, kt)
; #define D_STAGE_B(slot, half, kt) D_STAGE(rsB, voffB, slot, half, kt)
; #define D_LDA(dst, slot) do { _Pragma("unroll") for (int m = 0; m < 4; ++m) _Pragma("unroll") for (int k = 0; k < 2; ++k) \
;     dst[m][k] = *(const LDS_AS bf16x8*)(lds + (slot) + aoff + m * 2048 + k * 1024); } while (0)
; #define D_LDB(dst, slot) do { _Pragma("unroll") for (int n = 0; n < 2; ++n) _Pragma("unroll") for (int k = 0; k < 2; ++k) \
;     dst[n][k] = *(const LDS_AS bf16x8*)(lds + (slot) + boff + n * 2048 + k * 1024); } while (0)
; #define D_MMA(ai, bj, At, Bf) do { __builtin_amdgcn_s_setprio(1); _Pragma("unroll") for (int m = 0; m < 4; ++m) _Pragma("unroll") for (int n = 0; n < 2; ++n) _Pragma("unroll") for (int k = 0; k < 2; ++k) \
;     acc[ai][bj][m][n] = __builtin_amdgcn_mfma_f32_16x16x32_bf16(Bf[n][k], At[m][k], acc[ai][bj][m][n], 0, 0, 0); __builtin_amdgcn_s_setprio(0); } while (0)
; #define D_WAIT_L(n) asm volatile("s_waitcnt lgkmcnt(" #n ")" ::: "memory")
; #define D_STAGE_A(slot, half, kt) D_STAGE(rsA, voffA, slot, half, kt)
; #define D_STAGE_B(slot, half, kt) do { _Pragma("unroll") for (int _i = 0; _i < 2; ++_i) { const unsigned _m0 = ldsw + (unsigned)((slot) + _i * 8192); const unsigned _so = (unsigned)(kt) * 128u + (half) * bt_half + _i * bt_piece; \
;     asm volatile("s_mov_b32 m0, %0\n\ts_nop 4\n\tbuffer_load_dwordx4 %1, %2, %3 offen lds" :: "s"(_m0), "v"(voffB0), "s"(rsB), "s"(_so) : "m0", "memory"); } } while (0)
; #define D_WAIT_L(n) asm volatile("s_waitcnt lgkmcnt(" #n ")" ::: "memory")
;     ...
;     D_LDB(B0, G_SB(1, 0)); G_SCHED(); D_LDA(At, G_SA(1, 0)); D_STAGE_A(G_SA(0, 1), 1, t2);
;     D_WAIT_L(8); G_BAR(); D_WAIT_L(0); G_SCHED(); D_MMA(0, 0, At, B0); G_BAR(); G_SCHED();
;     D_LDB(B1, G_SB(1, 1)); D_STAGE_B(G_SB(1, 0), 0, t3);
;     G_BAR(); D_WAIT_L(0); G_SCHED(); D_MMA(0, 1, At, B1); G_BAR(); G_SCHED();
;     D_LDA(At, G_SA(1, 1)); D_STAGE_A(G_SA(1, 0), 0, t3);
;     G_BAR(); D_WAIT_L(0); G_SCHED(); D_MMA(1, 0, At, B0); G_BAR(); G_SCHED();
;     D_STAGE_B(G_SB(1, 1), 1, t3);
;     G_WAIT_V(6); G_BAR(); G_SCHED(); D_MMA(1, 1, At, B1); G_BAR(); G_SCHED();
;   }
	s_setprio 1
	v_mfma_scale_f32_16x16x128_f8f6f4 v[64:67], v[80:87], v[68:75], v[64:67], v165, v164 op_sel_hi:[0,0,0]
	v_mfma_scale_f32_16x16x128_f8f6f4 v[60:63], v[120:127], v[68:75], v[60:63], v165, v164 op_sel_hi:[0,0,0]
	v_mfma_scale_f32_16x16x128_f8f6f4 v[240:243], v[80:87], v[88:95], v[44:47], v165, v164 op_sel_hi:[0,0,0]
	v_mfma_scale_f32_16x16x128_f8f6f4 v[244:247], v[120:127], v[88:95], v[40:43], v165, v164 op_sel_hi:[0,0,0]
	v_mfma_scale_f32_16x16x128_f8f6f4 v[248:251], v[80:87], v[96:103], v[28:31], v165, v164 op_sel_hi:[0,0,0]
	v_mfma_scale_f32_16x16x128_f8f6f4 v[142:145], v[120:127], v[96:103], v[24:27], v165, v164 op_sel_hi:[0,0,0]
	v_mfma_scale_f32_16x16x128_f8f6f4 v[128:131], v[80:87], v[104:111], v[12:15], v165, v164 op_sel_hi:[0,0,0]
	v_mfma_scale_f32_16x16x128_f8f6f4 v[68:71], v[120:127], v[104:111], v[8:11], v165, v164 op_sel_hi:[0,0,0]
	s_setprio 0
	s_barrier
	v_add_u32_e32 v4, s73, v132
	s_nop 2
	v_add_u32_e32 v12, s73, v133
	ds_read_b128 v[0:3], v4
	ds_read_b128 v[8:11], v4 offset:2048
	ds_read_b128 v[4:7], v12
	ds_read_b128 v[12:15], v12 offset:2048
	ds_read_b128 v[16:19], v135 offset:32784
	ds_read_b128 v[24:27], v135 offset:34832
	ds_read_b128 v[20:23], v136 offset:32784
	ds_read_b128 v[28:31], v136 offset:34832
	ds_read_b128 v[32:35], v135 offset:36880
	ds_read_b128 v[40:43], v135 offset:38928
	ds_read_b128 v[36:39], v136 offset:36880
	ds_read_b128 v[44:47], v136 offset:38928
	s_mov_b32 m0, s27
	s_nop 0
	buffer_load_dwordx4 v166, s[8:11], s72 offen lds
	s_nop 0
	s_mov_b32 m0, s59
	s_nop 0
	buffer_load_dwordx4 v167, s[8:11], s72 offen lds
	s_waitcnt lgkmcnt(8)
	s_waitcnt vmcnt(10)
	s_barrier
	s_waitcnt lgkmcnt(0)
	s_setprio 1
	s_waitcnt lgkmcnt(5)
	v_mfma_scale_f32_16x16x128_f8f6f4 v[124:127], v[0:7], v[16:23], v[138:141], v165, v164 op_sel_hi:[0,0,0]
	v_mfma_scale_f32_16x16x128_f8f6f4 v[120:123], v[8:15], v[16:23], v[184:187], v165, v164 op_sel_hi:[0,0,0]
	s_waitcnt lgkmcnt(4)
	v_mfma_scale_f32_16x16x128_f8f6f4 v[108:111], v[0:7], v[24:31], v[188:191], v165, v164 op_sel_hi:[0,0,0]
	v_mfma_scale_f32_16x16x128_f8f6f4 v[100:103], v[8:15], v[24:31], v[208:211], v165, v164 op_sel_hi:[0,0,0]
	s_waitcnt lgkmcnt(1)
	v_mfma_scale_f32_16x16x128_f8f6f4 v[84:87], v[0:7], v[32:39], v[212:215], v165, v164 op_sel_hi:[0,0,0]
	v_mfma_scale_f32_16x16x128_f8f6f4 v[80:83], v[8:15], v[32:39], v[216:219], v165, v164 op_sel_hi:[0,0,0]
	s_waitcnt lgkmcnt(0)
	v_mfma_scale_f32_16x16x128_f8f6f4 v[220:223], v[0:7], v[40:47], v[220:223], v165, v164 op_sel_hi:[0,0,0]
	v_mfma_scale_f32_16x16x128_f8f6f4 v[48:51], v[8:15], v[40:47], v[48:51], v165, v164 op_sel_hi:[0,0,0]
	s_setprio 0
	s_barrier
	v_add_u32_e32 v72, s71, v132
	v_add_u32_e32 v73, s71, v133
	ds_read_b128 v[146:149], v72
	ds_read_b128 v[154:157], v72 offset:2048
	ds_read_b128 v[150:153], v73
	ds_read_b128 v[158:161], v73 offset:2048
	s_mov_b32 m0, s39
	s_nop 0
	buffer_load_dwordx4 v134, s[4:7], s67 offen lds
	s_nop 0
	s_mov_b32 m0, s60
	s_nop 0
	buffer_load_dwordx4 v134, s[4:7], s70 offen lds
	s_waitcnt vmcnt(10)
	s_barrier
	s_waitcnt lgkmcnt(0)
	s_setprio 1
	s_waitcnt lgkmcnt(1)
	v_mfma_scale_f32_16x16x128_f8f6f4 v[116:119], v[146:153], v[16:23], v[116:119], v165, v164 op_sel_hi:[0,0,0]
	s_waitcnt lgkmcnt(0)
	v_mfma_scale_f32_16x16x128_f8f6f4 v[112:115], v[154:161], v[16:23], v[112:115], v165, v164 op_sel_hi:[0,0,0]
	v_mfma_scale_f32_16x16x128_f8f6f4 v[104:107], v[146:153], v[24:31], v[168:171], v165, v164 op_sel_hi:[0,0,0]
	v_mfma_scale_f32_16x16x128_f8f6f4 v[96:99], v[154:161], v[24:31], v[172:175], v165, v164 op_sel_hi:[0,0,0]
	v_mfma_scale_f32_16x16x128_f8f6f4 v[92:95], v[146:153], v[32:39], v[176:179], v165, v164 op_sel_hi:[0,0,0]
	v_mfma_scale_f32_16x16x128_f8f6f4 v[88:91], v[154:161], v[32:39], v[180:183], v165, v164 op_sel_hi:[0,0,0]
	v_mfma_scale_f32_16x16x128_f8f6f4 v[76:79], v[146:153], v[40:47], v[76:79], v165, v164 op_sel_hi:[0,0,0]
	v_mfma_scale_f32_16x16x128_f8f6f4 v[72:75], v[154:161], v[40:47], v[192:195], v165, v164 op_sel_hi:[0,0,0]
	s_setprio 0
	s_barrier
	ds_read_b128 v[24:27], v135 offset:49168
	ds_read_b128 v[168:171], v135 offset:51216
	ds_read_b128 v[28:31], v136 offset:49168
	ds_read_b128 v[172:175], v136 offset:51216
	ds_read_b128 v[176:179], v135 offset:53264
	ds_read_b128 v[192:195], v135 offset:55312
	ds_read_b128 v[180:183], v136 offset:53264
	ds_read_b128 v[196:199], v136 offset:55312
	s_mov_b32 m0, s49
	s_nop 0
	buffer_load_dwordx4 v162, s[8:11], s67 offen lds
	s_nop 0
	s_mov_b32 m0, s61
	s_nop 0
	buffer_load_dwordx4 v163, s[8:11], s67 offen lds
	s_barrier
	s_waitcnt lgkmcnt(0)
	s_setprio 1
	s_waitcnt lgkmcnt(5)
	v_mfma_scale_f32_16x16x128_f8f6f4 v[56:59], v[0:7], v[24:31], v[56:59], v165, v164 op_sel_hi:[0,0,0]
	v_mfma_scale_f32_16x16x128_f8f6f4 v[52:55], v[8:15], v[24:31], v[52:55], v165, v164 op_sel_hi:[0,0,0]
	s_waitcnt lgkmcnt(4)
	v_mfma_scale_f32_16x16x128_f8f6f4 v[36:39], v[0:7], v[168:175], v[200:203], v165, v164 op_sel_hi:[0,0,0]
	v_mfma_scale_f32_16x16x128_f8f6f4 v[32:35], v[8:15], v[168:175], v[204:207], v165, v164 op_sel_hi:[0,0,0]
	s_waitcnt lgkmcnt(1)
	v_mfma_scale_f32_16x16x128_f8f6f4 v[20:23], v[0:7], v[176:183], v[224:227], v165, v164 op_sel_hi:[0,0,0]
	v_mfma_scale_f32_16x16x128_f8f6f4 v[16:19], v[8:15], v[176:183], v[228:231], v165, v164 op_sel_hi:[0,0,0]
	s_waitcnt lgkmcnt(0)
	v_mfma_scale_f32_16x16x128_f8f6f4 v[4:7], v[0:7], v[192:199], v[232:235], v165, v164 op_sel_hi:[0,0,0]
	v_mfma_scale_f32_16x16x128_f8f6f4 v[0:3], v[8:15], v[192:199], v[236:239], v165, v164 op_sel_hi:[0,0,0]
	s_setprio 0
	s_barrier
	s_mov_b32 m0, s50
	s_nop 0
	buffer_load_dwordx4 v134, s[4:7], s68 offen lds
	s_nop 0
	s_mov_b32 m0, s62
	s_nop 0
	buffer_load_dwordx4 v134, s[4:7], s69 offen lds
	s_waitcnt vmcnt(10)
	s_barrier
	s_setprio 1
	v_mfma_scale_f32_16x16x128_f8f6f4 v[64:67], v[146:153], v[24:31], v[64:67], v165, v164 op_sel_hi:[0,0,0]
	v_mfma_scale_f32_16x16x128_f8f6f4 v[60:63], v[154:161], v[24:31], v[60:63], v165, v164 op_sel_hi:[0,0,0]
	v_mfma_scale_f32_16x16x128_f8f6f4 v[44:47], v[146:153], v[168:175], v[240:243], v165, v164 op_sel_hi:[0,0,0]
	v_mfma_scale_f32_16x16x128_f8f6f4 v[40:43], v[154:161], v[168:175], v[244:247], v165, v164 op_sel_hi:[0,0,0]
	v_mfma_scale_f32_16x16x128_f8f6f4 v[28:31], v[146:153], v[176:183], v[248:251], v165, v164 op_sel_hi:[0,0,0]
	v_mfma_scale_f32_16x16x128_f8f6f4 v[24:27], v[154:161], v[176:183], v[142:145], v165, v164 op_sel_hi:[0,0,0]
	v_mfma_scale_f32_16x16x128_f8f6f4 v[12:15], v[146:153], v[192:199], v[128:131], v165, v164 op_sel_hi:[0,0,0]
	v_mfma_scale_f32_16x16x128_f8f6f4 v[8:11], v[154:161], v[192:199], v[68:71], v165, v164 op_sel_hi:[0,0,0]
	s_setprio 0
	s_barrier
	s_mov_b32 s63, s66
	s_mov_b32 s64, s65
	s_cbranch_scc0 .LBB0_1674
	s_waitcnt vmcnt(0)
	s_cmpk_lt_u32 s13, 0x100
	s_cbranch_scc0 .LBB0_1677
	s_barrier

; #define G_WAIT_V(n) asm volatile("s_waitcnt vmcnt(" #n ")" ::: "memory")
; #define G_BAR() __builtin_amdgcn_s_barrier()
; #define G_SCHED() __builtin_amdgcn_sched_barrier(0)
; #define D_STAGE_A(slot, half, kt) D_STAGE(rsA, voffA, slot, half, kt)
; #define D_STAGE_B(slot, half, kt) D_STAGE(rsB, voffB, slot, half, kt)
; #define D_LDA(dst, slot) do { _Pragma("unroll") for (int m = 0; m < 4; ++m) _Pragma("unroll") for (int k = 0; k < 2; ++k) \
;     dst[m][k] = *(const LDS_AS bf16x8*)(lds + (slot) + aoff + m * 2048 + k * 1024); } while (0)
; #define D_LDB(dst, slot) do { _Pragma("unroll") for (int n = 0; n < 2; ++n) _Pragma("unroll") for (int k = 0; k < 2; ++k) \
;     dst[n][k] = *(const LDS_AS bf16x8*)(lds + (slot) + boff + n * 2048 + k * 1024); } while (0)
; #define D_MMA(ai, bj, At, Bf) do { __builtin_amdgcn_s_setprio(1); _Pragma("unroll") for (int m = 0; m < 4; ++m) _Pragma("unroll") for (int n = 0; n < 2; ++n) _Pragma("unroll") for (int k = 0; k < 2; ++k) \
;     acc[ai][bj][m][n] = __builtin_amdgcn_mfma_f32_16x16x32_bf16(Bf[n][k], At[m][k], acc[ai][bj][m][n], 0, 0, 0); __builtin_amdgcn_s_setprio(0); } while (0)
; #define D_WAIT_L(n) asm volatile("s_waitcnt lgkmcnt(" #n ")" ::: "memory")
; #define D_STAGE_A(slot, half, kt) D_STAGE(rsA, voffA, slot, half, kt)
; #define D_WAIT_L(n) asm volatile("s_waitcnt lgkmcnt(" #n ")" ::: "memory")
;     ...
;   for (int t = 0; t < (F8_PEEL ? nt - 2 : nt); t += 2) {
;     const int t1 = t + 1;
;     const int t2 = (F8_PEEL || t + 2 < nt) ? t + 2 : t;
;     const int t3 = (F8_PEEL || t + 2 < nt) ? t + 3 : t + 1;
;     D_LDB(B0, G_SB(0, 0)); G_SCHED(); D_LDA(At, G_SA(0, 0)); D_STAGE_A(G_SA(1, 1), 1, t1);
;     D_WAIT_L(8); G_BAR(); D_WAIT_L(0); G_SCHED(); D_MMA(0, 0, At, B0); G_BAR(); G_SCHED();
;     D_LDB(B1, G_SB(0, 1)); D_STAGE_B(G_SB(0, 0), 0, t2);
;     G_BAR(); D_WAIT_L(0); G_SCHED(); D_MMA(0, 1, At, B1); G_BAR(); G_SCHED();
;     D_LDA(At, G_SA(0, 1)); D_STAGE_A(G_SA(0, 0), 0, t2);
;     G_BAR(); D_WAIT_L(0); G_SCHED(); D_MMA(1, 0, At, B0); G_BAR(); G_SCHED();
;     D_STAGE_B(G_SB(0, 1), 1, t2);
;     G_WAIT_V(6); G_BAR(); G_SCHED(); D_MMA(1, 1, At, B1); G_BAR(); G_SCHED();
.LBB0_1701:
	s_add_i32 s68, 0, 0x10010
	s_waitcnt vmcnt(62)
	v_add_u32_e32 v73, s68, v68
	s_waitcnt vmcnt(49)
	v_add_u32_e32 v86, s68, v69
	ds_read_b128 v[74:77], v73
	ds_read_b128 v[82:85], v73 offset:2048
	ds_read_b128 v[78:81], v86
	s_waitcnt vmcnt(46)
	ds_read_b128 v[86:89], v86 offset:2048
	s_add_i32 s38, s66, 1
	s_add_i32 s65, s66, 3
	s_add_i32 s64, s66, 2
	s_add_i32 s73, 0, 0x14010
	s_cmp_lt_u32 s66, 14
	s_cselect_b32 s67, s64, s66
	s_cselect_b32 s38, s65, s38
	s_lshl_b32 s72, s67, 7
	s_lshl_b32 s67, s38, 7
	s_add_i32 s74, s72, 0x20000
	s_add_i32 s75, s72, 0x40000
	s_add_i32 s76, s72, 0x60000
	s_add_i32 s77, 0, 0x18010
	s_add_i32 s71, 0, 0x1c010
	s_add_i32 s70, s67, 0x20000
	s_add_i32 s68, s67, 0x40000
	s_add_i32 s69, s67, 0x60000
	s_add_i32 s65, s63, 0x100
	s_cmp_gt_u32 s66, 13
	s_waitcnt vmcnt(42)
	ds_read_b128 v[90:93], v71 offset:16
	s_waitcnt vmcnt(34)
	ds_read_b128 v[98:101], v71 offset:2064
	ds_read_b128 v[94:97], v72 offset:16
	s_waitcnt vmcnt(30)
	ds_read_b128 v[102:105], v72 offset:2064
	s_waitcnt vmcnt(26)
	ds_read_b128 v[106:109], v71 offset:4112
	s_waitcnt vmcnt(18)
	ds_read_b128 v[114:117], v71 offset:6160
	ds_read_b128 v[110:113], v72 offset:4112
	s_waitcnt vmcnt(2)
	ds_read_b128 v[118:121], v72 offset:6160
	s_waitcnt lgkmcnt(12)
	s_mov_b32 m0, s24
	s_nop 0
	buffer_load_dwordx4 v66, s[8:11], s63 offen lds
	s_nop 0
	s_mov_b32 m0, s51
	s_nop 0
	buffer_load_dwordx4 v67, s[8:11], s63 offen lds
	s_waitcnt lgkmcnt(8)
	s_waitcnt vmcnt(10)
	s_barrier
	s_waitcnt lgkmcnt(0)
	s_setprio 1
	s_waitcnt lgkmcnt(4)
	v_mfma_scale_f32_16x16x128_f8f6f4 v[40:43], v[74:81], v[98:105], v[40:43], v165, v164 op_sel_hi:[0,0,0]
	v_mfma_scale_f32_16x16x128_f8f6f4 v[32:35], v[82:89], v[98:105], v[32:35], v165, v164 op_sel_hi:[0,0,0]
	s_waitcnt lgkmcnt(1)
	v_mfma_scale_f32_16x16x128_f8f6f4 v[24:27], v[74:81], v[106:113], v[24:27], v165, v164 op_sel_hi:[0,0,0]
	v_mfma_scale_f32_16x16x128_f8f6f4 v[16:19], v[82:89], v[106:113], v[16:19], v165, v164 op_sel_hi:[0,0,0]
	s_waitcnt lgkmcnt(0)
	v_mfma_scale_f32_16x16x128_f8f6f4 v[8:11], v[74:81], v[114:121], v[8:11], v165, v164 op_sel_hi:[0,0,0]
	s_waitcnt vmcnt(0)
	v_mfma_scale_f32_16x16x128_f8f6f4 v[122:125], v[74:81], v[90:97], v[48:51], v165, v164 op_sel_hi:[0,0,0]
	v_mfma_scale_f32_16x16x128_f8f6f4 v[126:129], v[82:89], v[90:97], v[52:55], v165, v164 op_sel_hi:[0,0,0]
	v_mfma_scale_f32_16x16x128_f8f6f4 v[130:133], v[82:89], v[114:121], v[0:3], v165, v164 op_sel_hi:[0,0,0]
	s_setprio 0
	s_barrier
	s_nop 4
	v_add_u32_e32 v0, s73, v68
	v_add_u32_e32 v1, s73, v69
	ds_read_b128 v[48:51], v0
	ds_read_b128 v[74:77], v0 offset:2048
	ds_read_b128 v[52:55], v1
	ds_read_b128 v[78:81], v1 offset:2048
	s_mov_b32 m0, s25
	s_nop 0
	buffer_load_dwordx4 v70, s[4:7], s72 offen lds
	s_nop 0
	s_mov_b32 m0, s54
	s_nop 0
	buffer_load_dwordx4 v70, s[4:7], s74 offen lds
	s_waitcnt vmcnt(10)
	s_barrier
	s_waitcnt lgkmcnt(0)
	s_setprio 1
	s_waitcnt lgkmcnt(1)
	v_mfma_scale_f32_16x16x128_f8f6f4 v[44:47], v[48:55], v[98:105], v[44:47], v165, v164 op_sel_hi:[0,0,0]
	s_waitcnt lgkmcnt(0)
	v_mfma_scale_f32_16x16x128_f8f6f4 v[36:39], v[74:81], v[98:105], v[36:39], v165, v164 op_sel_hi:[0,0,0]
	v_mfma_scale_f32_16x16x128_f8f6f4 v[28:31], v[48:55], v[106:113], v[28:31], v165, v164 op_sel_hi:[0,0,0]
	v_mfma_scale_f32_16x16x128_f8f6f4 v[20:23], v[74:81], v[106:113], v[20:23], v165, v164 op_sel_hi:[0,0,0]
	v_mfma_scale_f32_16x16x128_f8f6f4 v[12:15], v[48:55], v[114:121], v[12:15], v165, v164 op_sel_hi:[0,0,0]
	v_mfma_scale_f32_16x16x128_f8f6f4 v[134:137], v[48:55], v[90:97], v[60:63], v165, v164 op_sel_hi:[0,0,0]
	v_mfma_scale_f32_16x16x128_f8f6f4 v[138:141], v[74:81], v[90:97], v[56:59], v165, v164 op_sel_hi:[0,0,0]
	v_mfma_scale_f32_16x16x128_f8f6f4 v[146:149], v[74:81], v[114:121], v[4:7], v165, v164 op_sel_hi:[0,0,0]
	s_setprio 0
	s_barrier
	s_mov_b32 m0, s15
	s_nop 0
	buffer_load_dwordx4 v64, s[8:11], s72 offen lds
	s_nop 0
	s_mov_b32 m0, s55
	s_nop 0
	buffer_load_dwordx4 v65, s[8:11], s72 offen lds
	s_barrier
; #define G_WAIT_V(n) asm volatile("s_waitcnt vmcnt(" #n ")" ::: "memory")
; #define G_BAR() __builtin_amdgcn_s_barrier()
; #define G_SCHED() __builtin_amdgcn_sched_barrier(0)
; #define D_STAGE_A(slot, half, kt) D_STAGE(rsA, voffA, slot, half, kt)
; #define D_STAGE_B(slot, half, kt) D_STAGE(rsB, voffB, slot, half, kt)
; #define D_LDA(dst, slot) do { _Pragma("unroll") for (int m = 0; m < 4; ++m) _Pragma("unroll") for (int k = 0; k < 2; ++k) \
;     dst[m][k] = *(const LDS_AS bf16x8*)(lds + (slot) + aoff + m * 2048 + k * 1024); } while (0)
; #define D_LDB(dst, slot) do { _Pragma("unroll") for (int n = 0; n < 2; ++n) _Pragma("unroll") for (int k = 0; k < 2; ++k) \
;     dst[n][k] = *(const LDS_AS bf16x8*)(lds + (slot) + boff + n * 2048 + k * 1024); } while (0)
; #define D_MMA(ai, bj, At, Bf) do { __builtin_amdgcn_s_setprio(1); _Pragma("unroll") for (int m = 0; m < 4; ++m) _Pragma("unroll") for (int n = 0; n < 2; ++n) _Pragma("unroll") for (int k = 0; k < 2; ++k) \
;     acc[ai][bj][m][n] = __builtin_amdgcn_mfma_f32_16x16x32_bf16(Bf[n][k], At[m][k], acc[ai][bj][m][n], 0, 0, 0); __builtin_amdgcn_s_setprio(0); } while (0)
; #define D_WAIT_L(n) asm volatile("s_waitcnt lgkmcnt(" #n ")" ::: "memory")
; #define D_STAGE_A(slot, half, kt) D_STAGE(rsA, voffA, slot, half, kt)
; #define D_STAGE_B(slot, half, kt) do { _Pragma("unroll") for (int _i = 0; _i < 2; ++_i) { const unsigned _m0 = ldsw + (unsigned)((slot) + _i * 8192); const unsigned _so = (unsigned)(kt) * 128u + (half) * bt_half + _i * bt_piece; \
;     asm volatile("s_mov_b32 m0, %0\n\ts_nop 4\n\tbuffer_load_dwordx4 %1, %2, %3 offen lds" :: "s"(_m0), "v"(voffB0), "s"(rsB), "s"(_so) : "m0", "memory"); } } while (0)
; #define D_WAIT_L(n) asm volatile("s_waitcnt lgkmcnt(" #n ")" ::: "memory")
;     ...
;     D_LDB(B0, G_SB(1, 0)); G_SCHED(); D_LDA(At, G_SA(1, 0)); D_STAGE_A(G_SA(0, 1), 1, t2);
;     D_WAIT_L(8); G_BAR(); D_WAIT_L(0); G_SCHED(); D_MMA(0, 0, At, B0); G_BAR(); G_SCHED();
;     D_LDB(B1, G_SB(1, 1)); D_STAGE_B(G_SB(1, 0), 0, t3);
;     G_BAR(); D_WAIT_L(0); G_SCHED(); D_MMA(0, 1, At, B1); G_BAR(); G_SCHED();
;     D_LDA(At, G_SA(1, 1)); D_STAGE_A(G_SA(1, 0), 0, t3);
;     G_BAR(); D_WAIT_L(0); G_SCHED(); D_MMA(1, 0, At, B0); G_BAR(); G_SCHED();
;     D_STAGE_B(G_SB(1, 1), 1, t3);
;     G_WAIT_V(6); G_BAR(); G_SCHED(); D_MMA(1, 1, At, B1); G_BAR(); G_SCHED();
;   }
	s_waitcnt lgkmcnt(0)
	s_barrier
	s_mov_b32 m0, s26
	s_nop 0
	buffer_load_dwordx4 v70, s[4:7], s75 offen lds
	s_nop 0
	s_mov_b32 m0, s58
	s_nop 0
	buffer_load_dwordx4 v70, s[4:7], s76 offen lds
	s_waitcnt vmcnt(10)
	s_barrier
	s_barrier
	v_add_u32_e32 v4, s77, v68
	v_add_u32_e32 v48, s77, v69
	ds_read_b128 v[0:3], v4
	ds_read_b128 v[56:59], v4 offset:2048
	ds_read_b128 v[4:7], v48
	ds_read_b128 v[60:63], v48 offset:2048
	ds_read_b128 v[74:77], v71 offset:32784
	ds_read_b128 v[82:85], v71 offset:34832
	ds_read_b128 v[78:81], v72 offset:32784
	ds_read_b128 v[86:89], v72 offset:34832
	ds_read_b128 v[90:93], v71 offset:36880
	ds_read_b128 v[98:101], v71 offset:38928
	ds_read_b128 v[94:97], v72 offset:36880
	ds_read_b128 v[102:105], v72 offset:38928
	s_mov_b32 m0, s27
	s_nop 0
	buffer_load_dwordx4 v66, s[8:11], s72 offen lds
	s_nop 0
	s_mov_b32 m0, s59
	s_nop 0
	buffer_load_dwordx4 v67, s[8:11], s72 offen lds
	s_waitcnt lgkmcnt(8)
	s_waitcnt vmcnt(10)
	s_barrier
	s_waitcnt lgkmcnt(0)
	s_setprio 1
	s_waitcnt lgkmcnt(5)
	v_mfma_scale_f32_16x16x128_f8f6f4 v[48:51], v[0:7], v[74:81], v[122:125], v165, v164 op_sel_hi:[0,0,0]
	v_mfma_scale_f32_16x16x128_f8f6f4 v[52:55], v[56:63], v[74:81], v[126:129], v165, v164 op_sel_hi:[0,0,0]
	s_waitcnt lgkmcnt(4)
	v_mfma_scale_f32_16x16x128_f8f6f4 v[40:43], v[0:7], v[82:89], v[40:43], v165, v164 op_sel_hi:[0,0,0]
	v_mfma_scale_f32_16x16x128_f8f6f4 v[32:35], v[56:63], v[82:89], v[32:35], v165, v164 op_sel_hi:[0,0,0]
	s_waitcnt lgkmcnt(1)
	v_mfma_scale_f32_16x16x128_f8f6f4 v[24:27], v[0:7], v[90:97], v[24:27], v165, v164 op_sel_hi:[0,0,0]
	v_mfma_scale_f32_16x16x128_f8f6f4 v[16:19], v[56:63], v[90:97], v[16:19], v165, v164 op_sel_hi:[0,0,0]
	s_waitcnt lgkmcnt(0)
	v_mfma_scale_f32_16x16x128_f8f6f4 v[8:11], v[0:7], v[98:105], v[8:11], v165, v164 op_sel_hi:[0,0,0]
	v_mfma_scale_f32_16x16x128_f8f6f4 v[0:3], v[56:63], v[98:105], v[130:133], v165, v164 op_sel_hi:[0,0,0]
	s_setprio 0
	s_barrier
	v_add_u32_e32 v4, s71, v68
	v_add_u32_e32 v5, s71, v69
	ds_read_b128 v[106:109], v4
	ds_read_b128 v[114:117], v4 offset:2048
	ds_read_b128 v[110:113], v5
	ds_read_b128 v[118:121], v5 offset:2048
	s_mov_b32 m0, s39
	s_nop 0
	buffer_load_dwordx4 v70, s[4:7], s67 offen lds
	s_nop 0
	s_mov_b32 m0, s60
	s_nop 0
	buffer_load_dwordx4 v70, s[4:7], s70 offen lds
	s_waitcnt vmcnt(10)
	s_barrier
	s_waitcnt lgkmcnt(0)
	s_setprio 1
	s_waitcnt lgkmcnt(1)
	v_mfma_scale_f32_16x16x128_f8f6f4 v[60:63], v[106:113], v[74:81], v[134:137], v165, v164 op_sel_hi:[0,0,0]
	s_waitcnt lgkmcnt(0)
	v_mfma_scale_f32_16x16x128_f8f6f4 v[56:59], v[114:121], v[74:81], v[138:141], v165, v164 op_sel_hi:[0,0,0]
	v_mfma_scale_f32_16x16x128_f8f6f4 v[44:47], v[106:113], v[82:89], v[44:47], v165, v164 op_sel_hi:[0,0,0]
	v_mfma_scale_f32_16x16x128_f8f6f4 v[36:39], v[114:121], v[82:89], v[36:39], v165, v164 op_sel_hi:[0,0,0]
	v_mfma_scale_f32_16x16x128_f8f6f4 v[28:31], v[106:113], v[90:97], v[28:31], v165, v164 op_sel_hi:[0,0,0]
	v_mfma_scale_f32_16x16x128_f8f6f4 v[20:23], v[114:121], v[90:97], v[20:23], v165, v164 op_sel_hi:[0,0,0]
	v_mfma_scale_f32_16x16x128_f8f6f4 v[12:15], v[106:113], v[98:105], v[12:15], v165, v164 op_sel_hi:[0,0,0]
	v_mfma_scale_f32_16x16x128_f8f6f4 v[4:7], v[114:121], v[98:105], v[146:149], v165, v164 op_sel_hi:[0,0,0]
	s_setprio 0
	s_barrier
	s_mov_b32 m0, s49
	s_nop 0
	buffer_load_dwordx4 v64, s[8:11], s67 offen lds
	s_nop 0
	s_mov_b32 m0, s61
	s_nop 0
	buffer_load_dwordx4 v65, s[8:11], s67 offen lds
	s_barrier
	s_waitcnt lgkmcnt(0)
	s_barrier
	s_mov_b32 m0, s50
	s_nop 0
	buffer_load_dwordx4 v70, s[4:7], s68 offen lds
	s_nop 0
	s_mov_b32 m0, s62
	s_nop 0
	buffer_load_dwordx4 v70, s[4:7], s69 offen lds
	s_waitcnt vmcnt(10)
	s_barrier
	s_barrier
	s_mov_b32 s63, s65
	s_mov_b32 s66, s64
	s_cbranch_scc0 .LBB0_1701
	s_waitcnt vmcnt(0)
	s_cmpk_lt_u32 s13, 0x100
	s_cbranch_scc0 .LBB0_1704
	s_barrier
